# GEMM last stage: dropped conversion and LDS writes of the never-read dummy row piece
# baseline (speedup 1.0000x reference)
.Ltailv_skip:
	s_or_b64 exec, exec, s[4:5]
	s_waitcnt lgkmcnt(0)
	s_barrier
	v_sub_u32_e32 v245, v234, v243
	v_add_u32_e32 v246, 0xfffffdc0, v245
	v_min_u32_e32 v245, v245, v246
	v_add_u32_e32 v234, v242, v245
	v_sub_u32_e32 v245, v235, v243
	v_add_u32_e32 v246, 0xfffffdc0, v245
	v_min_u32_e32 v245, v245, v246
	v_add_u32_e32 v235, v242, v245
	v_sub_u32_e32 v245, v236, v243
	v_add_u32_e32 v246, 0xfffffdc0, v245
	v_min_u32_e32 v245, v245, v246
	v_add_u32_e32 v236, v242, v245
	v_sub_u32_e32 v245, v237, v243
	v_add_u32_e32 v246, 0xfffffdc0, v245
	v_min_u32_e32 v245, v245, v246
	v_add_u32_e32 v237, v242, v245
	v_sub_u32_e32 v245, v238, v243
	v_add_u32_e32 v246, 0xfffffdc0, v245
	v_min_u32_e32 v245, v245, v246
	v_add_u32_e32 v238, v242, v245
	v_sub_u32_e32 v245, v239, v243
	v_add_u32_e32 v246, 0xfffffdc0, v245
	v_min_u32_e32 v245, v245, v246
	v_add_u32_e32 v239, v242, v245
	v_sub_u32_e32 v245, v240, v243
	v_add_u32_e32 v246, 0xfffffdc0, v245
	v_min_u32_e32 v245, v245, v246
	v_add_u32_e32 v240, v242, v245
	v_sub_u32_e32 v245, v241, v243
	v_add_u32_e32 v246, 0xfffffdc0, v245
	v_min_u32_e32 v245, v245, v246
	v_add_u32_e32 v241, v242, v245
	s_mov_b32 s3, 0x10000
	v_add_co_u32_e32 v10, vcc, s3, v152
	s_mov_b32 s3, 0x14000
	s_nop 0
	v_addc_co_u32_e32 v11, vcc, 0, v153, vcc
	v_add_co_u32_e32 v58, vcc, s3, v152
	global_load_dwordx4 v[34:37], v[10:11], off sc1
	global_load_dwordx4 v[38:41], v[10:11], off offset:256 sc1
	v_addc_co_u32_e32 v59, vcc, 0, v153, vcc
	global_load_dwordx4 v[14:17], v[58:59], off sc1
	global_load_dwordx4 v[10:13], v[58:59], off offset:256 sc1
	v_lshlrev_b32_e32 v58, 4, v87
	v_add_u32_e32 v224, 0x111518dc, v154
	v_mad_u32_u24 v151, v86, s17, v58
	ds_read_b128 v[58:61], v151 offset:0
	v_add_u32_e32 v62, 0x400, v150
	s_waitcnt vmcnt(24) lgkmcnt(0)
	v_mfma_f32_16x16x32_f16 v[86:89], v[26:29], v[58:61], 0
	s_waitcnt vmcnt(23)
	v_mfma_f32_16x16x32_f16 v[122:125], v[50:53], v[58:61], 0
	v_min_u32_e32 v58, v62, v224
	global_load_dwordx4 v[58:61], v58, s[8:9] nt
	s_waitcnt vmcnt(17)
	v_cvt_pk_f16_f32 v63, v112, v113
	v_cvt_pk_f16_f32 v62, v110, v111
	v_add_u32_e32 v155, 0xea00, v1
	ds_write_b16 v234, v62 offset:0
	ds_write_b16_d16_hi v235, v62 offset:0
	ds_write_b16 v236, v63 offset:0
	ds_write_b16_d16_hi v237, v63 offset:0
	ds_read_b128 v[62:65], v151 offset:608
	ds_read_b128 v[66:69], v151 offset:1216
	s_waitcnt lgkmcnt(1)
	v_mfma_f32_16x16x32_f16 v[110:113], v[26:29], v[62:65], 0
	v_mfma_f32_16x16x32_f16 v[126:129], v[50:53], v[62:65], 0
	s_waitcnt lgkmcnt(0)
	v_mfma_f32_16x16x32_f16 v[130:133], v[26:29], v[66:69], 0
	v_mfma_f32_16x16x32_f16 v[134:137], v[50:53], v[66:69], 0
	ds_read_b128 v[62:65], v151 offset:1824
	ds_read_b128 v[66:69], v151 offset:2432
	s_waitcnt lgkmcnt(1)
	v_mfma_f32_16x16x32_f16 v[138:141], v[26:29], v[62:65], 0
	v_mfma_f32_16x16x32_f16 v[142:145], v[50:53], v[62:65], 0
	s_waitcnt lgkmcnt(0)
	v_mfma_f32_16x16x32_f16 v[146:149], v[26:29], v[66:69], 0
	v_mfma_f32_16x16x32_f16 v[156:159], v[50:53], v[66:69], 0
	v_add_u32_e32 v62, 0x16a40, v244
	v_min_u32_e32 v62, v62, v224
	global_load_dwordx4 v[62:65], v62, s[8:9] nt
	s_waitcnt vmcnt(17)
	v_cvt_pk_f16_f32 v67, v116, v117
	v_cvt_pk_f16_f32 v66, v114, v115
	ds_write_b16 v238, v66 offset:608
	ds_write_b16_d16_hi v239, v66 offset:608
	ds_write_b16 v240, v67 offset:608
	ds_write_b16_d16_hi v241, v67 offset:608
	ds_read_b128 v[66:69], v151 offset:3040
	ds_read_b128 v[70:73], v151 offset:4864
	s_waitcnt lgkmcnt(1)
	v_mfma_f32_16x16x32_f16 v[114:117], v[26:29], v[66:69], 0
	v_mfma_f32_16x16x32_f16 v[160:163], v[50:53], v[66:69], 0
	ds_read_b128 v[66:69], v151 offset:3648
	ds_read_b128 v[164:167], v151 offset:4256
	s_waitcnt lgkmcnt(1)
	v_mfma_f32_16x16x32_f16 v[168:171], v[26:29], v[66:69], 0
	v_mfma_f32_16x16x32_f16 v[172:175], v[50:53], v[66:69], 0
	s_waitcnt lgkmcnt(0)
	v_mfma_f32_16x16x32_f16 v[176:179], v[26:29], v[164:167], 0
	v_mfma_f32_16x16x32_f16 v[164:167], v[50:53], v[164:167], 0
	v_mfma_f32_16x16x32_f16 v[180:183], v[26:29], v[70:73], 0
	v_mfma_f32_16x16x32_f16 v[184:187], v[50:53], v[70:73], 0
	v_add_u32_e32 v66, 0x2d080, v150
	v_min_u32_e32 v66, v66, v224
	global_load_dwordx4 v[66:69], v66, s[8:9] nt
	s_waitcnt vmcnt(17)
	v_cvt_pk_f16_f32 v71, v120, v121
	v_cvt_pk_f16_f32 v70, v118, v119
	ds_write_b16 v234, v70 offset:1216
	ds_write_b16_d16_hi v235, v70 offset:1216
	ds_write_b16 v236, v71 offset:1216
	ds_write_b16_d16_hi v237, v71 offset:1216
	ds_read_b128 v[70:73], v151 offset:5472
	ds_read_b128 v[118:121], v151 offset:6080
	s_waitcnt lgkmcnt(1)
	v_mfma_f32_16x16x32_f16 v[188:191], v[26:29], v[70:73], 0
	v_mfma_f32_16x16x32_f16 v[192:195], v[50:53], v[70:73], 0
	ds_read_b128 v[70:73], v151 offset:6688
	ds_read_b128 v[200:203], v151 offset:7296
	s_waitcnt lgkmcnt(2)
	v_mfma_f32_16x16x32_f16 v[196:199], v[26:29], v[118:121], 0
	v_mfma_f32_16x16x32_f16 v[118:121], v[50:53], v[118:121], 0
	s_waitcnt lgkmcnt(1)
	v_mfma_f32_16x16x32_f16 v[204:207], v[26:29], v[70:73], 0
	v_mfma_f32_16x16x32_f16 v[208:211], v[50:53], v[70:73], 0
	s_waitcnt lgkmcnt(0)
	v_mfma_f32_16x16x32_f16 v[26:29], v[26:29], v[200:203], 0
	v_mfma_f32_16x16x32_f16 v[200:203], v[50:53], v[200:203], 0
	v_add_u32_e32 v50, 0x436c0, v244
	v_min_u32_e32 v50, v50, v224
	global_load_dwordx4 v[70:73], v50, s[8:9] nt
	s_waitcnt vmcnt(17)
	v_cvt_pk_f16_f32 v51, v76, v77
	v_cvt_pk_f16_f32 v50, v74, v75
	ds_write_b16 v238, v50 offset:1824
	ds_write_b16_d16_hi v239, v50 offset:1824
	ds_write_b16 v240, v51 offset:1824
	ds_write_b16_d16_hi v241, v51 offset:1824
	ds_read_b128 v[50:53], v151 offset:64
	ds_read_b128 v[74:77], v151 offset:672
	s_waitcnt lgkmcnt(1)
	v_mfma_f32_16x16x32_f16 v[86:89], v[18:21], v[50:53], v[86:89]
	v_mfma_f32_16x16x32_f16 v[122:125], v[42:45], v[50:53], v[122:125]
	s_waitcnt lgkmcnt(0)
	v_mfma_f32_16x16x32_f16 v[110:113], v[18:21], v[74:77], v[110:113]
	v_mfma_f32_16x16x32_f16 v[126:129], v[42:45], v[74:77], v[126:129]
	ds_read_b128 v[50:53], v151 offset:1280
	ds_read_b128 v[74:77], v151 offset:1888
	s_waitcnt lgkmcnt(1)
	v_mfma_f32_16x16x32_f16 v[130:133], v[18:21], v[50:53], v[130:133]
	v_mfma_f32_16x16x32_f16 v[134:137], v[42:45], v[50:53], v[134:137]
	s_waitcnt lgkmcnt(0)
	v_mfma_f32_16x16x32_f16 v[138:141], v[18:21], v[74:77], v[138:141]
	v_mfma_f32_16x16x32_f16 v[142:145], v[42:45], v[74:77], v[142:145]
	v_add_u32_e32 v50, 0x59d00, v150
	v_min_u32_e32 v50, v50, v224
	global_load_dwordx4 v[74:77], v50, s[8:9] nt
	s_waitcnt vmcnt(17)
	v_cvt_pk_f16_f32 v51, v80, v81
	v_cvt_pk_f16_f32 v50, v78, v79
	ds_write_b16 v234, v50 offset:2432
	ds_write_b16_d16_hi v235, v50 offset:2432
	ds_write_b16 v236, v51 offset:2432
	ds_write_b16_d16_hi v237, v51 offset:2432
	ds_read_b128 v[50:53], v151 offset:2496
	ds_read_b128 v[78:81], v151 offset:3104
	s_waitcnt lgkmcnt(1)
	v_mfma_f32_16x16x32_f16 v[146:149], v[18:21], v[50:53], v[146:149]
	v_mfma_f32_16x16x32_f16 v[156:159], v[42:45], v[50:53], v[156:159]
	s_waitcnt lgkmcnt(0)
	v_mfma_f32_16x16x32_f16 v[114:117], v[18:21], v[78:81], v[114:117]
	v_mfma_f32_16x16x32_f16 v[160:163], v[42:45], v[78:81], v[160:163]
	ds_read_b128 v[50:53], v151 offset:3712
	ds_read_b128 v[78:81], v151 offset:4320
	s_waitcnt lgkmcnt(1)
	v_mfma_f32_16x16x32_f16 v[168:171], v[18:21], v[50:53], v[168:171]
	v_mfma_f32_16x16x32_f16 v[172:175], v[42:45], v[50:53], v[172:175]
	s_waitcnt lgkmcnt(0)
	v_mfma_f32_16x16x32_f16 v[176:179], v[18:21], v[78:81], v[176:179]
	v_mfma_f32_16x16x32_f16 v[164:167], v[42:45], v[78:81], v[164:167]
	v_add_u32_e32 v50, 0x70340, v244
	v_min_u32_e32 v50, v50, v224
	global_load_dwordx4 v[78:81], v50, s[8:9] nt
	s_waitcnt vmcnt(17)
	v_cvt_pk_f16_f32 v51, v84, v85
	v_cvt_pk_f16_f32 v50, v82, v83
	ds_write_b16 v238, v50 offset:3040
	ds_write_b16_d16_hi v239, v50 offset:3040
	ds_write_b16 v240, v51 offset:3040
	ds_write_b16_d16_hi v241, v51 offset:3040
	ds_read_b128 v[50:53], v151 offset:4928
	ds_read_b128 v[82:85], v151 offset:5536
	s_waitcnt lgkmcnt(1)
	v_mfma_f32_16x16x32_f16 v[180:183], v[18:21], v[50:53], v[180:183]
	v_mfma_f32_16x16x32_f16 v[184:187], v[42:45], v[50:53], v[184:187]
	s_waitcnt lgkmcnt(0)
	v_mfma_f32_16x16x32_f16 v[188:191], v[18:21], v[82:85], v[188:191]
	v_mfma_f32_16x16x32_f16 v[192:195], v[42:45], v[82:85], v[192:195]
	ds_read_b128 v[50:53], v151 offset:6144
	ds_read_b128 v[82:85], v151 offset:6752
	s_waitcnt lgkmcnt(1)
	v_mfma_f32_16x16x32_f16 v[196:199], v[18:21], v[50:53], v[196:199]
	v_mfma_f32_16x16x32_f16 v[118:121], v[42:45], v[50:53], v[118:121]
	s_waitcnt lgkmcnt(0)
	v_mfma_f32_16x16x32_f16 v[204:207], v[18:21], v[82:85], v[204:207]
	v_mfma_f32_16x16x32_f16 v[208:211], v[42:45], v[82:85], v[208:211]
	v_add_u32_e32 v50, 0x86980, v150
	v_min_u32_e32 v50, v50, v224
	global_load_dwordx4 v[82:85], v50, s[8:9] nt
	s_waitcnt vmcnt(17)
	v_cvt_pk_f16_f32 v51, v56, v57
	v_cvt_pk_f16_f32 v50, v54, v55
	ds_write_b16 v234, v50 offset:3648
	ds_write_b16_d16_hi v235, v50 offset:3648
	ds_write_b16 v236, v51 offset:3648
	ds_write_b16_d16_hi v237, v51 offset:3648
	ds_read_b128 v[212:215], v151 offset:7360
	s_mov_b32 s2, 0x18000
	s_waitcnt lgkmcnt(0)
	v_mfma_f32_16x16x32_f16 v[216:219], v[18:21], v[212:215], v[26:29]
	v_add_co_u32_e32 v18, vcc, s2, v152
	s_mov_b32 s2, 0x1c000
	s_nop 0
	v_addc_co_u32_e32 v19, vcc, 0, v153, vcc
	global_load_dwordx4 v[50:53], v[18:19], off sc1
	global_load_dwordx4 v[54:57], v[18:19], off offset:256 sc1
	v_add_co_u32_e32 v18, vcc, s2, v152
	v_mfma_f32_16x16x32_f16 v[42:45], v[42:45], v[212:215], v[200:203]
	s_nop 0
	v_addc_co_u32_e32 v19, vcc, 0, v153, vcc
	global_load_dwordx4 v[26:29], v[18:19], off sc1
	s_nop 0
	global_load_dwordx4 v[18:21], v[18:19], off offset:256 sc1
	ds_read_b128 v[200:203], v151 offset:128
	ds_read_b128 v[212:215], v151 offset:736
	s_waitcnt lgkmcnt(1)
	v_mfma_f32_16x16x32_f16 v[220:223], v[22:25], v[200:203], v[86:89]
	s_nop 2
	ds_read_b128 v[86:89], v151 offset:1344
	v_mfma_f32_16x16x32_f16 v[122:125], v[30:33], v[200:203], v[122:125]
	s_waitcnt lgkmcnt(1)
	v_mfma_f32_16x16x32_f16 v[110:113], v[22:25], v[212:215], v[110:113]
	v_mfma_f32_16x16x32_f16 v[126:129], v[30:33], v[212:215], v[126:129]
	s_waitcnt lgkmcnt(0)
	v_mfma_f32_16x16x32_f16 v[130:133], v[22:25], v[86:89], v[130:133]
	v_mfma_f32_16x16x32_f16 v[134:137], v[30:33], v[86:89], v[134:137]
	v_add_u32_e32 v86, 0x9cfc0, v244
	v_min_u32_e32 v86, v86, v224
	global_load_dwordx4 v[86:89], v86, s[8:9] nt
	s_waitcnt vmcnt(21)
	v_cvt_pk_f16_f32 v93, v92, v93
	v_cvt_pk_f16_f32 v92, v90, v91
	ds_write_b16 v238, v92 offset:4256
	ds_write_b16_d16_hi v239, v92 offset:4256
	ds_write_b16 v240, v93 offset:4256
	ds_write_b16_d16_hi v241, v93 offset:4256
	ds_read_b128 v[90:93], v151 offset:1952
	ds_read_b128 v[200:203], v151 offset:2560
	s_waitcnt lgkmcnt(1)
	v_mfma_f32_16x16x32_f16 v[138:141], v[22:25], v[90:93], v[138:141]
	v_mfma_f32_16x16x32_f16 v[142:145], v[30:33], v[90:93], v[142:145]
	s_waitcnt lgkmcnt(0)
	v_mfma_f32_16x16x32_f16 v[146:149], v[22:25], v[200:203], v[146:149]
	v_mfma_f32_16x16x32_f16 v[156:159], v[30:33], v[200:203], v[156:159]
	ds_read_b128 v[90:93], v151 offset:3168
	ds_read_b128 v[200:203], v151 offset:3776
	s_waitcnt lgkmcnt(1)
	v_mfma_f32_16x16x32_f16 v[114:117], v[22:25], v[90:93], v[114:117]
	v_mfma_f32_16x16x32_f16 v[160:163], v[30:33], v[90:93], v[160:163]
	s_waitcnt lgkmcnt(0)
	v_mfma_f32_16x16x32_f16 v[168:171], v[22:25], v[200:203], v[168:171]
	v_mfma_f32_16x16x32_f16 v[172:175], v[30:33], v[200:203], v[172:175]
	v_add_u32_e32 v90, 0xb3600, v150
	v_min_u32_e32 v90, v90, v224
	global_load_dwordx4 v[90:93], v90, s[8:9] nt
	s_waitcnt vmcnt(21)
	v_cvt_pk_f16_f32 v97, v96, v97
	v_cvt_pk_f16_f32 v96, v94, v95
	ds_write_b16 v234, v96 offset:4864
	ds_write_b16_d16_hi v235, v96 offset:4864
	ds_write_b16 v236, v97 offset:4864
	ds_write_b16_d16_hi v237, v97 offset:4864
	ds_read_b128 v[94:97], v151 offset:4384
	ds_read_b128 v[200:203], v151 offset:6208
	s_waitcnt lgkmcnt(1)
	v_mfma_f32_16x16x32_f16 v[176:179], v[22:25], v[94:97], v[176:179]
	v_mfma_f32_16x16x32_f16 v[164:167], v[30:33], v[94:97], v[164:167]
	ds_read_b128 v[94:97], v151 offset:4992
	ds_read_b128 v[212:215], v151 offset:5600
	s_waitcnt lgkmcnt(1)
	v_mfma_f32_16x16x32_f16 v[180:183], v[22:25], v[94:97], v[180:183]
	v_mfma_f32_16x16x32_f16 v[184:187], v[30:33], v[94:97], v[184:187]
	s_waitcnt lgkmcnt(0)
	v_mfma_f32_16x16x32_f16 v[188:191], v[22:25], v[212:215], v[188:191]
	v_mfma_f32_16x16x32_f16 v[192:195], v[30:33], v[212:215], v[192:195]
	v_mfma_f32_16x16x32_f16 v[196:199], v[22:25], v[200:203], v[196:199]
	v_mfma_f32_16x16x32_f16 v[118:121], v[30:33], v[200:203], v[118:121]
	v_add_u32_e32 v94, 0xc9c40, v244
	v_min_u32_e32 v94, v94, v224
	global_load_dwordx4 v[94:97], v94, s[8:9] nt
	s_waitcnt vmcnt(21)
	v_cvt_pk_f16_f32 v101, v100, v101
	v_cvt_pk_f16_f32 v100, v98, v99
	ds_write_b16 v238, v100 offset:5472
	ds_write_b16_d16_hi v239, v100 offset:5472
	ds_write_b16 v240, v101 offset:5472
	ds_write_b16_d16_hi v241, v101 offset:5472
	ds_read_b128 v[98:101], v151 offset:6816
	ds_read_b128 v[200:203], v151 offset:7424
	s_waitcnt lgkmcnt(1)
	v_mfma_f32_16x16x32_f16 v[204:207], v[22:25], v[98:101], v[204:207]
	v_mfma_f32_16x16x32_f16 v[208:211], v[30:33], v[98:101], v[208:211]
	s_waitcnt lgkmcnt(0)
	v_mfma_f32_16x16x32_f16 v[30:33], v[30:33], v[200:203], v[42:45]
	s_nop 2
	ds_read_b128 v[42:45], v151 offset:192
	ds_read_b128 v[98:101], v151 offset:800
	v_mfma_f32_16x16x32_f16 v[22:25], v[22:25], v[200:203], v[216:219]
	s_waitcnt lgkmcnt(1)
	v_mfma_f32_16x16x32_f16 v[200:203], v[6:9], v[42:45], v[220:223]
	v_mfma_f32_16x16x32_f16 v[122:125], v[2:5], v[42:45], v[122:125]
	s_waitcnt lgkmcnt(0)
	v_mfma_f32_16x16x32_f16 v[212:215], v[6:9], v[98:101], v[110:113]
	v_mfma_f32_16x16x32_f16 v[126:129], v[2:5], v[98:101], v[126:129]
	v_add_u32_e32 v42, 0xe0280, v150
	v_min_u32_e32 v42, v42, v224
	global_load_dwordx4 v[98:101], v42, s[8:9] nt
	s_waitcnt vmcnt(21)
	v_cvt_pk_f16_f32 v43, v104, v105
	v_cvt_pk_f16_f32 v42, v102, v103
	ds_write_b16 v234, v42 offset:6080
	ds_write_b16_d16_hi v235, v42 offset:6080
	ds_write_b16 v236, v43 offset:6080
	ds_write_b16_d16_hi v237, v43 offset:6080
	ds_read_b128 v[42:45], v151 offset:1408
	ds_read_b128 v[102:105], v151 offset:2016
	s_waitcnt lgkmcnt(1)
	v_mfma_f32_16x16x32_f16 v[130:133], v[6:9], v[42:45], v[130:133]
	v_mfma_f32_16x16x32_f16 v[134:137], v[2:5], v[42:45], v[134:137]
	s_waitcnt lgkmcnt(0)
	v_mfma_f32_16x16x32_f16 v[138:141], v[6:9], v[102:105], v[138:141]
	v_mfma_f32_16x16x32_f16 v[142:145], v[2:5], v[102:105], v[142:145]
	ds_read_b128 v[42:45], v151 offset:2624
	ds_read_b128 v[102:105], v151 offset:3232
	s_waitcnt lgkmcnt(1)
	v_mfma_f32_16x16x32_f16 v[146:149], v[6:9], v[42:45], v[146:149]
	v_mfma_f32_16x16x32_f16 v[216:219], v[2:5], v[42:45], v[156:159]
	s_waitcnt lgkmcnt(0)
	v_mfma_f32_16x16x32_f16 v[220:223], v[6:9], v[102:105], v[114:117]
	v_mfma_f32_16x16x32_f16 v[158:161], v[2:5], v[102:105], v[160:163]
	v_add_u32_e32 v42, 0xf68c0, v244
	v_min_u32_e32 v42, v42, v224
	global_load_dwordx4 v[102:105], v42, s[8:9] nt
	s_waitcnt vmcnt(21)
	v_cvt_pk_f16_f32 v43, v108, v109
	v_cvt_pk_f16_f32 v42, v106, v107
	ds_write_b16 v238, v42 offset:6688
	ds_write_b16_d16_hi v239, v42 offset:6688
	ds_write_b16 v240, v43 offset:6688
	ds_write_b16_d16_hi v241, v43 offset:6688
	ds_read_b128 v[42:45], v151 offset:3840
	ds_read_b128 v[106:109], v151 offset:4448
	s_waitcnt lgkmcnt(1)
	v_mfma_f32_16x16x32_f16 v[168:171], v[6:9], v[42:45], v[168:171]
	v_mfma_f32_16x16x32_f16 v[172:175], v[2:5], v[42:45], v[172:175]
	s_waitcnt lgkmcnt(0)
	v_mfma_f32_16x16x32_f16 v[176:179], v[6:9], v[106:109], v[176:179]
	v_mfma_f32_16x16x32_f16 v[162:165], v[2:5], v[106:109], v[164:167]
	ds_read_b128 v[42:45], v151 offset:5056
	ds_read_b128 v[106:109], v151 offset:5664
	s_waitcnt lgkmcnt(1)
	v_mfma_f32_16x16x32_f16 v[180:183], v[6:9], v[42:45], v[180:183]
	v_mfma_f32_16x16x32_f16 v[184:187], v[2:5], v[42:45], v[184:187]
	s_waitcnt lgkmcnt(0)
	v_mfma_f32_16x16x32_f16 v[188:191], v[6:9], v[106:109], v[188:191]
	v_mfma_f32_16x16x32_f16 v[192:195], v[2:5], v[106:109], v[192:195]
	v_add_u32_e32 v42, 0x10cf00, v150
	v_min_u32_e32 v42, v42, v224
	v_cndmask_b32_e64 v42, 0, v42, s[0:1]
	global_load_dwordx4 v[106:109], v42, s[8:9] nt
	s_waitcnt vmcnt(21)
	v_cvt_pk_f16_f32 v43, v48, v49
	v_cvt_pk_f16_f32 v42, v46, v47
	ds_write_b16 v234, v42 offset:7296
	ds_write_b16_d16_hi v235, v42 offset:7296
	ds_write_b16 v236, v43 offset:7296
	ds_write_b16_d16_hi v237, v43 offset:7296
	ds_read_b128 v[42:45], v151 offset:6272
	ds_read_b128 v[46:49], v151 offset:6880
	ds_read_b128 v[110:113], v151 offset:7488
	s_mov_b32 s2, 0x20000
	v_add_co_u32_e32 v114, vcc, s2, v152
	s_mov_b32 s2, 0x24000
	s_nop 0
	v_addc_co_u32_e32 v115, vcc, 0, v153, vcc
	s_waitcnt lgkmcnt(2)
	v_mfma_f32_16x16x32_f16 v[196:199], v[6:9], v[42:45], v[196:199]
	s_waitcnt lgkmcnt(0)
	s_barrier
	v_sub_u32_e32 v245, v234, v243
	v_add_u32_e32 v246, 0xfffffdc0, v245
	v_min_u32_e32 v245, v245, v246
	v_add_u32_e32 v234, v242, v245
	v_sub_u32_e32 v245, v235, v243
	v_add_u32_e32 v246, 0xfffffdc0, v245
	v_min_u32_e32 v245, v245, v246
	v_add_u32_e32 v235, v242, v245
	v_sub_u32_e32 v245, v236, v243
	v_add_u32_e32 v246, 0xfffffdc0, v245
	v_min_u32_e32 v245, v245, v246
	v_add_u32_e32 v236, v242, v245
	v_sub_u32_e32 v245, v237, v243
	v_add_u32_e32 v246, 0xfffffdc0, v245
	v_min_u32_e32 v245, v245, v246
	v_add_u32_e32 v237, v242, v245
	v_sub_u32_e32 v245, v238, v243
	v_add_u32_e32 v246, 0xfffffdc0, v245
	v_min_u32_e32 v245, v245, v246
	v_add_u32_e32 v238, v242, v245
	v_sub_u32_e32 v245, v239, v243
	v_add_u32_e32 v246, 0xfffffdc0, v245
	v_min_u32_e32 v245, v245, v246
	v_add_u32_e32 v239, v242, v245
	v_sub_u32_e32 v245, v240, v243
	v_add_u32_e32 v246, 0xfffffdc0, v245
	v_min_u32_e32 v245, v245, v246
	v_add_u32_e32 v240, v242, v245
	v_sub_u32_e32 v245, v241, v243
	v_add_u32_e32 v246, 0xfffffdc0, v245
	v_min_u32_e32 v245, v245, v246
	v_add_u32_e32 v241, v242, v245
	v_mfma_f32_16x16x32_f16 v[204:207], v[6:9], v[46:49], v[204:207]
	v_mfma_f32_16x16x32_f16 v[228:231], v[6:9], v[110:113], v[22:25]
	v_add_co_u32_e32 v6, vcc, s2, v152
	s_nop 1
	v_addc_co_u32_e32 v7, vcc, 0, v153, vcc
	v_mfma_f32_16x16x32_f16 v[224:227], v[2:5], v[42:45], v[118:121]
	v_mfma_f32_16x16x32_f16 v[208:211], v[2:5], v[46:49], v[208:211]
	global_load_dwordx4 v[42:45], v[114:115], off sc1
	global_load_dwordx4 v[46:49], v[114:115], off offset:256 sc1
	global_load_dwordx4 v[22:25], v[6:7], off sc1
	s_nop 0
	global_load_dwordx4 v[6:9], v[6:7], off offset:256 sc1
	v_mfma_f32_16x16x32_f16 v[2:5], v[2:5], v[110:113], v[30:33]
	v_add_u32_e32 v157, 0x11151adc, v154
	s_nop 1
	ds_read_b128 v[30:33], v151 offset:256
	v_add_u32_e32 v156, 0xea00, v151
	v_add_u32_e32 v110, 0x600, v150
	s_waitcnt vmcnt(24) lgkmcnt(0)
	v_mfma_f32_16x16x32_f16 v[200:203], v[34:37], v[30:33], v[200:203]
	s_waitcnt vmcnt(23)
	v_mfma_f32_16x16x32_f16 v[30:33], v[38:41], v[30:33], v[122:125]
	v_min_u32_e32 v110, v110, v157
	global_load_dwordx4 v[110:113], v110, s[8:9] nt
	s_waitcnt vmcnt(21)
	v_cvt_pk_f16_f32 v61, v60, v61
	v_cvt_pk_f16_f32 v60, v58, v59
	ds_write_b16 v234, v60 offset:0
	ds_write_b16_d16_hi v235, v60 offset:0
	ds_write_b16 v236, v61 offset:0
	ds_write_b16_d16_hi v237, v61 offset:0
	ds_read_b128 v[58:61], v151 offset:864
	ds_read_b128 v[114:117], v151 offset:1472
	s_waitcnt lgkmcnt(1)
	v_mfma_f32_16x16x32_f16 v[122:125], v[34:37], v[58:61], v[212:215]
	v_mfma_f32_16x16x32_f16 v[58:61], v[38:41], v[58:61], v[126:129]
	s_waitcnt lgkmcnt(0)
	v_mfma_f32_16x16x32_f16 v[126:129], v[34:37], v[114:117], v[130:133]
	v_mfma_f32_16x16x32_f16 v[130:133], v[38:41], v[114:117], v[134:137]
	ds_read_b128 v[114:117], v151 offset:2080
	ds_read_b128 v[118:121], v151 offset:2688
	s_waitcnt lgkmcnt(1)
	v_mfma_f32_16x16x32_f16 v[134:137], v[34:37], v[114:117], v[138:141]
	v_mfma_f32_16x16x32_f16 v[138:141], v[38:41], v[114:117], v[142:145]
	s_waitcnt lgkmcnt(0)
	v_mfma_f32_16x16x32_f16 v[142:145], v[34:37], v[118:121], v[146:149]
	v_mfma_f32_16x16x32_f16 v[146:149], v[38:41], v[118:121], v[216:219]
	v_add_u32_e32 v114, 0x16c40, v244
	v_min_u32_e32 v114, v114, v157
	global_load_dwordx4 v[114:117], v114, s[8:9] nt
	s_waitcnt vmcnt(21)
	v_cvt_pk_f16_f32 v65, v64, v65
	v_cvt_pk_f16_f32 v64, v62, v63
	ds_write_b16 v238, v64 offset:608
	ds_write_b16_d16_hi v239, v64 offset:608
	ds_write_b16 v240, v65 offset:608
	ds_write_b16_d16_hi v241, v65 offset:608
	ds_read_b128 v[62:65], v151 offset:3296
	ds_read_b128 v[118:121], v151 offset:5120
	s_waitcnt lgkmcnt(1)
	v_mfma_f32_16x16x32_f16 v[212:215], v[34:37], v[62:65], v[220:223]
	v_mfma_f32_16x16x32_f16 v[62:65], v[38:41], v[62:65], v[158:161]
	s_nop 2
	ds_read_b128 v[158:161], v151 offset:3904
	ds_read_b128 v[216:219], v151 offset:4512
	s_waitcnt lgkmcnt(1)
	v_mfma_f32_16x16x32_f16 v[166:169], v[34:37], v[158:161], v[168:171]
	v_mfma_f32_16x16x32_f16 v[158:161], v[38:41], v[158:161], v[172:175]
	s_waitcnt lgkmcnt(0)
	v_mfma_f32_16x16x32_f16 v[170:173], v[34:37], v[216:219], v[176:179]
	v_mfma_f32_16x16x32_f16 v[162:165], v[38:41], v[216:219], v[162:165]
	v_mfma_f32_16x16x32_f16 v[174:177], v[34:37], v[118:121], v[180:183]
	v_mfma_f32_16x16x32_f16 v[178:181], v[38:41], v[118:121], v[184:187]
	v_add_u32_e32 v118, 0x2d280, v150
	v_min_u32_e32 v118, v118, v157
	global_load_dwordx4 v[118:121], v118, s[8:9] nt
	s_waitcnt vmcnt(21)
	v_cvt_pk_f16_f32 v69, v68, v69
	v_cvt_pk_f16_f32 v68, v66, v67
	ds_write_b16 v234, v68 offset:1216
	ds_write_b16_d16_hi v235, v68 offset:1216
	ds_write_b16 v236, v69 offset:1216
	ds_write_b16_d16_hi v237, v69 offset:1216
	ds_read_b128 v[66:69], v151 offset:5728
	ds_read_b128 v[182:185], v151 offset:6336
	s_waitcnt lgkmcnt(1)
	v_mfma_f32_16x16x32_f16 v[186:189], v[34:37], v[66:69], v[188:191]
	v_mfma_f32_16x16x32_f16 v[190:193], v[38:41], v[66:69], v[192:195]
	ds_read_b128 v[66:69], v151 offset:6944
	ds_read_b128 v[216:219], v151 offset:7552
	s_waitcnt lgkmcnt(2)
	v_mfma_f32_16x16x32_f16 v[194:197], v[34:37], v[182:185], v[196:199]
	v_mfma_f32_16x16x32_f16 v[182:185], v[38:41], v[182:185], v[224:227]
	s_waitcnt lgkmcnt(1)
	v_mfma_f32_16x16x32_f16 v[204:207], v[34:37], v[66:69], v[204:207]
	v_mfma_f32_16x16x32_f16 v[208:211], v[38:41], v[66:69], v[208:211]
	s_waitcnt lgkmcnt(0)
	v_mfma_f32_16x16x32_f16 v[220:223], v[34:37], v[216:219], v[228:231]
	v_mfma_f32_16x16x32_f16 v[2:5], v[38:41], v[216:219], v[2:5]
	v_add_u32_e32 v34, 0x438c0, v244
	v_min_u32_e32 v34, v34, v157
	global_load_dwordx4 v[34:37], v34, s[8:9] nt
	s_waitcnt vmcnt(21)
	v_cvt_pk_f16_f32 v39, v72, v73
	v_cvt_pk_f16_f32 v38, v70, v71
	ds_write_b16 v238, v38 offset:1824
	ds_write_b16_d16_hi v239, v38 offset:1824
	ds_write_b16 v240, v39 offset:1824
	ds_write_b16_d16_hi v241, v39 offset:1824
	ds_read_b128 v[38:41], v151 offset:320
	ds_read_b128 v[66:69], v151 offset:928
	s_waitcnt lgkmcnt(1)
	v_mfma_f32_16x16x32_f16 v[198:201], v[14:17], v[38:41], v[200:203]
	v_mfma_f32_16x16x32_f16 v[38:41], v[10:13], v[38:41], v[30:33]
	s_waitcnt lgkmcnt(0)
	v_mfma_f32_16x16x32_f16 v[216:219], v[10:13], v[66:69], v[58:61]
	s_nop 0
	ds_read_b128 v[30:33], v151 offset:1536
	s_nop 0
	ds_read_b128 v[58:61], v151 offset:2144
	v_mfma_f32_16x16x32_f16 v[122:125], v[14:17], v[66:69], v[122:125]
	s_waitcnt lgkmcnt(1)
	v_mfma_f32_16x16x32_f16 v[126:129], v[14:17], v[30:33], v[126:129]
	v_mfma_f32_16x16x32_f16 v[130:133], v[10:13], v[30:33], v[130:133]
	s_waitcnt lgkmcnt(0)
	v_mfma_f32_16x16x32_f16 v[134:137], v[14:17], v[58:61], v[134:137]
	v_mfma_f32_16x16x32_f16 v[138:141], v[10:13], v[58:61], v[138:141]
	v_add_u32_e32 v30, 0x59f00, v150
	v_min_u32_e32 v30, v30, v157
	global_load_dwordx4 v[66:69], v30, s[8:9] nt
	s_waitcnt vmcnt(21)
	v_cvt_pk_f16_f32 v31, v76, v77
	v_cvt_pk_f16_f32 v30, v74, v75
	ds_write_b16 v234, v30 offset:2432
	ds_write_b16_d16_hi v235, v30 offset:2432
	ds_write_b16 v236, v31 offset:2432
	ds_write_b16_d16_hi v237, v31 offset:2432
	ds_read_b128 v[30:33], v151 offset:2752
	ds_read_b128 v[58:61], v151 offset:3360
	s_waitcnt lgkmcnt(1)
	v_mfma_f32_16x16x32_f16 v[142:145], v[14:17], v[30:33], v[142:145]
	v_mfma_f32_16x16x32_f16 v[146:149], v[10:13], v[30:33], v[146:149]
	s_waitcnt lgkmcnt(0)
	v_mfma_f32_16x16x32_f16 v[212:215], v[14:17], v[58:61], v[212:215]
	v_mfma_f32_16x16x32_f16 v[224:227], v[10:13], v[58:61], v[62:65]
	ds_read_b128 v[30:33], v151 offset:3968
	ds_read_b128 v[58:61], v151 offset:4576
	s_waitcnt lgkmcnt(1)
	v_mfma_f32_16x16x32_f16 v[166:169], v[14:17], v[30:33], v[166:169]
	v_mfma_f32_16x16x32_f16 v[158:161], v[10:13], v[30:33], v[158:161]
	s_waitcnt lgkmcnt(0)
	v_mfma_f32_16x16x32_f16 v[170:173], v[14:17], v[58:61], v[170:173]
	v_mfma_f32_16x16x32_f16 v[162:165], v[10:13], v[58:61], v[162:165]
	v_add_u32_e32 v30, 0x70540, v244
	v_min_u32_e32 v30, v30, v157
	global_load_dwordx4 v[70:73], v30, s[8:9] nt
	s_waitcnt vmcnt(21)
	v_cvt_pk_f16_f32 v31, v80, v81
	v_cvt_pk_f16_f32 v30, v78, v79
	ds_write_b16 v238, v30 offset:3040
	ds_write_b16_d16_hi v239, v30 offset:3040
	ds_write_b16 v240, v31 offset:3040
	ds_write_b16_d16_hi v241, v31 offset:3040
	ds_read_b128 v[30:33], v151 offset:5184
	ds_read_b128 v[58:61], v151 offset:5792
	s_waitcnt lgkmcnt(1)
	v_mfma_f32_16x16x32_f16 v[174:177], v[14:17], v[30:33], v[174:177]
	v_mfma_f32_16x16x32_f16 v[178:181], v[10:13], v[30:33], v[178:181]
	s_waitcnt lgkmcnt(0)
	v_mfma_f32_16x16x32_f16 v[186:189], v[14:17], v[58:61], v[186:189]
	v_mfma_f32_16x16x32_f16 v[190:193], v[10:13], v[58:61], v[190:193]
	ds_read_b128 v[30:33], v151 offset:6400
	ds_read_b128 v[58:61], v151 offset:7008
	s_waitcnt lgkmcnt(1)
	v_mfma_f32_16x16x32_f16 v[194:197], v[14:17], v[30:33], v[194:197]
	v_mfma_f32_16x16x32_f16 v[182:185], v[10:13], v[30:33], v[182:185]
	s_waitcnt lgkmcnt(0)
	v_mfma_f32_16x16x32_f16 v[202:205], v[14:17], v[58:61], v[204:207]
	v_mfma_f32_16x16x32_f16 v[206:209], v[10:13], v[58:61], v[208:211]
	v_add_u32_e32 v30, 0x86b80, v150
	v_min_u32_e32 v30, v30, v157
	global_load_dwordx4 v[74:77], v30, s[8:9] nt
	s_waitcnt vmcnt(21)
	v_cvt_pk_f16_f32 v31, v84, v85
	v_cvt_pk_f16_f32 v30, v82, v83
	ds_write_b16 v234, v30 offset:3648
	ds_write_b16_d16_hi v235, v30 offset:3648
	ds_write_b16 v236, v31 offset:3648
	ds_write_b16_d16_hi v237, v31 offset:3648
	ds_read_b128 v[78:81], v151 offset:7616
	s_mov_b32 s2, 0x28000
	s_waitcnt lgkmcnt(0)
	v_mfma_f32_16x16x32_f16 v[220:223], v[14:17], v[78:81], v[220:223]
	v_add_co_u32_e32 v14, vcc, s2, v152
	s_mov_b32 s2, 0x2c000
	s_nop 0
	v_addc_co_u32_e32 v15, vcc, 0, v153, vcc
	global_load_dwordx4 v[58:61], v[14:15], off sc1
	global_load_dwordx4 v[62:65], v[14:15], off offset:256 sc1
	v_add_co_u32_e32 v14, vcc, s2, v152
	v_mfma_f32_16x16x32_f16 v[2:5], v[10:13], v[78:81], v[2:5]
	s_nop 0
	v_addc_co_u32_e32 v15, vcc, 0, v153, vcc
	global_load_dwordx4 v[30:33], v[14:15], off sc1
	s_nop 0
	global_load_dwordx4 v[14:17], v[14:15], off offset:256 sc1
	ds_read_b128 v[10:13], v151 offset:384
	ds_read_b128 v[78:81], v151 offset:992
	s_waitcnt vmcnt(24) lgkmcnt(1)
	v_mfma_f32_16x16x32_f16 v[198:201], v[50:53], v[10:13], v[198:201]
	s_waitcnt vmcnt(23)
	v_mfma_f32_16x16x32_f16 v[10:13], v[54:57], v[10:13], v[38:41]
	s_waitcnt lgkmcnt(0)
	v_mfma_f32_16x16x32_f16 v[38:41], v[50:53], v[78:81], v[122:125]
	v_mfma_f32_16x16x32_f16 v[122:125], v[54:57], v[78:81], v[216:219]
	ds_read_b128 v[78:81], v151 offset:1600
	s_waitcnt lgkmcnt(0)
	v_mfma_f32_16x16x32_f16 v[126:129], v[50:53], v[78:81], v[126:129]
	v_mfma_f32_16x16x32_f16 v[130:133], v[54:57], v[78:81], v[130:133]
	v_add_u32_e32 v78, 0x9d1c0, v244
	v_min_u32_e32 v78, v78, v157
	global_load_dwordx4 v[78:81], v78, s[8:9] nt
	s_waitcnt vmcnt(21)
	v_cvt_pk_f16_f32 v83, v88, v89
	v_cvt_pk_f16_f32 v82, v86, v87
	ds_write_b16 v238, v82 offset:4256
	ds_write_b16_d16_hi v239, v82 offset:4256
	ds_write_b16 v240, v83 offset:4256
	ds_write_b16_d16_hi v241, v83 offset:4256
	ds_read_b128 v[82:85], v151 offset:2208
	ds_read_b128 v[86:89], v151 offset:2816
	s_waitcnt lgkmcnt(1)
	v_mfma_f32_16x16x32_f16 v[134:137], v[50:53], v[82:85], v[134:137]
	v_mfma_f32_16x16x32_f16 v[138:141], v[54:57], v[82:85], v[138:141]
	s_waitcnt lgkmcnt(0)
	v_mfma_f32_16x16x32_f16 v[142:145], v[50:53], v[86:89], v[142:145]
	v_mfma_f32_16x16x32_f16 v[146:149], v[54:57], v[86:89], v[146:149]
	ds_read_b128 v[82:85], v151 offset:3424
	ds_read_b128 v[86:89], v151 offset:4032
	s_waitcnt lgkmcnt(1)
	v_mfma_f32_16x16x32_f16 v[210:213], v[50:53], v[82:85], v[212:215]
	v_mfma_f32_16x16x32_f16 v[214:217], v[54:57], v[82:85], v[224:227]
	s_waitcnt lgkmcnt(0)
	v_mfma_f32_16x16x32_f16 v[166:169], v[50:53], v[86:89], v[166:169]
	v_mfma_f32_16x16x32_f16 v[158:161], v[54:57], v[86:89], v[158:161]
	v_add_u32_e32 v82, 0xb3800, v150
	v_min_u32_e32 v82, v82, v157
	global_load_dwordx4 v[82:85], v82, s[8:9] nt
	s_waitcnt vmcnt(21)
	v_cvt_pk_f16_f32 v87, v92, v93
	v_cvt_pk_f16_f32 v86, v90, v91
	ds_write_b16 v234, v86 offset:4864
	ds_write_b16_d16_hi v235, v86 offset:4864
	ds_write_b16 v236, v87 offset:4864
	ds_write_b16_d16_hi v237, v87 offset:4864
	ds_read_b128 v[86:89], v151 offset:4640
	ds_read_b128 v[90:93], v151 offset:6464
	s_waitcnt lgkmcnt(1)
	v_mfma_f32_16x16x32_f16 v[170:173], v[50:53], v[86:89], v[170:173]
	v_mfma_f32_16x16x32_f16 v[162:165], v[54:57], v[86:89], v[162:165]
	ds_read_b128 v[86:89], v151 offset:5248
	ds_read_b128 v[224:227], v151 offset:5856
	s_waitcnt lgkmcnt(1)
	v_mfma_f32_16x16x32_f16 v[174:177], v[50:53], v[86:89], v[174:177]
	v_mfma_f32_16x16x32_f16 v[178:181], v[54:57], v[86:89], v[178:181]
	s_waitcnt lgkmcnt(0)
	v_mfma_f32_16x16x32_f16 v[186:189], v[50:53], v[224:227], v[186:189]
	v_mfma_f32_16x16x32_f16 v[190:193], v[54:57], v[224:227], v[190:193]
	v_mfma_f32_16x16x32_f16 v[194:197], v[50:53], v[90:93], v[194:197]
	v_mfma_f32_16x16x32_f16 v[182:185], v[54:57], v[90:93], v[182:185]
	v_add_u32_e32 v86, 0xc9e40, v244
	v_min_u32_e32 v86, v86, v157
	global_load_dwordx4 v[86:89], v86, s[8:9] nt
	s_waitcnt vmcnt(21)
	v_cvt_pk_f16_f32 v91, v96, v97
	v_cvt_pk_f16_f32 v90, v94, v95
	ds_write_b16 v238, v90 offset:5472
	ds_write_b16_d16_hi v239, v90 offset:5472
	ds_write_b16 v240, v91 offset:5472
	ds_write_b16_d16_hi v241, v91 offset:5472
	ds_read_b128 v[90:93], v151 offset:7072
	ds_read_b128 v[94:97], v151 offset:7680
	s_waitcnt lgkmcnt(1)
	v_mfma_f32_16x16x32_f16 v[202:205], v[50:53], v[90:93], v[202:205]
	v_mfma_f32_16x16x32_f16 v[206:209], v[54:57], v[90:93], v[206:209]
	s_waitcnt lgkmcnt(0)
	v_mfma_f32_16x16x32_f16 v[218:221], v[50:53], v[94:97], v[220:223]
	v_mfma_f32_16x16x32_f16 v[54:57], v[54:57], v[94:97], v[2:5]
	s_nop 2
	ds_read_b128 v[2:5], v151 offset:448
	ds_read_b128 v[50:53], v151 offset:1056
	s_waitcnt lgkmcnt(1)
	v_mfma_f32_16x16x32_f16 v[198:201], v[26:29], v[2:5], v[198:201]
	v_mfma_f32_16x16x32_f16 v[222:225], v[18:21], v[2:5], v[10:13]
	s_waitcnt lgkmcnt(0)
	v_mfma_f32_16x16x32_f16 v[226:229], v[26:29], v[50:53], v[38:41]
	v_mfma_f32_16x16x32_f16 v[122:125], v[18:21], v[50:53], v[122:125]
	v_add_u32_e32 v2, 0xe0480, v150
	v_min_u32_e32 v2, v2, v157
	global_load_dwordx4 v[90:93], v2, s[8:9] nt
	s_waitcnt vmcnt(21)
	v_cvt_pk_f16_f32 v3, v100, v101
	v_cvt_pk_f16_f32 v2, v98, v99
	ds_write_b16 v234, v2 offset:6080
	ds_write_b16_d16_hi v235, v2 offset:6080
	ds_write_b16 v236, v3 offset:6080
	ds_write_b16_d16_hi v237, v3 offset:6080
	ds_read_b128 v[2:5], v151 offset:1664
	ds_read_b128 v[10:13], v151 offset:2272
	s_waitcnt lgkmcnt(1)
	v_mfma_f32_16x16x32_f16 v[126:129], v[26:29], v[2:5], v[126:129]
	v_mfma_f32_16x16x32_f16 v[130:133], v[18:21], v[2:5], v[130:133]
	s_waitcnt lgkmcnt(0)
	v_mfma_f32_16x16x32_f16 v[134:137], v[26:29], v[10:13], v[134:137]
	v_mfma_f32_16x16x32_f16 v[138:141], v[18:21], v[10:13], v[138:141]
	ds_read_b128 v[2:5], v151 offset:2880
	ds_read_b128 v[10:13], v151 offset:3488
	s_waitcnt lgkmcnt(1)
	v_mfma_f32_16x16x32_f16 v[142:145], v[26:29], v[2:5], v[142:145]
	v_mfma_f32_16x16x32_f16 v[146:149], v[18:21], v[2:5], v[146:149]
	s_waitcnt lgkmcnt(0)
	v_mfma_f32_16x16x32_f16 v[210:213], v[26:29], v[10:13], v[210:213]
	v_mfma_f32_16x16x32_f16 v[214:217], v[18:21], v[10:13], v[214:217]
	v_add_u32_e32 v2, 0xf6ac0, v244
	v_min_u32_e32 v2, v2, v157
	global_load_dwordx4 v[94:97], v2, s[8:9] nt
	s_waitcnt vmcnt(21)
	v_cvt_pk_f16_f32 v3, v104, v105
	v_cvt_pk_f16_f32 v2, v102, v103
	ds_write_b16 v238, v2 offset:6688
	ds_write_b16_d16_hi v239, v2 offset:6688
	ds_write_b16 v240, v3 offset:6688
	ds_write_b16_d16_hi v241, v3 offset:6688
	ds_read_b128 v[2:5], v151 offset:4096
	ds_read_b128 v[10:13], v151 offset:4704
	s_waitcnt lgkmcnt(1)
	v_mfma_f32_16x16x32_f16 v[166:169], v[26:29], v[2:5], v[166:169]
	v_mfma_f32_16x16x32_f16 v[158:161], v[18:21], v[2:5], v[158:161]
	s_waitcnt lgkmcnt(0)
	v_mfma_f32_16x16x32_f16 v[170:173], v[26:29], v[10:13], v[170:173]
	v_mfma_f32_16x16x32_f16 v[162:165], v[18:21], v[10:13], v[162:165]
	ds_read_b128 v[2:5], v151 offset:5312
	ds_read_b128 v[10:13], v151 offset:5920
	s_waitcnt lgkmcnt(1)
	v_mfma_f32_16x16x32_f16 v[174:177], v[26:29], v[2:5], v[174:177]
	v_mfma_f32_16x16x32_f16 v[178:181], v[18:21], v[2:5], v[178:181]
	s_waitcnt lgkmcnt(0)
	v_mfma_f32_16x16x32_f16 v[186:189], v[26:29], v[10:13], v[186:189]
	v_mfma_f32_16x16x32_f16 v[190:193], v[18:21], v[10:13], v[190:193]
	v_add_u32_e32 v2, 0x10d100, v150
	v_min_u32_e32 v2, v2, v157
	v_cndmask_b32_e64 v2, 0, v2, s[0:1]
	global_load_dwordx4 v[98:101], v2, s[8:9] nt
	s_waitcnt vmcnt(21)
	v_cvt_pk_f16_f32 v3, v108, v109
	v_cvt_pk_f16_f32 v2, v106, v107
	ds_write_b16 v234, v2 offset:7296
	ds_write_b16_d16_hi v235, v2 offset:7296
	ds_write_b16 v236, v3 offset:7296
	ds_write_b16_d16_hi v237, v3 offset:7296
	ds_read_b128 v[2:5], v151 offset:6528
	ds_read_b128 v[10:13], v151 offset:7136
	s_mov_b32 s2, 0x30000
	ds_read_b128 v[102:105], v151 offset:7744
	s_waitcnt lgkmcnt(0)
	v_mfma_f32_16x16x32_f16 v[194:197], v[26:29], v[2:5], v[194:197]
	s_barrier
	v_sub_u32_e32 v245, v234, v243
	v_add_u32_e32 v246, 0xfffffdc0, v245
	v_min_u32_e32 v245, v245, v246
	v_add_u32_e32 v234, v242, v245
	v_sub_u32_e32 v245, v235, v243
	v_add_u32_e32 v246, 0xfffffdc0, v245
	v_min_u32_e32 v245, v245, v246
	v_add_u32_e32 v235, v242, v245
	v_sub_u32_e32 v245, v236, v243
	v_add_u32_e32 v246, 0xfffffdc0, v245
	v_min_u32_e32 v245, v245, v246
	v_add_u32_e32 v236, v242, v245
	v_sub_u32_e32 v245, v237, v243
	v_add_u32_e32 v246, 0xfffffdc0, v245
	v_min_u32_e32 v245, v245, v246
	v_add_u32_e32 v237, v242, v245
	v_sub_u32_e32 v245, v238, v243
	v_add_u32_e32 v246, 0xfffffdc0, v245
	v_min_u32_e32 v245, v245, v246
	v_add_u32_e32 v238, v242, v245
	v_sub_u32_e32 v245, v239, v243
	v_add_u32_e32 v246, 0xfffffdc0, v245
	v_min_u32_e32 v245, v245, v246
	v_add_u32_e32 v239, v242, v245
	v_sub_u32_e32 v245, v240, v243
	v_add_u32_e32 v246, 0xfffffdc0, v245
	v_min_u32_e32 v245, v245, v246
	v_add_u32_e32 v240, v242, v245
	v_sub_u32_e32 v245, v241, v243
	v_add_u32_e32 v246, 0xfffffdc0, v245
	v_min_u32_e32 v245, v245, v246
	v_add_u32_e32 v241, v242, v245
	v_mfma_f32_16x16x32_f16 v[182:185], v[18:21], v[2:5], v[182:185]
	v_add_co_u32_e32 v2, vcc, s2, v152
	s_mov_b32 s2, 0x34000
	s_nop 0
	v_addc_co_u32_e32 v3, vcc, 0, v153, vcc
	global_load_dwordx4 v[38:41], v[2:3], off sc1
	global_load_dwordx4 v[50:53], v[2:3], off offset:256 sc1
	v_add_co_u32_e32 v2, vcc, s2, v152
	v_mfma_f32_16x16x32_f16 v[202:205], v[26:29], v[10:13], v[202:205]
	s_nop 0
	v_addc_co_u32_e32 v3, vcc, 0, v153, vcc
	v_mfma_f32_16x16x32_f16 v[206:209], v[18:21], v[10:13], v[206:209]
	global_load_dwordx4 v[10:13], v[2:3], off sc1
	s_nop 0
	global_load_dwordx4 v[2:5], v[2:3], off offset:256 sc1
	v_mfma_f32_16x16x32_f16 v[26:29], v[26:29], v[102:105], v[218:221]
	v_mfma_f32_16x16x32_f16 v[18:21], v[18:21], v[102:105], v[54:57]
	v_add_u32_e32 v157, 0x11151cdc, v154
	s_nop 1
	ds_read_b128 v[54:57], v151 offset:512
	v_add_u32_e32 v102, 0x800, v150
	s_waitcnt vmcnt(24) lgkmcnt(0)
	v_mfma_f32_16x16x32_f16 v[198:201], v[42:45], v[54:57], v[198:201]
	s_waitcnt vmcnt(23)
	v_mfma_f32_16x16x32_f16 v[54:57], v[46:49], v[54:57], v[222:225]
	v_min_u32_e32 v102, v102, v157
	global_load_dwordx4 v[102:105], v102, s[8:9] nt
	s_waitcnt vmcnt(21)
	v_cvt_pk_f16_f32 v107, v112, v113
	v_cvt_pk_f16_f32 v106, v110, v111
	ds_write_b16 v234, v106 offset:0
	ds_write_b16_d16_hi v235, v106 offset:0
	ds_write_b16 v236, v107 offset:0
	ds_write_b16_d16_hi v237, v107 offset:0
	ds_read_b128 v[106:109], v151 offset:1120
	ds_read_b128 v[110:113], v151 offset:1728
	s_waitcnt lgkmcnt(1)
	v_mfma_f32_16x16x32_f16 v[218:221], v[42:45], v[106:109], v[226:229]
	v_mfma_f32_16x16x32_f16 v[122:125], v[46:49], v[106:109], v[122:125]
	s_waitcnt lgkmcnt(0)
	v_mfma_f32_16x16x32_f16 v[126:129], v[42:45], v[110:113], v[126:129]
	v_mfma_f32_16x16x32_f16 v[130:133], v[46:49], v[110:113], v[130:133]
	ds_read_b128 v[106:109], v151 offset:2336
	ds_read_b128 v[110:113], v151 offset:2944
	s_waitcnt lgkmcnt(1)
	v_mfma_f32_16x16x32_f16 v[134:137], v[42:45], v[106:109], v[134:137]
	v_mfma_f32_16x16x32_f16 v[138:141], v[46:49], v[106:109], v[138:141]
	s_waitcnt lgkmcnt(0)
	v_mfma_f32_16x16x32_f16 v[142:145], v[42:45], v[110:113], v[142:145]
	v_mfma_f32_16x16x32_f16 v[146:149], v[46:49], v[110:113], v[146:149]
	v_add_u32_e32 v106, 0x16e40, v244
	v_min_u32_e32 v106, v106, v157
	global_load_dwordx4 v[106:109], v106, s[8:9] nt
	s_waitcnt vmcnt(21)
	v_cvt_pk_f16_f32 v111, v116, v117
	v_cvt_pk_f16_f32 v110, v114, v115
	ds_write_b16 v238, v110 offset:608
	ds_write_b16_d16_hi v239, v110 offset:608
	ds_write_b16 v240, v111 offset:608
	ds_write_b16_d16_hi v241, v111 offset:608
	ds_read_b128 v[110:113], v151 offset:3552
	ds_read_b128 v[114:117], v151 offset:5376
	s_waitcnt lgkmcnt(1)
	v_mfma_f32_16x16x32_f16 v[210:213], v[42:45], v[110:113], v[210:213]
	v_mfma_f32_16x16x32_f16 v[214:217], v[46:49], v[110:113], v[214:217]
	ds_read_b128 v[110:113], v151 offset:4160
	ds_read_b128 v[222:225], v151 offset:4768
	s_waitcnt lgkmcnt(1)
	v_mfma_f32_16x16x32_f16 v[166:169], v[42:45], v[110:113], v[166:169]
	v_mfma_f32_16x16x32_f16 v[158:161], v[46:49], v[110:113], v[158:161]
	s_waitcnt lgkmcnt(0)
	v_mfma_f32_16x16x32_f16 v[170:173], v[42:45], v[222:225], v[170:173]
	v_mfma_f32_16x16x32_f16 v[162:165], v[46:49], v[222:225], v[162:165]
	v_mfma_f32_16x16x32_f16 v[174:177], v[42:45], v[114:117], v[174:177]
	v_mfma_f32_16x16x32_f16 v[178:181], v[46:49], v[114:117], v[178:181]
	v_add_u32_e32 v110, 0x2d480, v150
	v_min_u32_e32 v110, v110, v157
	global_load_dwordx4 v[110:113], v110, s[8:9] nt
	s_waitcnt vmcnt(21)
	v_cvt_pk_f16_f32 v115, v120, v121
	v_cvt_pk_f16_f32 v114, v118, v119
	ds_write_b16 v234, v114 offset:1216
	ds_write_b16_d16_hi v235, v114 offset:1216
	ds_write_b16 v236, v115 offset:1216
	ds_write_b16_d16_hi v237, v115 offset:1216
	ds_read_b128 v[114:117], v151 offset:5984
	ds_read_b128 v[118:121], v151 offset:6592
	s_waitcnt lgkmcnt(1)
	v_mfma_f32_16x16x32_f16 v[186:189], v[42:45], v[114:117], v[186:189]
	v_mfma_f32_16x16x32_f16 v[190:193], v[46:49], v[114:117], v[190:193]
	s_waitcnt lgkmcnt(0)
	v_mfma_f32_16x16x32_f16 v[194:197], v[42:45], v[118:121], v[194:197]
	v_mfma_f32_16x16x32_f16 v[182:185], v[46:49], v[118:121], v[182:185]
	ds_read_b128 v[114:117], v151 offset:7200
	ds_read_b128 v[118:121], v151 offset:7808
	s_waitcnt lgkmcnt(1)
	v_mfma_f32_16x16x32_f16 v[202:205], v[42:45], v[114:117], v[202:205]
	v_mfma_f32_16x16x32_f16 v[206:209], v[46:49], v[114:117], v[206:209]
	s_waitcnt lgkmcnt(0)
	v_mfma_f32_16x16x32_f16 v[26:29], v[42:45], v[118:121], v[26:29]
	v_mfma_f32_16x16x32_f16 v[42:45], v[46:49], v[118:121], v[18:21]
	s_nop 2
	v_add_u32_e32 v18, 0x43ac0, v244
	v_min_u32_e32 v18, v18, v157
	global_load_dwordx4 v[114:117], v18, s[8:9] nt
	s_waitcnt vmcnt(21)
	v_cvt_pk_f16_f32 v19, v36, v37
	v_cvt_pk_f16_f32 v18, v34, v35
	ds_write_b16 v238, v18 offset:1824
	ds_write_b16_d16_hi v239, v18 offset:1824
	ds_write_b16 v240, v19 offset:1824
	ds_write_b16_d16_hi v241, v19 offset:1824
	ds_read_b128 v[18:21], v151 offset:0
	ds_read_b128 v[34:37], v151 offset:608
	s_waitcnt lgkmcnt(1)
	v_mfma_f32_16x16x32_f16 v[46:49], v[22:25], v[18:21], v[198:201]
	v_mfma_f32_16x16x32_f16 v[198:201], v[6:9], v[18:21], v[54:57]
	s_waitcnt lgkmcnt(0)
	v_mfma_f32_16x16x32_f16 v[218:221], v[22:25], v[34:37], v[218:221]
	v_mfma_f32_16x16x32_f16 v[222:225], v[6:9], v[34:37], v[122:125]
	ds_read_b128 v[18:21], v151 offset:1216
	ds_read_b128 v[34:37], v151 offset:1824
	s_waitcnt lgkmcnt(1)
	v_mfma_f32_16x16x32_f16 v[126:129], v[22:25], v[18:21], v[126:129]
	v_mfma_f32_16x16x32_f16 v[130:133], v[6:9], v[18:21], v[130:133]
	s_waitcnt lgkmcnt(0)
	v_mfma_f32_16x16x32_f16 v[134:137], v[22:25], v[34:37], v[134:137]
	v_mfma_f32_16x16x32_f16 v[138:141], v[6:9], v[34:37], v[138:141]
	v_add_u32_e32 v18, 0x5a100, v150
	v_min_u32_e32 v18, v18, v157
	global_load_dwordx4 v[118:121], v18, s[8:9] nt
	s_waitcnt vmcnt(21)
	v_cvt_pk_f16_f32 v19, v68, v69
	v_cvt_pk_f16_f32 v18, v66, v67
	ds_write_b16 v234, v18 offset:2432
	ds_write_b16_d16_hi v235, v18 offset:2432
	ds_write_b16 v236, v19 offset:2432
	ds_write_b16_d16_hi v237, v19 offset:2432
	ds_read_b128 v[18:21], v151 offset:2432
	ds_read_b128 v[34:37], v151 offset:3040
	s_waitcnt lgkmcnt(1)
	v_mfma_f32_16x16x32_f16 v[142:145], v[22:25], v[18:21], v[142:145]
	v_mfma_f32_16x16x32_f16 v[146:149], v[6:9], v[18:21], v[146:149]
	s_waitcnt lgkmcnt(0)
	v_mfma_f32_16x16x32_f16 v[210:213], v[22:25], v[34:37], v[210:213]
	v_mfma_f32_16x16x32_f16 v[214:217], v[6:9], v[34:37], v[214:217]
	ds_read_b128 v[18:21], v151 offset:3648
	ds_read_b128 v[34:37], v151 offset:4256
	s_waitcnt lgkmcnt(1)
	v_mfma_f32_16x16x32_f16 v[166:169], v[22:25], v[18:21], v[166:169]
	v_mfma_f32_16x16x32_f16 v[158:161], v[6:9], v[18:21], v[158:161]
	s_waitcnt lgkmcnt(0)
	v_mfma_f32_16x16x32_f16 v[170:173], v[22:25], v[34:37], v[170:173]
	v_mfma_f32_16x16x32_f16 v[162:165], v[6:9], v[34:37], v[162:165]
	v_add_u32_e32 v18, 0x70740, v244
	v_min_u32_e32 v18, v18, v157
	global_load_dwordx4 v[122:125], v18, s[8:9] nt
	s_waitcnt vmcnt(21)
	v_cvt_pk_f16_f32 v19, v72, v73
	v_cvt_pk_f16_f32 v18, v70, v71
	ds_write_b16 v238, v18 offset:3040
	ds_write_b16_d16_hi v239, v18 offset:3040
	ds_write_b16 v240, v19 offset:3040
	ds_write_b16_d16_hi v241, v19 offset:3040
	ds_read_b128 v[18:21], v151 offset:4864
	ds_read_b128 v[34:37], v151 offset:5472
	s_waitcnt lgkmcnt(1)
	v_mfma_f32_16x16x32_f16 v[174:177], v[22:25], v[18:21], v[174:177]
	v_mfma_f32_16x16x32_f16 v[178:181], v[6:9], v[18:21], v[178:181]
	s_waitcnt lgkmcnt(0)
	v_mfma_f32_16x16x32_f16 v[186:189], v[22:25], v[34:37], v[186:189]
	v_mfma_f32_16x16x32_f16 v[190:193], v[6:9], v[34:37], v[190:193]
	ds_read_b128 v[18:21], v151 offset:6080
	ds_read_b128 v[34:37], v151 offset:6688
	s_waitcnt lgkmcnt(1)
	v_mfma_f32_16x16x32_f16 v[194:197], v[22:25], v[18:21], v[194:197]
	v_mfma_f32_16x16x32_f16 v[182:185], v[6:9], v[18:21], v[182:185]
	s_waitcnt lgkmcnt(0)
	v_mfma_f32_16x16x32_f16 v[202:205], v[22:25], v[34:37], v[202:205]
	v_mfma_f32_16x16x32_f16 v[206:209], v[6:9], v[34:37], v[206:209]
	v_add_u32_e32 v18, 0x86d80, v150
	v_min_u32_e32 v18, v18, v157
	global_load_dwordx4 v[70:73], v18, s[8:9] nt
	s_waitcnt vmcnt(21)
	v_cvt_pk_f16_f32 v19, v76, v77
	v_cvt_pk_f16_f32 v18, v74, v75
	ds_write_b16 v234, v18 offset:3648
	ds_write_b16_d16_hi v235, v18 offset:3648
	ds_write_b16 v236, v19 offset:3648
	ds_write_b16_d16_hi v237, v19 offset:3648
	s_mov_b32 s2, 0x38000
	v_add_co_u32_e32 v18, vcc, s2, v152
	s_mov_b32 s2, 0x3c000
	s_nop 0
	v_addc_co_u32_e32 v19, vcc, 0, v153, vcc
	ds_read_b128 v[74:77], v151 offset:7296
	global_load_dwordx4 v[54:57], v[18:19], off sc1
	global_load_dwordx4 v[66:69], v[18:19], off offset:256 sc1
	v_add_co_u32_e32 v18, vcc, s2, v152
	s_waitcnt lgkmcnt(0)
	v_mfma_f32_16x16x32_f16 v[22:25], v[22:25], v[74:77], v[26:29]
	v_addc_co_u32_e32 v19, vcc, 0, v153, vcc
	global_load_dwordx4 v[34:37], v[18:19], off sc1
	s_nop 0
	global_load_dwordx4 v[18:21], v[18:19], off offset:256 sc1
	v_mfma_f32_16x16x32_f16 v[6:9], v[6:9], v[74:77], v[42:45]
	ds_read_b128 v[26:29], v151 offset:64
	s_nop 1
	ds_read_b128 v[42:45], v151 offset:672
	s_waitcnt vmcnt(24) lgkmcnt(1)
	v_mfma_f32_16x16x32_f16 v[46:49], v[58:61], v[26:29], v[46:49]
	s_waitcnt vmcnt(23)
	v_mfma_f32_16x16x32_f16 v[26:29], v[62:65], v[26:29], v[198:201]
	s_nop 2
	ds_read_b128 v[198:201], v151 offset:1280
	s_waitcnt lgkmcnt(1)
	v_mfma_f32_16x16x32_f16 v[74:77], v[58:61], v[42:45], v[218:221]
	v_mfma_f32_16x16x32_f16 v[42:45], v[62:65], v[42:45], v[222:225]
	s_waitcnt lgkmcnt(0)
	v_mfma_f32_16x16x32_f16 v[218:221], v[58:61], v[198:201], v[126:129]
	v_mfma_f32_16x16x32_f16 v[130:133], v[62:65], v[198:201], v[130:133]
	s_nop 1
	v_add_u32_e32 v126, 0x9d3c0, v244
	v_min_u32_e32 v126, v126, v157
	global_load_dwordx4 v[126:129], v126, s[8:9] nt
	s_waitcnt vmcnt(21)
	v_cvt_pk_f16_f32 v81, v80, v81
	v_cvt_pk_f16_f32 v80, v78, v79
	ds_write_b16 v238, v80 offset:4256
	ds_write_b16_d16_hi v239, v80 offset:4256
	ds_write_b16 v240, v81 offset:4256
	ds_write_b16_d16_hi v241, v81 offset:4256
	ds_read_b128 v[78:81], v151 offset:1888
	ds_read_b128 v[198:201], v151 offset:2496
	s_waitcnt lgkmcnt(1)
	v_mfma_f32_16x16x32_f16 v[134:137], v[58:61], v[78:81], v[134:137]
	v_mfma_f32_16x16x32_f16 v[138:141], v[62:65], v[78:81], v[138:141]
	s_waitcnt lgkmcnt(0)
	v_mfma_f32_16x16x32_f16 v[142:145], v[58:61], v[198:201], v[142:145]
	v_mfma_f32_16x16x32_f16 v[146:149], v[62:65], v[198:201], v[146:149]
	ds_read_b128 v[78:81], v151 offset:3104
	ds_read_b128 v[198:201], v151 offset:3712
	s_waitcnt lgkmcnt(1)
	v_mfma_f32_16x16x32_f16 v[210:213], v[58:61], v[78:81], v[210:213]
	v_mfma_f32_16x16x32_f16 v[214:217], v[62:65], v[78:81], v[214:217]
	s_waitcnt lgkmcnt(0)
	v_mfma_f32_16x16x32_f16 v[166:169], v[58:61], v[198:201], v[166:169]
	v_mfma_f32_16x16x32_f16 v[158:161], v[62:65], v[198:201], v[158:161]
	v_add_u32_e32 v78, 0xb3a00, v150
	v_min_u32_e32 v78, v78, v157
	global_load_dwordx4 v[78:81], v78, s[8:9] nt
	s_waitcnt vmcnt(21)
	v_cvt_pk_f16_f32 v85, v84, v85
	v_cvt_pk_f16_f32 v84, v82, v83
	ds_write_b16 v234, v84 offset:4864
	ds_write_b16_d16_hi v235, v84 offset:4864
	ds_write_b16 v236, v85 offset:4864
	ds_write_b16_d16_hi v237, v85 offset:4864
	ds_read_b128 v[82:85], v151 offset:4320
	ds_read_b128 v[198:201], v151 offset:6144
	s_waitcnt lgkmcnt(1)
	v_mfma_f32_16x16x32_f16 v[170:173], v[58:61], v[82:85], v[170:173]
	v_mfma_f32_16x16x32_f16 v[162:165], v[62:65], v[82:85], v[162:165]
	ds_read_b128 v[82:85], v151 offset:4928
	ds_read_b128 v[222:225], v151 offset:5536
	s_waitcnt lgkmcnt(1)
	v_mfma_f32_16x16x32_f16 v[174:177], v[58:61], v[82:85], v[174:177]
	v_mfma_f32_16x16x32_f16 v[178:181], v[62:65], v[82:85], v[178:181]
	s_waitcnt lgkmcnt(0)
	v_mfma_f32_16x16x32_f16 v[186:189], v[58:61], v[222:225], v[186:189]
	v_mfma_f32_16x16x32_f16 v[190:193], v[62:65], v[222:225], v[190:193]
	v_mfma_f32_16x16x32_f16 v[194:197], v[58:61], v[198:201], v[194:197]
	v_mfma_f32_16x16x32_f16 v[182:185], v[62:65], v[198:201], v[182:185]
	v_add_u32_e32 v82, 0xca040, v244
	v_min_u32_e32 v82, v82, v157
	global_load_dwordx4 v[82:85], v82, s[8:9] nt
	s_waitcnt vmcnt(21)
	v_cvt_pk_f16_f32 v89, v88, v89
	v_cvt_pk_f16_f32 v88, v86, v87
	ds_write_b16 v238, v88 offset:5472
	ds_write_b16_d16_hi v239, v88 offset:5472
	ds_write_b16 v240, v89 offset:5472
	ds_write_b16_d16_hi v241, v89 offset:5472
	ds_read_b128 v[86:89], v151 offset:6752
	ds_read_b128 v[198:201], v151 offset:7360
	s_waitcnt lgkmcnt(1)
	v_mfma_f32_16x16x32_f16 v[202:205], v[58:61], v[86:89], v[202:205]
	s_waitcnt lgkmcnt(0)
	v_mfma_f32_16x16x32_f16 v[22:25], v[58:61], v[198:201], v[22:25]
	v_mfma_f32_16x16x32_f16 v[198:201], v[62:65], v[198:201], v[6:9]
	s_nop 2
	ds_read_b128 v[6:9], v151 offset:128
	ds_read_b128 v[58:61], v151 offset:736
	v_mfma_f32_16x16x32_f16 v[206:209], v[62:65], v[86:89], v[206:209]
	s_waitcnt lgkmcnt(1)
	v_mfma_f32_16x16x32_f16 v[222:225], v[30:33], v[6:9], v[46:49]
	v_mfma_f32_16x16x32_f16 v[226:229], v[14:17], v[6:9], v[26:29]
	s_waitcnt lgkmcnt(0)
	v_mfma_f32_16x16x32_f16 v[74:77], v[30:33], v[58:61], v[74:77]
	v_mfma_f32_16x16x32_f16 v[230:233], v[14:17], v[58:61], v[42:45]
	v_add_u32_e32 v6, 0xe0680, v150
	v_min_u32_e32 v6, v6, v157
	global_load_dwordx4 v[58:61], v6, s[8:9] nt
	s_waitcnt vmcnt(21)
	v_cvt_pk_f16_f32 v7, v92, v93
	v_cvt_pk_f16_f32 v6, v90, v91
	ds_write_b16 v234, v6 offset:6080
	ds_write_b16_d16_hi v235, v6 offset:6080
	ds_write_b16 v236, v7 offset:6080
	ds_write_b16_d16_hi v237, v7 offset:6080
	ds_read_b128 v[6:9], v151 offset:1344
	ds_read_b128 v[26:29], v151 offset:1952
	s_waitcnt lgkmcnt(1)
	v_mfma_f32_16x16x32_f16 v[90:93], v[30:33], v[6:9], v[218:221]
	v_mfma_f32_16x16x32_f16 v[130:133], v[14:17], v[6:9], v[130:133]
	s_waitcnt lgkmcnt(0)
	v_mfma_f32_16x16x32_f16 v[134:137], v[30:33], v[26:29], v[134:137]
	v_mfma_f32_16x16x32_f16 v[138:141], v[14:17], v[26:29], v[138:141]
	ds_read_b128 v[6:9], v151 offset:2560
	ds_read_b128 v[26:29], v151 offset:3168
	s_waitcnt lgkmcnt(1)
	v_mfma_f32_16x16x32_f16 v[142:145], v[30:33], v[6:9], v[142:145]
	v_mfma_f32_16x16x32_f16 v[146:149], v[14:17], v[6:9], v[146:149]
	s_waitcnt lgkmcnt(0)
	v_mfma_f32_16x16x32_f16 v[210:213], v[30:33], v[26:29], v[210:213]
	v_mfma_f32_16x16x32_f16 v[214:217], v[14:17], v[26:29], v[214:217]
	v_add_u32_e32 v6, 0xf6cc0, v244
	v_min_u32_e32 v6, v6, v157
	global_load_dwordx4 v[62:65], v6, s[8:9] nt
	s_waitcnt vmcnt(21)
	v_cvt_pk_f16_f32 v7, v96, v97
	v_cvt_pk_f16_f32 v6, v94, v95
	ds_write_b16 v238, v6 offset:6688
	ds_write_b16_d16_hi v239, v6 offset:6688
	ds_write_b16 v240, v7 offset:6688
	ds_write_b16_d16_hi v241, v7 offset:6688
	ds_read_b128 v[6:9], v151 offset:3776
	ds_read_b128 v[26:29], v151 offset:4384
	s_waitcnt lgkmcnt(1)
	v_mfma_f32_16x16x32_f16 v[94:97], v[30:33], v[6:9], v[166:169]
	v_mfma_f32_16x16x32_f16 v[158:161], v[14:17], v[6:9], v[158:161]
	s_waitcnt lgkmcnt(0)
	v_mfma_f32_16x16x32_f16 v[166:169], v[30:33], v[26:29], v[170:173]
	v_mfma_f32_16x16x32_f16 v[162:165], v[14:17], v[26:29], v[162:165]
	ds_read_b128 v[6:9], v151 offset:4992
	ds_read_b128 v[26:29], v151 offset:5600
	s_waitcnt lgkmcnt(1)
	v_mfma_f32_16x16x32_f16 v[170:173], v[30:33], v[6:9], v[174:177]
	v_mfma_f32_16x16x32_f16 v[174:177], v[14:17], v[6:9], v[178:181]
	s_waitcnt lgkmcnt(0)
	v_mfma_f32_16x16x32_f16 v[178:181], v[30:33], v[26:29], v[186:189]
	v_mfma_f32_16x16x32_f16 v[186:189], v[14:17], v[26:29], v[190:193]
	v_add_u32_e32 v6, 0x10d300, v150
	v_min_u32_e32 v6, v6, v157
	v_cndmask_b32_e64 v6, 0, v6, s[0:1]
	global_load_dwordx4 v[86:89], v6, s[8:9] nt
	s_waitcnt vmcnt(21)
	v_cvt_pk_f16_f32 v7, v100, v101
	v_cvt_pk_f16_f32 v6, v98, v99
	ds_write_b16 v234, v6 offset:7296
	ds_write_b16_d16_hi v235, v6 offset:7296
	ds_write_b16 v236, v7 offset:7296
	ds_write_b16_d16_hi v237, v7 offset:7296
	ds_read_b128 v[6:9], v151 offset:6208
	ds_read_b128 v[26:29], v151 offset:6816
	s_mov_b32 s2, 0x40000
	ds_read_b128 v[190:193], v151 offset:7424
	s_waitcnt lgkmcnt(0)
	v_mfma_f32_16x16x32_f16 v[98:101], v[30:33], v[6:9], v[194:197]
	s_barrier
	v_sub_u32_e32 v245, v234, v243
	v_add_u32_e32 v246, 0xfffffdc0, v245
	v_min_u32_e32 v245, v245, v246
	v_add_u32_e32 v234, v242, v245
	v_sub_u32_e32 v245, v235, v243
	v_add_u32_e32 v246, 0xfffffdc0, v245
	v_min_u32_e32 v245, v245, v246
	v_add_u32_e32 v235, v242, v245
	v_sub_u32_e32 v245, v236, v243
	v_add_u32_e32 v246, 0xfffffdc0, v245
	v_min_u32_e32 v245, v245, v246
	v_add_u32_e32 v236, v242, v245
	v_sub_u32_e32 v245, v237, v243
	v_add_u32_e32 v246, 0xfffffdc0, v245
	v_min_u32_e32 v245, v245, v246
	v_add_u32_e32 v237, v242, v245
	v_sub_u32_e32 v245, v238, v243
	v_add_u32_e32 v246, 0xfffffdc0, v245
	v_min_u32_e32 v245, v245, v246
	v_add_u32_e32 v238, v242, v245
	v_sub_u32_e32 v245, v239, v243
	v_add_u32_e32 v246, 0xfffffdc0, v245
	v_min_u32_e32 v245, v245, v246
	v_add_u32_e32 v239, v242, v245
	v_sub_u32_e32 v245, v240, v243
	v_add_u32_e32 v246, 0xfffffdc0, v245
	v_min_u32_e32 v245, v245, v246
	v_add_u32_e32 v240, v242, v245
	v_sub_u32_e32 v245, v241, v243
	v_add_u32_e32 v246, 0xfffffdc0, v245
	v_min_u32_e32 v245, v245, v246
	v_add_u32_e32 v241, v242, v245
	v_mfma_f32_16x16x32_f16 v[182:185], v[14:17], v[6:9], v[182:185]
	v_add_co_u32_e32 v6, vcc, s2, v152
	s_mov_b32 s2, 0x44000
	s_nop 0
	v_addc_co_u32_e32 v7, vcc, 0, v153, vcc
	global_load_dwordx4 v[42:45], v[6:7], off sc1
	global_load_dwordx4 v[46:49], v[6:7], off offset:256 sc1
	v_add_co_u32_e32 v6, vcc, s2, v152
	v_mfma_f32_16x16x32_f16 v[194:197], v[30:33], v[26:29], v[202:205]
	s_nop 0
	v_addc_co_u32_e32 v7, vcc, 0, v153, vcc
	v_mfma_f32_16x16x32_f16 v[202:205], v[14:17], v[26:29], v[206:209]
	global_load_dwordx4 v[26:29], v[6:7], off sc1
	s_nop 0
	global_load_dwordx4 v[6:9], v[6:7], off offset:256 sc1
	v_mfma_f32_16x16x32_f16 v[22:25], v[30:33], v[190:193], v[22:25]
	v_mfma_f32_16x16x32_f16 v[30:33], v[14:17], v[190:193], v[198:201]
	v_add_u32_e32 v157, 0x11151edc, v154
	ds_read_b128 v[14:17], v151 offset:192
	v_add_u32_e32 v206, 0xa00, v150
	s_waitcnt vmcnt(24) lgkmcnt(0)
	v_mfma_f32_16x16x32_f16 v[190:193], v[38:41], v[14:17], v[222:225]
	s_waitcnt vmcnt(23)
	v_mfma_f32_16x16x32_f16 v[198:201], v[50:53], v[14:17], v[226:229]
	v_min_u32_e32 v14, v206, v157
	global_load_dwordx4 v[14:17], v14, s[8:9] nt
	s_waitcnt vmcnt(21)
	v_cvt_pk_f16_f32 v105, v104, v105
	v_cvt_pk_f16_f32 v104, v102, v103
	ds_write_b16 v234, v104 offset:0
	ds_write_b16_d16_hi v235, v104 offset:0
	ds_write_b16 v236, v105 offset:0
	ds_write_b16_d16_hi v237, v105 offset:0
	ds_read_b128 v[102:105], v151 offset:800
	ds_read_b128 v[206:209], v151 offset:1408
	s_waitcnt lgkmcnt(1)
	v_mfma_f32_16x16x32_f16 v[74:77], v[38:41], v[102:105], v[74:77]
	s_waitcnt lgkmcnt(0)
	v_mfma_f32_16x16x32_f16 v[218:221], v[38:41], v[206:209], v[90:93]
	v_mfma_f32_16x16x32_f16 v[130:133], v[50:53], v[206:209], v[130:133]
	s_nop 1
	ds_read_b128 v[90:93], v151 offset:2016
	ds_read_b128 v[206:209], v151 offset:2624
	v_mfma_f32_16x16x32_f16 v[102:105], v[50:53], v[102:105], v[230:233]
	s_waitcnt lgkmcnt(1)
	v_mfma_f32_16x16x32_f16 v[134:137], v[38:41], v[90:93], v[134:137]
	v_mfma_f32_16x16x32_f16 v[138:141], v[50:53], v[90:93], v[138:141]
	s_waitcnt lgkmcnt(0)
	v_mfma_f32_16x16x32_f16 v[142:145], v[38:41], v[206:209], v[142:145]
	v_mfma_f32_16x16x32_f16 v[146:149], v[50:53], v[206:209], v[146:149]
	v_add_u32_e32 v90, 0x17040, v244
	v_min_u32_e32 v90, v90, v157
	global_load_dwordx4 v[90:93], v90, s[8:9] nt
	s_waitcnt vmcnt(21)
	v_cvt_pk_f16_f32 v109, v108, v109
	v_cvt_pk_f16_f32 v108, v106, v107
	ds_write_b16 v238, v108 offset:608
	ds_write_b16_d16_hi v239, v108 offset:608
	ds_write_b16 v240, v109 offset:608
	ds_write_b16_d16_hi v241, v109 offset:608
	ds_read_b128 v[106:109], v151 offset:3232
	ds_read_b128 v[206:209], v151 offset:5056
	s_waitcnt lgkmcnt(1)
	v_mfma_f32_16x16x32_f16 v[210:213], v[38:41], v[106:109], v[210:213]
	v_mfma_f32_16x16x32_f16 v[106:109], v[50:53], v[106:109], v[214:217]
	s_nop 2
	ds_read_b128 v[214:217], v151 offset:3840
	ds_read_b128 v[222:225], v151 offset:4448
	s_waitcnt lgkmcnt(1)
	v_mfma_f32_16x16x32_f16 v[226:229], v[38:41], v[214:217], v[94:97]
	v_mfma_f32_16x16x32_f16 v[158:161], v[50:53], v[214:217], v[158:161]
	s_waitcnt lgkmcnt(0)
	v_mfma_f32_16x16x32_f16 v[166:169], v[38:41], v[222:225], v[166:169]
	v_mfma_f32_16x16x32_f16 v[162:165], v[50:53], v[222:225], v[162:165]
	v_mfma_f32_16x16x32_f16 v[170:173], v[38:41], v[206:209], v[170:173]
	v_mfma_f32_16x16x32_f16 v[174:177], v[50:53], v[206:209], v[174:177]
	v_add_u32_e32 v94, 0x2d680, v150
	v_min_u32_e32 v94, v94, v157
	global_load_dwordx4 v[94:97], v94, s[8:9] nt
	s_waitcnt vmcnt(21)
	v_cvt_pk_f16_f32 v113, v112, v113
	v_cvt_pk_f16_f32 v112, v110, v111
	ds_write_b16 v234, v112 offset:1216
	ds_write_b16_d16_hi v235, v112 offset:1216
	ds_write_b16 v236, v113 offset:1216
	ds_write_b16_d16_hi v237, v113 offset:1216
	ds_read_b128 v[110:113], v151 offset:5664
	ds_read_b128 v[206:209], v151 offset:6272
	s_waitcnt lgkmcnt(1)
	v_mfma_f32_16x16x32_f16 v[178:181], v[38:41], v[110:113], v[178:181]
	v_mfma_f32_16x16x32_f16 v[110:113], v[50:53], v[110:113], v[186:189]
	s_waitcnt lgkmcnt(0)
	v_mfma_f32_16x16x32_f16 v[186:189], v[38:41], v[206:209], v[98:101]
	v_mfma_f32_16x16x32_f16 v[182:185], v[50:53], v[206:209], v[182:185]
	s_nop 1
	ds_read_b128 v[98:101], v151 offset:6880
	ds_read_b128 v[206:209], v151 offset:7488
	s_waitcnt lgkmcnt(1)
	v_mfma_f32_16x16x32_f16 v[194:197], v[38:41], v[98:101], v[194:197]
	v_mfma_f32_16x16x32_f16 v[202:205], v[50:53], v[98:101], v[202:205]
	s_waitcnt lgkmcnt(0)
	v_mfma_f32_16x16x32_f16 v[22:25], v[38:41], v[206:209], v[22:25]
	v_mfma_f32_16x16x32_f16 v[30:33], v[50:53], v[206:209], v[30:33]
	v_add_u32_e32 v38, 0x43cc0, v244
	v_min_u32_e32 v38, v38, v157
	global_load_dwordx4 v[98:101], v38, s[8:9] nt
	s_waitcnt vmcnt(21)
	v_cvt_pk_f16_f32 v39, v116, v117
	v_cvt_pk_f16_f32 v38, v114, v115
	ds_write_b16 v238, v38 offset:1824
	ds_write_b16_d16_hi v239, v38 offset:1824
	ds_write_b16 v240, v39 offset:1824
	ds_write_b16_d16_hi v241, v39 offset:1824
	ds_read_b128 v[38:41], v151 offset:256
	ds_read_b128 v[50:53], v151 offset:864
	s_waitcnt lgkmcnt(1)
	v_mfma_f32_16x16x32_f16 v[114:117], v[10:13], v[38:41], v[190:193]
	v_mfma_f32_16x16x32_f16 v[190:193], v[2:5], v[38:41], v[198:201]
	s_waitcnt lgkmcnt(0)
	v_mfma_f32_16x16x32_f16 v[198:201], v[10:13], v[50:53], v[74:77]
	ds_read_b128 v[38:41], v151 offset:1472
	s_nop 1
	ds_read_b128 v[74:77], v151 offset:2080
	v_mfma_f32_16x16x32_f16 v[50:53], v[2:5], v[50:53], v[102:105]
	s_waitcnt lgkmcnt(1)
	v_mfma_f32_16x16x32_f16 v[206:209], v[10:13], v[38:41], v[218:221]
	v_mfma_f32_16x16x32_f16 v[130:133], v[2:5], v[38:41], v[130:133]
	s_waitcnt lgkmcnt(0)
	v_mfma_f32_16x16x32_f16 v[134:137], v[10:13], v[74:77], v[134:137]
	v_mfma_f32_16x16x32_f16 v[138:141], v[2:5], v[74:77], v[138:141]
	v_add_u32_e32 v38, 0x5a300, v150
	v_min_u32_e32 v38, v38, v157
	global_load_dwordx4 v[102:105], v38, s[8:9] nt
	s_waitcnt vmcnt(21)
	v_cvt_pk_f16_f32 v39, v120, v121
	v_cvt_pk_f16_f32 v38, v118, v119
	ds_write_b16 v234, v38 offset:2432
	ds_write_b16_d16_hi v235, v38 offset:2432
	ds_write_b16 v236, v39 offset:2432
	ds_write_b16_d16_hi v237, v39 offset:2432
	ds_read_b128 v[38:41], v151 offset:2688
	ds_read_b128 v[74:77], v151 offset:3296
	s_waitcnt lgkmcnt(1)
	v_mfma_f32_16x16x32_f16 v[118:121], v[10:13], v[38:41], v[142:145]
	v_mfma_f32_16x16x32_f16 v[142:145], v[2:5], v[38:41], v[146:149]
	s_waitcnt lgkmcnt(0)
	v_mfma_f32_16x16x32_f16 v[146:149], v[10:13], v[74:77], v[210:213]
	v_mfma_f32_16x16x32_f16 v[210:213], v[2:5], v[74:77], v[106:109]
	ds_read_b128 v[38:41], v151 offset:3904
	ds_read_b128 v[74:77], v151 offset:4512
	s_waitcnt lgkmcnt(1)
	v_mfma_f32_16x16x32_f16 v[214:217], v[10:13], v[38:41], v[226:229]
	v_mfma_f32_16x16x32_f16 v[158:161], v[2:5], v[38:41], v[158:161]
	s_waitcnt lgkmcnt(0)
	v_mfma_f32_16x16x32_f16 v[166:169], v[10:13], v[74:77], v[166:169]
	v_mfma_f32_16x16x32_f16 v[162:165], v[2:5], v[74:77], v[162:165]
	v_add_u32_e32 v38, 0x70940, v244
	v_min_u32_e32 v38, v38, v157
	global_load_dwordx4 v[106:109], v38, s[8:9] nt
	s_waitcnt vmcnt(21)
	v_cvt_pk_f16_f32 v39, v124, v125
	v_cvt_pk_f16_f32 v38, v122, v123
	ds_write_b16 v238, v38 offset:3040
	ds_write_b16_d16_hi v239, v38 offset:3040
	ds_write_b16 v240, v39 offset:3040
	ds_write_b16_d16_hi v241, v39 offset:3040
	ds_read_b128 v[38:41], v151 offset:5120
	ds_read_b128 v[74:77], v151 offset:5728
	s_waitcnt lgkmcnt(1)
	v_mfma_f32_16x16x32_f16 v[122:125], v[10:13], v[38:41], v[170:173]
	v_mfma_f32_16x16x32_f16 v[170:173], v[2:5], v[38:41], v[174:177]
	s_waitcnt lgkmcnt(0)
	v_mfma_f32_16x16x32_f16 v[174:177], v[10:13], v[74:77], v[178:181]
	v_mfma_f32_16x16x32_f16 v[178:181], v[2:5], v[74:77], v[110:113]
	ds_read_b128 v[38:41], v151 offset:6336
	ds_read_b128 v[74:77], v151 offset:6944
	s_waitcnt lgkmcnt(1)
	v_mfma_f32_16x16x32_f16 v[186:189], v[10:13], v[38:41], v[186:189]
	v_mfma_f32_16x16x32_f16 v[182:185], v[2:5], v[38:41], v[182:185]
	s_waitcnt lgkmcnt(0)
	v_mfma_f32_16x16x32_f16 v[194:197], v[10:13], v[74:77], v[194:197]
	v_mfma_f32_16x16x32_f16 v[202:205], v[2:5], v[74:77], v[202:205]
	v_add_u32_e32 v38, 0x86f80, v150
	v_min_u32_e32 v38, v38, v157
	global_load_dwordx4 v[110:113], v38, s[8:9] nt
	s_waitcnt vmcnt(21)
	v_cvt_pk_f16_f32 v39, v72, v73
	v_cvt_pk_f16_f32 v38, v70, v71
	ds_write_b16 v234, v38 offset:3648
	ds_write_b16_d16_hi v235, v38 offset:3648
	ds_write_b16 v236, v39 offset:3648
	ds_write_b16_d16_hi v237, v39 offset:3648
	ds_read_b128 v[218:221], v151 offset:7552
	s_mov_b32 s2, 0x48000
	s_waitcnt lgkmcnt(0)
	v_mfma_f32_16x16x32_f16 v[10:13], v[10:13], v[218:221], v[22:25]
	s_nop 2
	v_add_co_u32_e32 v22, vcc, s2, v152
	s_mov_b32 s2, 0x4c000
	s_nop 0
	v_addc_co_u32_e32 v23, vcc, 0, v153, vcc
	global_load_dwordx4 v[70:73], v[22:23], off sc1
	global_load_dwordx4 v[74:77], v[22:23], off offset:256 sc1
	v_add_co_u32_e32 v22, vcc, s2, v152
	v_mfma_f32_16x16x32_f16 v[30:33], v[2:5], v[218:221], v[30:33]
	s_nop 0
	v_addc_co_u32_e32 v23, vcc, 0, v153, vcc
	global_load_dwordx4 v[38:41], v[22:23], off sc1
	s_nop 0
	global_load_dwordx4 v[22:25], v[22:23], off offset:256 sc1
	ds_read_b128 v[2:5], v151 offset:320
	ds_read_b128 v[218:221], v151 offset:928
	s_waitcnt vmcnt(24) lgkmcnt(1)
	v_mfma_f32_16x16x32_f16 v[222:225], v[54:57], v[2:5], v[114:117]
	s_waitcnt vmcnt(23)
	v_mfma_f32_16x16x32_f16 v[190:193], v[66:69], v[2:5], v[190:193]
	ds_read_b128 v[2:5], v151 offset:1536
	s_waitcnt lgkmcnt(1)
	v_mfma_f32_16x16x32_f16 v[198:201], v[54:57], v[218:221], v[198:201]
	v_mfma_f32_16x16x32_f16 v[50:53], v[66:69], v[218:221], v[50:53]
	s_waitcnt lgkmcnt(0)
	v_mfma_f32_16x16x32_f16 v[206:209], v[54:57], v[2:5], v[206:209]
	v_mfma_f32_16x16x32_f16 v[130:133], v[66:69], v[2:5], v[130:133]
	v_add_u32_e32 v2, 0x9d5c0, v244
	v_min_u32_e32 v2, v2, v157
	global_load_dwordx4 v[2:5], v2, s[8:9] nt
	s_waitcnt vmcnt(21)
	v_cvt_pk_f16_f32 v115, v128, v129
	v_cvt_pk_f16_f32 v114, v126, v127
	ds_write_b16 v238, v114 offset:4256
	ds_write_b16_d16_hi v239, v114 offset:4256
	ds_write_b16 v240, v115 offset:4256
	ds_write_b16_d16_hi v241, v115 offset:4256
	ds_read_b128 v[114:117], v151 offset:2144
	ds_read_b128 v[126:129], v151 offset:2752
	s_waitcnt lgkmcnt(1)
	v_mfma_f32_16x16x32_f16 v[134:137], v[54:57], v[114:117], v[134:137]
	v_mfma_f32_16x16x32_f16 v[138:141], v[66:69], v[114:117], v[138:141]
	s_waitcnt lgkmcnt(0)
	v_mfma_f32_16x16x32_f16 v[118:121], v[54:57], v[126:129], v[118:121]
	v_mfma_f32_16x16x32_f16 v[126:129], v[66:69], v[126:129], v[142:145]
	ds_read_b128 v[114:117], v151 offset:3360
	s_nop 1
	ds_read_b128 v[142:145], v151 offset:3968
	s_waitcnt lgkmcnt(1)
	v_mfma_f32_16x16x32_f16 v[146:149], v[54:57], v[114:117], v[146:149]
	v_mfma_f32_16x16x32_f16 v[210:213], v[66:69], v[114:117], v[210:213]
	s_waitcnt lgkmcnt(0)
	v_mfma_f32_16x16x32_f16 v[214:217], v[54:57], v[142:145], v[214:217]
	v_mfma_f32_16x16x32_f16 v[142:145], v[66:69], v[142:145], v[158:161]
	v_add_u32_e32 v114, 0xb3c00, v150
	v_min_u32_e32 v114, v114, v157
	global_load_dwordx4 v[114:117], v114, s[8:9] nt
	s_waitcnt vmcnt(21)
	v_cvt_pk_f16_f32 v81, v80, v81
	v_cvt_pk_f16_f32 v80, v78, v79
	ds_write_b16 v234, v80 offset:4864
	ds_write_b16_d16_hi v235, v80 offset:4864
	ds_write_b16 v236, v81 offset:4864
	ds_write_b16_d16_hi v237, v81 offset:4864
	ds_read_b128 v[78:81], v151 offset:4576
	ds_read_b128 v[158:161], v151 offset:6400
	s_waitcnt lgkmcnt(1)
	v_mfma_f32_16x16x32_f16 v[166:169], v[54:57], v[78:81], v[166:169]
	v_mfma_f32_16x16x32_f16 v[162:165], v[66:69], v[78:81], v[162:165]
	ds_read_b128 v[78:81], v151 offset:5184
	ds_read_b128 v[218:221], v151 offset:5792
	s_waitcnt lgkmcnt(1)
	v_mfma_f32_16x16x32_f16 v[122:125], v[54:57], v[78:81], v[122:125]
	v_mfma_f32_16x16x32_f16 v[170:173], v[66:69], v[78:81], v[170:173]
	s_waitcnt lgkmcnt(0)
	v_mfma_f32_16x16x32_f16 v[174:177], v[54:57], v[218:221], v[174:177]
	v_mfma_f32_16x16x32_f16 v[178:181], v[66:69], v[218:221], v[178:181]
	v_mfma_f32_16x16x32_f16 v[186:189], v[54:57], v[158:161], v[186:189]
	v_mfma_f32_16x16x32_f16 v[158:161], v[66:69], v[158:161], v[182:185]
	v_add_u32_e32 v78, 0xca240, v244
	v_min_u32_e32 v78, v78, v157
	global_load_dwordx4 v[78:81], v78, s[8:9] nt
	s_waitcnt vmcnt(21)
	v_cvt_pk_f16_f32 v85, v84, v85
	v_cvt_pk_f16_f32 v84, v82, v83
	ds_write_b16 v238, v84 offset:5472
	ds_write_b16_d16_hi v239, v84 offset:5472
	ds_write_b16 v240, v85 offset:5472
	ds_write_b16_d16_hi v241, v85 offset:5472
	ds_read_b128 v[82:85], v151 offset:7008
	ds_read_b128 v[182:185], v151 offset:7616
	s_waitcnt lgkmcnt(1)
	v_mfma_f32_16x16x32_f16 v[194:197], v[54:57], v[82:85], v[194:197]
	s_waitcnt lgkmcnt(0)
	v_mfma_f32_16x16x32_f16 v[10:13], v[54:57], v[182:185], v[10:13]
	v_mfma_f32_16x16x32_f16 v[182:185], v[66:69], v[182:185], v[30:33]
	s_nop 2
	ds_read_b128 v[30:33], v151 offset:384
	ds_read_b128 v[54:57], v151 offset:992
	v_mfma_f32_16x16x32_f16 v[202:205], v[66:69], v[82:85], v[202:205]
	s_waitcnt lgkmcnt(1)
	v_mfma_f32_16x16x32_f16 v[218:221], v[34:37], v[30:33], v[222:225]
	v_mfma_f32_16x16x32_f16 v[190:193], v[18:21], v[30:33], v[190:193]
	s_waitcnt lgkmcnt(0)
	v_mfma_f32_16x16x32_f16 v[198:201], v[34:37], v[54:57], v[198:201]
	v_mfma_f32_16x16x32_f16 v[222:225], v[18:21], v[54:57], v[50:53]
	v_add_u32_e32 v30, 0xe0880, v150
	v_min_u32_e32 v30, v30, v157
	global_load_dwordx4 v[66:69], v30, s[8:9] nt
	s_waitcnt vmcnt(21)
	v_cvt_pk_f16_f32 v31, v60, v61
	v_cvt_pk_f16_f32 v30, v58, v59
	ds_write_b16 v234, v30 offset:6080
	ds_write_b16_d16_hi v235, v30 offset:6080
	ds_write_b16 v236, v31 offset:6080
	ds_write_b16_d16_hi v237, v31 offset:6080
	ds_read_b128 v[30:33], v151 offset:1600
	ds_read_b128 v[50:53], v151 offset:2208
	s_waitcnt lgkmcnt(1)
	v_mfma_f32_16x16x32_f16 v[58:61], v[34:37], v[30:33], v[206:209]
	v_mfma_f32_16x16x32_f16 v[130:133], v[18:21], v[30:33], v[130:133]
	s_waitcnt lgkmcnt(0)
	v_mfma_f32_16x16x32_f16 v[134:137], v[34:37], v[50:53], v[134:137]
	v_mfma_f32_16x16x32_f16 v[138:141], v[18:21], v[50:53], v[138:141]
	ds_read_b128 v[30:33], v151 offset:2816
	ds_read_b128 v[50:53], v151 offset:3424
	s_waitcnt lgkmcnt(1)
	v_mfma_f32_16x16x32_f16 v[206:209], v[34:37], v[30:33], v[118:121]
	v_mfma_f32_16x16x32_f16 v[126:129], v[18:21], v[30:33], v[126:129]
	s_waitcnt lgkmcnt(0)
	v_mfma_f32_16x16x32_f16 v[146:149], v[34:37], v[50:53], v[146:149]
	v_mfma_f32_16x16x32_f16 v[210:213], v[18:21], v[50:53], v[210:213]
	v_add_u32_e32 v30, 0xf6ec0, v244
	v_min_u32_e32 v30, v30, v157
	global_load_dwordx4 v[82:85], v30, s[8:9] nt
	s_waitcnt vmcnt(21)
	v_cvt_pk_f16_f32 v31, v64, v65
	v_cvt_pk_f16_f32 v30, v62, v63
	ds_write_b16 v238, v30 offset:6688
	ds_write_b16_d16_hi v239, v30 offset:6688
	ds_write_b16 v240, v31 offset:6688
	ds_write_b16_d16_hi v241, v31 offset:6688
	ds_read_b128 v[30:33], v151 offset:4032
	ds_read_b128 v[50:53], v151 offset:4640
	s_waitcnt lgkmcnt(1)
	v_mfma_f32_16x16x32_f16 v[62:65], v[34:37], v[30:33], v[214:217]
	v_mfma_f32_16x16x32_f16 v[142:145], v[18:21], v[30:33], v[142:145]
	s_waitcnt lgkmcnt(0)
	v_mfma_f32_16x16x32_f16 v[166:169], v[34:37], v[50:53], v[166:169]
	v_mfma_f32_16x16x32_f16 v[162:165], v[18:21], v[50:53], v[162:165]
	ds_read_b128 v[30:33], v151 offset:5248
	ds_read_b128 v[50:53], v151 offset:5856
	s_waitcnt lgkmcnt(1)
	v_mfma_f32_16x16x32_f16 v[214:217], v[34:37], v[30:33], v[122:125]
	v_mfma_f32_16x16x32_f16 v[170:173], v[18:21], v[30:33], v[170:173]
	s_waitcnt lgkmcnt(0)
	v_mfma_f32_16x16x32_f16 v[174:177], v[34:37], v[50:53], v[174:177]
	v_mfma_f32_16x16x32_f16 v[178:181], v[18:21], v[50:53], v[178:181]
	v_add_u32_e32 v30, 0x10d500, v150
	v_min_u32_e32 v30, v30, v157
	v_cndmask_b32_e64 v30, 0, v30, s[0:1]
	global_load_dwordx4 v[118:121], v30, s[8:9] nt
	s_waitcnt vmcnt(21)
	v_cvt_pk_f16_f32 v31, v88, v89
	v_cvt_pk_f16_f32 v30, v86, v87
	ds_write_b16 v234, v30 offset:7296
	ds_write_b16_d16_hi v235, v30 offset:7296
	ds_write_b16 v236, v31 offset:7296
	ds_write_b16_d16_hi v237, v31 offset:7296
	ds_read_b128 v[30:33], v151 offset:6464
	ds_read_b128 v[50:53], v151 offset:7072
	ds_read_b128 v[122:125], v151 offset:7680
	s_mov_b32 s2, 0x50000
	s_waitcnt lgkmcnt(0)
	v_mfma_f32_16x16x32_f16 v[86:89], v[34:37], v[30:33], v[186:189]
	s_barrier
	v_sub_u32_e32 v245, v234, v243
	v_add_u32_e32 v246, 0xfffffdc0, v245
	v_min_u32_e32 v245, v245, v246
	v_add_u32_e32 v234, v242, v245
	v_sub_u32_e32 v245, v235, v243
	v_add_u32_e32 v246, 0xfffffdc0, v245
	v_min_u32_e32 v245, v245, v246
	v_add_u32_e32 v235, v242, v245
	v_sub_u32_e32 v245, v236, v243
	v_add_u32_e32 v246, 0xfffffdc0, v245
	v_min_u32_e32 v245, v245, v246
	v_add_u32_e32 v236, v242, v245
	v_sub_u32_e32 v245, v237, v243
	v_add_u32_e32 v246, 0xfffffdc0, v245
	v_min_u32_e32 v245, v245, v246
	v_add_u32_e32 v237, v242, v245
	v_sub_u32_e32 v245, v238, v243
	v_add_u32_e32 v246, 0xfffffdc0, v245
	v_min_u32_e32 v245, v245, v246
	v_add_u32_e32 v238, v242, v245
	v_sub_u32_e32 v245, v239, v243
	v_add_u32_e32 v246, 0xfffffdc0, v245
	v_min_u32_e32 v245, v245, v246
	v_add_u32_e32 v239, v242, v245
	v_sub_u32_e32 v245, v240, v243
	v_add_u32_e32 v246, 0xfffffdc0, v245
	v_min_u32_e32 v245, v245, v246
	v_add_u32_e32 v240, v242, v245
	v_sub_u32_e32 v245, v241, v243
	v_add_u32_e32 v246, 0xfffffdc0, v245
	v_min_u32_e32 v245, v245, v246
	v_add_u32_e32 v241, v242, v245
	v_mfma_f32_16x16x32_f16 v[158:161], v[18:21], v[30:33], v[158:161]
	v_add_co_u32_e32 v30, vcc, s2, v152
	s_mov_b32 s2, 0x54000
	s_nop 0
	v_addc_co_u32_e32 v31, vcc, 0, v153, vcc
	v_mfma_f32_16x16x32_f16 v[186:189], v[34:37], v[50:53], v[194:197]
	v_mfma_f32_16x16x32_f16 v[34:37], v[34:37], v[122:125], v[10:13]
	s_nop 2
	v_add_co_u32_e32 v10, vcc, s2, v152
	v_mfma_f32_16x16x32_f16 v[194:197], v[18:21], v[50:53], v[202:205]
	s_nop 0
	v_addc_co_u32_e32 v11, vcc, 0, v153, vcc
	global_load_dwordx4 v[50:53], v[30:31], off sc1
	global_load_dwordx4 v[54:57], v[30:31], off offset:256 sc1
	s_nop 0
	global_load_dwordx4 v[30:33], v[10:11], off sc1
	s_nop 0
	global_load_dwordx4 v[10:13], v[10:11], off offset:256 sc1
	v_mfma_f32_16x16x32_f16 v[182:185], v[18:21], v[122:125], v[182:185]
	v_add_u32_e32 v157, 0x111520dc, v154
	ds_read_b128 v[18:21], v151 offset:448
	v_add_u32_e32 v122, 0xc00, v150
	s_waitcnt vmcnt(24) lgkmcnt(0)
	v_mfma_f32_16x16x32_f16 v[202:205], v[42:45], v[18:21], v[218:221]
	s_waitcnt vmcnt(23)
	v_mfma_f32_16x16x32_f16 v[190:193], v[46:49], v[18:21], v[190:193]
	v_min_u32_e32 v18, v122, v157
	global_load_dwordx4 v[18:21], v18, s[8:9] nt
	s_waitcnt vmcnt(21)
	v_cvt_pk_f16_f32 v17, v16, v17
	v_cvt_pk_f16_f32 v16, v14, v15
	ds_write_b16 v234, v16 offset:0
	ds_write_b16_d16_hi v235, v16 offset:0
	ds_write_b16 v236, v17 offset:0
	ds_write_b16_d16_hi v237, v17 offset:0
	ds_read_b128 v[14:17], v151 offset:1056
	ds_read_b128 v[122:125], v151 offset:1664
	s_waitcnt lgkmcnt(1)
	v_mfma_f32_16x16x32_f16 v[198:201], v[42:45], v[14:17], v[198:201]
	s_waitcnt lgkmcnt(0)
	v_mfma_f32_16x16x32_f16 v[58:61], v[42:45], v[122:125], v[58:61]
	v_mfma_f32_16x16x32_f16 v[218:221], v[46:49], v[122:125], v[130:133]
	ds_read_b128 v[122:125], v151 offset:2272
	s_nop 1
	ds_read_b128 v[130:133], v151 offset:2880
	v_mfma_f32_16x16x32_f16 v[14:17], v[46:49], v[14:17], v[222:225]
	s_waitcnt lgkmcnt(1)
	v_mfma_f32_16x16x32_f16 v[134:137], v[42:45], v[122:125], v[134:137]
	v_mfma_f32_16x16x32_f16 v[138:141], v[46:49], v[122:125], v[138:141]
	s_waitcnt lgkmcnt(0)
	v_mfma_f32_16x16x32_f16 v[206:209], v[42:45], v[130:133], v[206:209]
	v_mfma_f32_16x16x32_f16 v[222:225], v[46:49], v[130:133], v[126:129]
	v_add_u32_e32 v122, 0x17240, v244
	v_min_u32_e32 v122, v122, v157
	global_load_dwordx4 v[122:125], v122, s[8:9] nt
	s_waitcnt vmcnt(21)
	v_cvt_pk_f16_f32 v93, v92, v93
	v_cvt_pk_f16_f32 v92, v90, v91
	ds_write_b16 v238, v92 offset:608
	ds_write_b16_d16_hi v239, v92 offset:608
	ds_write_b16 v240, v93 offset:608
	ds_write_b16_d16_hi v241, v93 offset:608
	ds_read_b128 v[90:93], v151 offset:3488
	ds_read_b128 v[126:129], v151 offset:5312
	s_waitcnt lgkmcnt(1)
	v_mfma_f32_16x16x32_f16 v[146:149], v[42:45], v[90:93], v[146:149]
	v_mfma_f32_16x16x32_f16 v[90:93], v[46:49], v[90:93], v[210:213]
	ds_read_b128 v[130:133], v151 offset:4096
	s_nop 1
	ds_read_b128 v[210:213], v151 offset:4704
	s_waitcnt lgkmcnt(1)
	v_mfma_f32_16x16x32_f16 v[62:65], v[42:45], v[130:133], v[62:65]
	v_mfma_f32_16x16x32_f16 v[142:145], v[46:49], v[130:133], v[142:145]
	s_waitcnt lgkmcnt(0)
	v_mfma_f32_16x16x32_f16 v[166:169], v[42:45], v[210:213], v[166:169]
	v_mfma_f32_16x16x32_f16 v[162:165], v[46:49], v[210:213], v[162:165]
	v_mfma_f32_16x16x32_f16 v[210:213], v[42:45], v[126:129], v[214:217]
	v_mfma_f32_16x16x32_f16 v[170:173], v[46:49], v[126:129], v[170:173]
	v_add_u32_e32 v126, 0x2d880, v150
	v_min_u32_e32 v126, v126, v157
	global_load_dwordx4 v[126:129], v126, s[8:9] nt
	s_waitcnt vmcnt(21)
	v_cvt_pk_f16_f32 v97, v96, v97
	v_cvt_pk_f16_f32 v96, v94, v95
	ds_write_b16 v234, v96 offset:1216
	ds_write_b16_d16_hi v235, v96 offset:1216
	ds_write_b16 v236, v97 offset:1216
	ds_write_b16_d16_hi v237, v97 offset:1216
	ds_read_b128 v[94:97], v151 offset:5920
	ds_read_b128 v[130:133], v151 offset:6528
	s_waitcnt lgkmcnt(1)
	v_mfma_f32_16x16x32_f16 v[174:177], v[42:45], v[94:97], v[174:177]
	v_mfma_f32_16x16x32_f16 v[94:97], v[46:49], v[94:97], v[178:181]
	s_waitcnt lgkmcnt(0)
	v_mfma_f32_16x16x32_f16 v[86:89], v[42:45], v[130:133], v[86:89]
	v_mfma_f32_16x16x32_f16 v[158:161], v[46:49], v[130:133], v[158:161]
	ds_read_b128 v[130:133], v151 offset:7136
	ds_read_b128 v[178:181], v151 offset:7744
	s_waitcnt lgkmcnt(1)
	v_mfma_f32_16x16x32_f16 v[186:189], v[42:45], v[130:133], v[186:189]
	v_mfma_f32_16x16x32_f16 v[194:197], v[46:49], v[130:133], v[194:197]
	s_waitcnt lgkmcnt(0)
	v_mfma_f32_16x16x32_f16 v[34:37], v[42:45], v[178:181], v[34:37]
	v_mfma_f32_16x16x32_f16 v[42:45], v[46:49], v[178:181], v[182:185]
	v_add_u32_e32 v46, 0x43ec0, v244
	v_min_u32_e32 v46, v46, v157
	global_load_dwordx4 v[130:133], v46, s[8:9] nt
	s_waitcnt vmcnt(21)
	v_cvt_pk_f16_f32 v47, v100, v101
	v_cvt_pk_f16_f32 v46, v98, v99
	ds_write_b16 v238, v46 offset:1824
	ds_write_b16_d16_hi v239, v46 offset:1824
	ds_write_b16 v240, v47 offset:1824
	ds_write_b16_d16_hi v241, v47 offset:1824
	ds_read_b128 v[46:49], v151 offset:512
	ds_read_b128 v[98:101], v151 offset:1120
	s_waitcnt lgkmcnt(1)
	v_mfma_f32_16x16x32_f16 v[178:181], v[26:29], v[46:49], v[202:205]
	v_mfma_f32_16x16x32_f16 v[46:49], v[6:9], v[46:49], v[190:193]
	s_waitcnt lgkmcnt(0)
	v_mfma_f32_16x16x32_f16 v[182:185], v[26:29], v[98:101], v[198:201]
	v_mfma_f32_16x16x32_f16 v[98:101], v[6:9], v[98:101], v[14:17]
	s_nop 2
	ds_read_b128 v[14:17], v151 offset:1728
	ds_read_b128 v[190:193], v151 offset:2336
	s_waitcnt lgkmcnt(1)
	v_mfma_f32_16x16x32_f16 v[198:201], v[26:29], v[14:17], v[58:61]
	v_mfma_f32_16x16x32_f16 v[202:205], v[6:9], v[14:17], v[218:221]
	s_waitcnt lgkmcnt(0)
	v_mfma_f32_16x16x32_f16 v[214:217], v[26:29], v[190:193], v[134:137]
	v_mfma_f32_16x16x32_f16 v[190:193], v[6:9], v[190:193], v[138:141]
	v_add_u32_e32 v14, 0x5a500, v150
	v_min_u32_e32 v14, v14, v157
	global_load_dwordx4 v[134:137], v14, s[8:9] nt
	s_waitcnt vmcnt(21)
	v_cvt_pk_f16_f32 v15, v104, v105
	v_cvt_pk_f16_f32 v14, v102, v103
	ds_write_b16 v234, v14 offset:2432
	ds_write_b16_d16_hi v235, v14 offset:2432
	ds_write_b16 v236, v15 offset:2432
	ds_write_b16_d16_hi v237, v15 offset:2432
	ds_read_b128 v[14:17], v151 offset:2944
	ds_read_b128 v[58:61], v151 offset:3552
	s_waitcnt lgkmcnt(1)
	v_mfma_f32_16x16x32_f16 v[102:105], v[26:29], v[14:17], v[206:209]
	v_mfma_f32_16x16x32_f16 v[206:209], v[6:9], v[14:17], v[222:225]
	s_waitcnt lgkmcnt(0)
	v_mfma_f32_16x16x32_f16 v[218:221], v[26:29], v[58:61], v[146:149]
	v_mfma_f32_16x16x32_f16 v[90:93], v[6:9], v[58:61], v[90:93]
	ds_read_b128 v[14:17], v151 offset:4160
	ds_read_b128 v[58:61], v151 offset:4768
	s_waitcnt lgkmcnt(1)
	v_mfma_f32_16x16x32_f16 v[222:225], v[26:29], v[14:17], v[62:65]
	v_mfma_f32_16x16x32_f16 v[226:229], v[6:9], v[14:17], v[142:145]
	s_waitcnt lgkmcnt(0)
	v_mfma_f32_16x16x32_f16 v[166:169], v[26:29], v[58:61], v[166:169]
	v_mfma_f32_16x16x32_f16 v[162:165], v[6:9], v[58:61], v[162:165]
	v_add_u32_e32 v14, 0x70b40, v244
	v_min_u32_e32 v14, v14, v157
	global_load_dwordx4 v[138:141], v14, s[8:9] nt
	s_waitcnt vmcnt(21)
	v_cvt_pk_f16_f32 v15, v108, v109
	v_cvt_pk_f16_f32 v14, v106, v107
	ds_write_b16 v238, v14 offset:3040
	ds_write_b16_d16_hi v239, v14 offset:3040
	ds_write_b16 v240, v15 offset:3040
	ds_write_b16_d16_hi v241, v15 offset:3040
	ds_read_b128 v[14:17], v151 offset:5376
	ds_read_b128 v[58:61], v151 offset:5984
	s_waitcnt lgkmcnt(1)
	v_mfma_f32_16x16x32_f16 v[106:109], v[26:29], v[14:17], v[210:213]
	v_mfma_f32_16x16x32_f16 v[170:173], v[6:9], v[14:17], v[170:173]
	s_waitcnt lgkmcnt(0)
	v_mfma_f32_16x16x32_f16 v[174:177], v[26:29], v[58:61], v[174:177]
	v_mfma_f32_16x16x32_f16 v[94:97], v[6:9], v[58:61], v[94:97]
	ds_read_b128 v[14:17], v151 offset:6592
	ds_read_b128 v[58:61], v151 offset:7200
	s_waitcnt lgkmcnt(1)
	v_mfma_f32_16x16x32_f16 v[86:89], v[26:29], v[14:17], v[86:89]
	v_mfma_f32_16x16x32_f16 v[158:161], v[6:9], v[14:17], v[158:161]
	s_waitcnt lgkmcnt(0)
	v_mfma_f32_16x16x32_f16 v[186:189], v[26:29], v[58:61], v[186:189]
	v_mfma_f32_16x16x32_f16 v[194:197], v[6:9], v[58:61], v[194:197]
	v_add_u32_e32 v14, 0x87180, v150
	v_min_u32_e32 v14, v14, v157
	global_load_dwordx4 v[142:145], v14, s[8:9] nt
	s_waitcnt vmcnt(21)
	v_cvt_pk_f16_f32 v15, v112, v113
	v_cvt_pk_f16_f32 v14, v110, v111
	ds_write_b16 v234, v14 offset:3648
	ds_write_b16_d16_hi v235, v14 offset:3648
	ds_write_b16 v236, v15 offset:3648
	ds_write_b16_d16_hi v237, v15 offset:3648
	ds_read_b128 v[110:113], v151 offset:7808
	s_mov_b32 s2, 0x58000
	v_add_co_u32_e32 v14, vcc, s2, v152
	s_mov_b32 s2, 0x5c000
	s_nop 0
	v_addc_co_u32_e32 v15, vcc, 0, v153, vcc
	global_load_dwordx4 v[58:61], v[14:15], off sc1
	global_load_dwordx4 v[62:65], v[14:15], off offset:256 sc1
	v_add_co_u32_e32 v14, vcc, s2, v152
	s_waitcnt lgkmcnt(0)
	v_mfma_f32_16x16x32_f16 v[26:29], v[26:29], v[110:113], v[34:37]
	v_addc_co_u32_e32 v15, vcc, 0, v153, vcc
	s_nop 1
	global_load_dwordx4 v[34:37], v[14:15], off sc1
	s_nop 0
	global_load_dwordx4 v[14:17], v[14:15], off offset:256 sc1
	v_mfma_f32_16x16x32_f16 v[42:45], v[6:9], v[110:113], v[42:45]
	ds_read_b128 v[6:9], v151 offset:0
	ds_read_b128 v[110:113], v151 offset:608
	s_waitcnt vmcnt(24) lgkmcnt(1)
	v_mfma_f32_16x16x32_f16 v[178:181], v[70:73], v[6:9], v[178:181]
	s_waitcnt vmcnt(23)
	v_mfma_f32_16x16x32_f16 v[46:49], v[74:77], v[6:9], v[46:49]
	ds_read_b128 v[6:9], v151 offset:1216
	s_waitcnt lgkmcnt(1)
	v_mfma_f32_16x16x32_f16 v[182:185], v[70:73], v[110:113], v[182:185]
	v_mfma_f32_16x16x32_f16 v[98:101], v[74:77], v[110:113], v[98:101]
	s_waitcnt lgkmcnt(0)
	v_mfma_f32_16x16x32_f16 v[198:201], v[70:73], v[6:9], v[198:201]
	v_mfma_f32_16x16x32_f16 v[202:205], v[74:77], v[6:9], v[202:205]
	v_add_u32_e32 v6, 0x9d7c0, v244
	v_min_u32_e32 v6, v6, v157
	global_load_dwordx4 v[146:149], v6, s[8:9] nt
	s_waitcnt vmcnt(21)
	v_cvt_pk_f16_f32 v5, v4, v5
	v_cvt_pk_f16_f32 v4, v2, v3
	ds_write_b16 v238, v4 offset:4256
	ds_write_b16_d16_hi v239, v4 offset:4256
	ds_write_b16 v240, v5 offset:4256
	ds_write_b16_d16_hi v241, v5 offset:4256
	ds_read_b128 v[2:5], v151 offset:1824
	ds_read_b128 v[6:9], v151 offset:2432
	s_waitcnt lgkmcnt(1)
	v_mfma_f32_16x16x32_f16 v[210:213], v[70:73], v[2:5], v[214:217]
	v_mfma_f32_16x16x32_f16 v[2:5], v[74:77], v[2:5], v[190:193]
	s_waitcnt lgkmcnt(0)
	v_mfma_f32_16x16x32_f16 v[102:105], v[70:73], v[6:9], v[102:105]
	v_mfma_f32_16x16x32_f16 v[190:193], v[74:77], v[6:9], v[206:209]
	ds_read_b128 v[6:9], v151 offset:3040
	ds_read_b128 v[110:113], v151 offset:3648
	s_waitcnt lgkmcnt(1)
	v_mfma_f32_16x16x32_f16 v[206:209], v[70:73], v[6:9], v[218:221]
	v_mfma_f32_16x16x32_f16 v[90:93], v[74:77], v[6:9], v[90:93]
	s_waitcnt lgkmcnt(0)
	v_mfma_f32_16x16x32_f16 v[214:217], v[70:73], v[110:113], v[222:225]
	v_mfma_f32_16x16x32_f16 v[218:221], v[74:77], v[110:113], v[226:229]
	v_add_u32_e32 v6, 0xb3e00, v150
	v_min_u32_e32 v6, v6, v157
	global_load_dwordx4 v[110:113], v6, s[8:9] nt
	s_waitcnt vmcnt(21)
	v_cvt_pk_f16_f32 v7, v116, v117
	v_cvt_pk_f16_f32 v6, v114, v115
	ds_write_b16 v234, v6 offset:4864
	ds_write_b16_d16_hi v235, v6 offset:4864
	ds_write_b16 v236, v7 offset:4864
	ds_write_b16_d16_hi v237, v7 offset:4864
	ds_read_b128 v[6:9], v151 offset:4256
	ds_read_b128 v[114:117], v151 offset:6080
	s_waitcnt lgkmcnt(1)
	v_mfma_f32_16x16x32_f16 v[166:169], v[70:73], v[6:9], v[166:169]
	v_mfma_f32_16x16x32_f16 v[162:165], v[74:77], v[6:9], v[162:165]
	ds_read_b128 v[6:9], v151 offset:4864
	ds_read_b128 v[222:225], v151 offset:5472
	s_waitcnt lgkmcnt(2)
	v_mfma_f32_16x16x32_f16 v[86:89], v[70:73], v[114:117], v[86:89]
	v_mfma_f32_16x16x32_f16 v[114:117], v[74:77], v[114:117], v[158:161]
	s_waitcnt lgkmcnt(1)
	v_mfma_f32_16x16x32_f16 v[106:109], v[70:73], v[6:9], v[106:109]
	v_mfma_f32_16x16x32_f16 v[170:173], v[74:77], v[6:9], v[170:173]
	s_waitcnt lgkmcnt(0)
	v_mfma_f32_16x16x32_f16 v[174:177], v[70:73], v[222:225], v[174:177]
	v_mfma_f32_16x16x32_f16 v[94:97], v[74:77], v[222:225], v[94:97]
	v_add_u32_e32 v6, 0xca440, v244
	v_min_u32_e32 v6, v6, v157
	global_load_dwordx4 v[6:9], v6, s[8:9] nt
	s_waitcnt vmcnt(21)
	v_cvt_pk_f16_f32 v81, v80, v81
	v_cvt_pk_f16_f32 v80, v78, v79
	ds_write_b16 v238, v80 offset:5472
	ds_write_b16_d16_hi v239, v80 offset:5472
	ds_write_b16 v240, v81 offset:5472
	ds_write_b16_d16_hi v241, v81 offset:5472
	ds_read_b128 v[78:81], v151 offset:6688
	ds_read_b128 v[158:161], v151 offset:7296
	s_waitcnt lgkmcnt(1)
	v_mfma_f32_16x16x32_f16 v[186:189], v[70:73], v[78:81], v[186:189]
	s_waitcnt lgkmcnt(0)
	v_mfma_f32_16x16x32_f16 v[26:29], v[70:73], v[158:161], v[26:29]
	v_mfma_f32_16x16x32_f16 v[158:161], v[74:77], v[158:161], v[42:45]
	s_nop 2
	ds_read_b128 v[42:45], v151 offset:64
	ds_read_b128 v[70:73], v151 offset:672
	v_mfma_f32_16x16x32_f16 v[194:197], v[74:77], v[78:81], v[194:197]
	s_waitcnt lgkmcnt(1)
	v_mfma_f32_16x16x32_f16 v[178:181], v[38:41], v[42:45], v[178:181]
	v_mfma_f32_16x16x32_f16 v[222:225], v[22:25], v[42:45], v[46:49]
	s_waitcnt lgkmcnt(0)
	v_mfma_f32_16x16x32_f16 v[182:185], v[38:41], v[70:73], v[182:185]
	v_mfma_f32_16x16x32_f16 v[98:101], v[22:25], v[70:73], v[98:101]
	v_add_u32_e32 v42, 0xe0a80, v150
	v_min_u32_e32 v42, v42, v157
	global_load_dwordx4 v[70:73], v42, s[8:9] nt
	s_waitcnt vmcnt(21)
	v_cvt_pk_f16_f32 v43, v68, v69
	v_cvt_pk_f16_f32 v42, v66, v67
	ds_write_b16 v234, v42 offset:6080
	ds_write_b16_d16_hi v235, v42 offset:6080
	ds_write_b16 v236, v43 offset:6080
	ds_write_b16_d16_hi v237, v43 offset:6080
	ds_read_b128 v[42:45], v151 offset:1280
	ds_read_b128 v[46:49], v151 offset:1888
	s_waitcnt lgkmcnt(1)
	v_mfma_f32_16x16x32_f16 v[66:69], v[38:41], v[42:45], v[198:201]
	v_mfma_f32_16x16x32_f16 v[198:201], v[22:25], v[42:45], v[202:205]
	s_waitcnt lgkmcnt(0)
	v_mfma_f32_16x16x32_f16 v[202:205], v[38:41], v[46:49], v[210:213]
	v_mfma_f32_16x16x32_f16 v[210:213], v[22:25], v[46:49], v[2:5]
	s_nop 2
	ds_read_b128 v[2:5], v151 offset:2496
	ds_read_b128 v[42:45], v151 offset:3104
	s_waitcnt lgkmcnt(1)
	v_mfma_f32_16x16x32_f16 v[102:105], v[38:41], v[2:5], v[102:105]
	v_mfma_f32_16x16x32_f16 v[190:193], v[22:25], v[2:5], v[190:193]
	s_waitcnt lgkmcnt(0)
	v_mfma_f32_16x16x32_f16 v[206:209], v[38:41], v[42:45], v[206:209]
	v_mfma_f32_16x16x32_f16 v[90:93], v[22:25], v[42:45], v[90:93]
	v_add_u32_e32 v2, 0xf70c0, v244
	v_min_u32_e32 v2, v2, v157
	global_load_dwordx4 v[74:77], v2, s[8:9] nt
	s_waitcnt vmcnt(21)
	v_cvt_pk_f16_f32 v3, v84, v85
	v_cvt_pk_f16_f32 v2, v82, v83
	ds_write_b16 v238, v2 offset:6688
	ds_write_b16_d16_hi v239, v2 offset:6688
	ds_write_b16 v240, v3 offset:6688
	ds_write_b16_d16_hi v241, v3 offset:6688
	ds_read_b128 v[2:5], v151 offset:3712
	ds_read_b128 v[42:45], v151 offset:4320
	s_waitcnt lgkmcnt(1)
	v_mfma_f32_16x16x32_f16 v[214:217], v[38:41], v[2:5], v[214:217]
	v_mfma_f32_16x16x32_f16 v[218:221], v[22:25], v[2:5], v[218:221]
	s_waitcnt lgkmcnt(0)
	v_mfma_f32_16x16x32_f16 v[166:169], v[38:41], v[42:45], v[166:169]
	v_mfma_f32_16x16x32_f16 v[162:165], v[22:25], v[42:45], v[162:165]
	ds_read_b128 v[2:5], v151 offset:4928
	ds_read_b128 v[42:45], v151 offset:5536
	s_waitcnt lgkmcnt(1)
	v_mfma_f32_16x16x32_f16 v[106:109], v[38:41], v[2:5], v[106:109]
	v_mfma_f32_16x16x32_f16 v[170:173], v[22:25], v[2:5], v[170:173]
	s_waitcnt lgkmcnt(0)
	v_mfma_f32_16x16x32_f16 v[174:177], v[38:41], v[42:45], v[174:177]
	v_mfma_f32_16x16x32_f16 v[94:97], v[22:25], v[42:45], v[94:97]
	v_add_u32_e32 v2, 0x10d700, v150
	v_min_u32_e32 v2, v2, v157
	v_cndmask_b32_e64 v2, 0, v2, s[0:1]
	global_load_dwordx4 v[78:81], v2, s[8:9] nt
	s_waitcnt vmcnt(21)
	v_cvt_pk_f16_f32 v3, v120, v121
	v_cvt_pk_f16_f32 v2, v118, v119
	ds_write_b16 v234, v2 offset:7296
	ds_write_b16_d16_hi v235, v2 offset:7296
	ds_write_b16 v236, v3 offset:7296
	ds_write_b16_d16_hi v237, v3 offset:7296
	ds_read_b128 v[2:5], v151 offset:6144
	ds_read_b128 v[42:45], v151 offset:6752
	ds_read_b128 v[82:85], v151 offset:7360
	s_mov_b32 s2, 0x60000
	s_waitcnt lgkmcnt(0)
	v_mfma_f32_16x16x32_f16 v[118:121], v[38:41], v[2:5], v[86:89]
	s_barrier
	v_sub_u32_e32 v245, v234, v243
	v_add_u32_e32 v246, 0xfffffdc0, v245
	v_min_u32_e32 v245, v245, v246
	v_add_u32_e32 v234, v242, v245
	v_sub_u32_e32 v245, v235, v243
	v_add_u32_e32 v246, 0xfffffdc0, v245
	v_min_u32_e32 v245, v245, v246
	v_add_u32_e32 v235, v242, v245
	v_sub_u32_e32 v245, v236, v243
	v_add_u32_e32 v246, 0xfffffdc0, v245
	v_min_u32_e32 v245, v245, v246
	v_add_u32_e32 v236, v242, v245
	v_sub_u32_e32 v245, v237, v243
	v_add_u32_e32 v246, 0xfffffdc0, v245
	v_min_u32_e32 v245, v245, v246
	v_add_u32_e32 v237, v242, v245
	v_sub_u32_e32 v245, v238, v243
	v_add_u32_e32 v246, 0xfffffdc0, v245
	v_min_u32_e32 v245, v245, v246
	v_add_u32_e32 v238, v242, v245
	v_sub_u32_e32 v245, v239, v243
	v_add_u32_e32 v246, 0xfffffdc0, v245
	v_min_u32_e32 v245, v245, v246
	v_add_u32_e32 v239, v242, v245
	v_sub_u32_e32 v245, v240, v243
	v_add_u32_e32 v246, 0xfffffdc0, v245
	v_min_u32_e32 v245, v245, v246
	v_add_u32_e32 v240, v242, v245
	v_sub_u32_e32 v245, v241, v243
	v_add_u32_e32 v246, 0xfffffdc0, v245
	v_min_u32_e32 v245, v245, v246
	v_add_u32_e32 v241, v242, v245
	v_mfma_f32_16x16x32_f16 v[114:117], v[22:25], v[2:5], v[114:117]
	v_add_co_u32_e32 v2, vcc, s2, v152
	s_mov_b32 s2, 0x64000
	s_nop 0
	v_addc_co_u32_e32 v3, vcc, 0, v153, vcc
	v_mfma_f32_16x16x32_f16 v[186:189], v[38:41], v[42:45], v[186:189]
	v_mfma_f32_16x16x32_f16 v[194:197], v[22:25], v[42:45], v[194:197]
	global_load_dwordx4 v[42:45], v[2:3], off sc1
	global_load_dwordx4 v[46:49], v[2:3], off offset:256 sc1
	v_add_co_u32_e32 v2, vcc, s2, v152
	v_mfma_f32_16x16x32_f16 v[38:41], v[38:41], v[82:85], v[26:29]
	s_nop 0
	v_addc_co_u32_e32 v3, vcc, 0, v153, vcc
	s_nop 0
	global_load_dwordx4 v[26:29], v[2:3], off sc1
	s_nop 0
	global_load_dwordx4 v[2:5], v[2:3], off offset:256 sc1
	v_mfma_f32_16x16x32_f16 v[22:25], v[22:25], v[82:85], v[158:161]
	v_add_u32_e32 v157, 0x111522dc, v154
	ds_read_b128 v[82:85], v151 offset:128
	v_add_u32_e32 v86, 0xe00, v150
	s_waitcnt vmcnt(24) lgkmcnt(0)
	v_mfma_f32_16x16x32_f16 v[158:161], v[50:53], v[82:85], v[178:181]
	s_waitcnt vmcnt(23)
	v_mfma_f32_16x16x32_f16 v[178:181], v[54:57], v[82:85], v[222:225]
	v_min_u32_e32 v82, v86, v157
	global_load_dwordx4 v[82:85], v82, s[8:9] nt
	s_waitcnt vmcnt(21)
	v_cvt_pk_f16_f32 v21, v20, v21
	v_cvt_pk_f16_f32 v20, v18, v19
	ds_write_b16 v234, v20 offset:0
	ds_write_b16_d16_hi v235, v20 offset:0
	ds_write_b16 v236, v21 offset:0
	ds_write_b16_d16_hi v237, v21 offset:0
	ds_read_b128 v[18:21], v151 offset:736
	ds_read_b128 v[86:89], v151 offset:1344
	s_waitcnt lgkmcnt(1)
	v_mfma_f32_16x16x32_f16 v[182:185], v[50:53], v[18:21], v[182:185]
	v_mfma_f32_16x16x32_f16 v[18:21], v[54:57], v[18:21], v[98:101]
	s_waitcnt lgkmcnt(0)
	v_mfma_f32_16x16x32_f16 v[66:69], v[50:53], v[86:89], v[66:69]
	v_mfma_f32_16x16x32_f16 v[98:101], v[54:57], v[86:89], v[198:201]
	ds_read_b128 v[86:89], v151 offset:1952
	s_nop 1
	ds_read_b128 v[198:201], v151 offset:2560
	s_waitcnt lgkmcnt(1)
	v_mfma_f32_16x16x32_f16 v[202:205], v[50:53], v[86:89], v[202:205]
	v_mfma_f32_16x16x32_f16 v[210:213], v[54:57], v[86:89], v[210:213]
	s_waitcnt lgkmcnt(0)
	v_mfma_f32_16x16x32_f16 v[102:105], v[50:53], v[198:201], v[102:105]
	v_mfma_f32_16x16x32_f16 v[190:193], v[54:57], v[198:201], v[190:193]
	v_add_u32_e32 v86, 0x17440, v244
	v_min_u32_e32 v86, v86, v157
	global_load_dwordx4 v[86:89], v86, s[8:9] nt
	s_waitcnt vmcnt(21)
	v_cvt_pk_f16_f32 v125, v124, v125
	v_cvt_pk_f16_f32 v124, v122, v123
	ds_write_b16 v238, v124 offset:608
	ds_write_b16_d16_hi v239, v124 offset:608
	ds_write_b16 v240, v125 offset:608
	ds_write_b16_d16_hi v241, v125 offset:608
	ds_read_b128 v[122:125], v151 offset:3168
	ds_read_b128 v[198:201], v151 offset:4992
	s_waitcnt lgkmcnt(1)
	v_mfma_f32_16x16x32_f16 v[206:209], v[50:53], v[122:125], v[206:209]
	v_mfma_f32_16x16x32_f16 v[122:125], v[54:57], v[122:125], v[90:93]
	s_nop 2
	ds_read_b128 v[90:93], v151 offset:3776
	ds_read_b128 v[222:225], v151 offset:4384
	s_waitcnt lgkmcnt(1)
	v_mfma_f32_16x16x32_f16 v[214:217], v[50:53], v[90:93], v[214:217]
	v_mfma_f32_16x16x32_f16 v[218:221], v[54:57], v[90:93], v[218:221]
	s_waitcnt lgkmcnt(0)
	v_mfma_f32_16x16x32_f16 v[166:169], v[50:53], v[222:225], v[166:169]
	v_mfma_f32_16x16x32_f16 v[162:165], v[54:57], v[222:225], v[162:165]
	v_mfma_f32_16x16x32_f16 v[106:109], v[50:53], v[198:201], v[106:109]
	v_mfma_f32_16x16x32_f16 v[170:173], v[54:57], v[198:201], v[170:173]
	v_add_u32_e32 v90, 0x2da80, v150
	v_min_u32_e32 v90, v90, v157
	global_load_dwordx4 v[90:93], v90, s[8:9] nt
	s_waitcnt vmcnt(21)
	v_cvt_pk_f16_f32 v129, v128, v129
	v_cvt_pk_f16_f32 v128, v126, v127
	ds_write_b16 v234, v128 offset:1216
	ds_write_b16_d16_hi v235, v128 offset:1216
	ds_write_b16 v236, v129 offset:1216
	ds_write_b16_d16_hi v237, v129 offset:1216
	ds_read_b128 v[126:129], v151 offset:5600
	ds_read_b128 v[198:201], v151 offset:6208
	s_waitcnt lgkmcnt(1)
	v_mfma_f32_16x16x32_f16 v[174:177], v[50:53], v[126:129], v[174:177]
	v_mfma_f32_16x16x32_f16 v[126:129], v[54:57], v[126:129], v[94:97]
	s_waitcnt lgkmcnt(0)
	v_mfma_f32_16x16x32_f16 v[118:121], v[50:53], v[198:201], v[118:121]
	v_mfma_f32_16x16x32_f16 v[114:117], v[54:57], v[198:201], v[114:117]
	ds_read_b128 v[94:97], v151 offset:6816
	ds_read_b128 v[198:201], v151 offset:7424
	s_waitcnt lgkmcnt(1)
	v_mfma_f32_16x16x32_f16 v[186:189], v[50:53], v[94:97], v[186:189]
	v_mfma_f32_16x16x32_f16 v[194:197], v[54:57], v[94:97], v[194:197]
	s_waitcnt lgkmcnt(0)
	v_mfma_f32_16x16x32_f16 v[38:41], v[50:53], v[198:201], v[38:41]
	v_mfma_f32_16x16x32_f16 v[22:25], v[54:57], v[198:201], v[22:25]
	v_add_u32_e32 v50, 0x440c0, v244
	v_min_u32_e32 v50, v50, v157
	global_load_dwordx4 v[94:97], v50, s[8:9] nt
	s_waitcnt vmcnt(21)
	v_cvt_pk_f16_f32 v51, v132, v133
	v_cvt_pk_f16_f32 v50, v130, v131
	ds_write_b16 v238, v50 offset:1824
	ds_write_b16_d16_hi v239, v50 offset:1824
	ds_write_b16 v240, v51 offset:1824
	ds_write_b16_d16_hi v241, v51 offset:1824
	ds_read_b128 v[50:53], v151 offset:192
	ds_read_b128 v[54:57], v151 offset:800
	s_waitcnt lgkmcnt(1)
	v_mfma_f32_16x16x32_f16 v[130:133], v[30:33], v[50:53], v[158:161]
	v_mfma_f32_16x16x32_f16 v[50:53], v[10:13], v[50:53], v[178:181]
	s_waitcnt lgkmcnt(0)
	v_mfma_f32_16x16x32_f16 v[158:161], v[30:33], v[54:57], v[182:185]
	v_mfma_f32_16x16x32_f16 v[178:181], v[10:13], v[54:57], v[18:21]
	s_nop 2
	ds_read_b128 v[18:21], v151 offset:1408
	ds_read_b128 v[54:57], v151 offset:2016
	s_waitcnt lgkmcnt(1)
	v_mfma_f32_16x16x32_f16 v[182:185], v[30:33], v[18:21], v[66:69]
	v_mfma_f32_16x16x32_f16 v[198:201], v[10:13], v[18:21], v[98:101]
	s_waitcnt lgkmcnt(0)
	v_mfma_f32_16x16x32_f16 v[202:205], v[30:33], v[54:57], v[202:205]
	v_mfma_f32_16x16x32_f16 v[210:213], v[10:13], v[54:57], v[210:213]
	v_add_u32_e32 v18, 0x5a700, v150
	v_min_u32_e32 v18, v18, v157
	global_load_dwordx4 v[98:101], v18, s[8:9] nt
	s_waitcnt vmcnt(21)
	v_cvt_pk_f16_f32 v19, v136, v137
	v_cvt_pk_f16_f32 v18, v134, v135
	ds_write_b16 v234, v18 offset:2432
	ds_write_b16_d16_hi v235, v18 offset:2432
	ds_write_b16 v236, v19 offset:2432
	ds_write_b16_d16_hi v237, v19 offset:2432
	ds_read_b128 v[18:21], v151 offset:2624
	ds_read_b128 v[54:57], v151 offset:3232
	s_waitcnt lgkmcnt(1)
	v_mfma_f32_16x16x32_f16 v[134:137], v[30:33], v[18:21], v[102:105]
	v_mfma_f32_16x16x32_f16 v[190:193], v[10:13], v[18:21], v[190:193]
	s_waitcnt lgkmcnt(0)
	v_mfma_f32_16x16x32_f16 v[206:209], v[30:33], v[54:57], v[206:209]
	v_mfma_f32_16x16x32_f16 v[122:125], v[10:13], v[54:57], v[122:125]
	ds_read_b128 v[18:21], v151 offset:3840
	ds_read_b128 v[54:57], v151 offset:4448
	s_waitcnt lgkmcnt(1)
	v_mfma_f32_16x16x32_f16 v[214:217], v[30:33], v[18:21], v[214:217]
	v_mfma_f32_16x16x32_f16 v[218:221], v[10:13], v[18:21], v[218:221]
	s_waitcnt lgkmcnt(0)
	v_mfma_f32_16x16x32_f16 v[166:169], v[30:33], v[54:57], v[166:169]
	v_mfma_f32_16x16x32_f16 v[162:165], v[10:13], v[54:57], v[162:165]
	v_add_u32_e32 v18, 0x70d40, v244
	v_min_u32_e32 v18, v18, v157
	global_load_dwordx4 v[102:105], v18, s[8:9] nt
	s_waitcnt vmcnt(21)
	v_cvt_pk_f16_f32 v19, v140, v141
	v_cvt_pk_f16_f32 v18, v138, v139
	ds_write_b16 v238, v18 offset:3040
	ds_write_b16_d16_hi v239, v18 offset:3040
	ds_write_b16 v240, v19 offset:3040
	ds_write_b16_d16_hi v241, v19 offset:3040
	ds_read_b128 v[18:21], v151 offset:5056
	ds_read_b128 v[54:57], v151 offset:5664
	s_waitcnt lgkmcnt(1)
	v_mfma_f32_16x16x32_f16 v[138:141], v[30:33], v[18:21], v[106:109]
	v_mfma_f32_16x16x32_f16 v[170:173], v[10:13], v[18:21], v[170:173]
	s_waitcnt lgkmcnt(0)
	v_mfma_f32_16x16x32_f16 v[174:177], v[30:33], v[54:57], v[174:177]
	v_mfma_f32_16x16x32_f16 v[126:129], v[10:13], v[54:57], v[126:129]
	ds_read_b128 v[18:21], v151 offset:6272
	ds_read_b128 v[54:57], v151 offset:6880
	s_waitcnt lgkmcnt(1)
	v_mfma_f32_16x16x32_f16 v[118:121], v[30:33], v[18:21], v[118:121]
	v_mfma_f32_16x16x32_f16 v[222:225], v[10:13], v[18:21], v[114:117]
	s_waitcnt lgkmcnt(0)
	v_mfma_f32_16x16x32_f16 v[186:189], v[30:33], v[54:57], v[186:189]
	v_mfma_f32_16x16x32_f16 v[194:197], v[10:13], v[54:57], v[194:197]
	v_add_u32_e32 v18, 0x87380, v150
	v_min_u32_e32 v18, v18, v157
	global_load_dwordx4 v[106:109], v18, s[8:9] nt
	s_waitcnt vmcnt(21)
	v_cvt_pk_f16_f32 v19, v144, v145
	v_cvt_pk_f16_f32 v18, v142, v143
	ds_write_b16 v234, v18 offset:3648
	ds_write_b16_d16_hi v235, v18 offset:3648
	ds_write_b16 v236, v19 offset:3648
	ds_write_b16_d16_hi v237, v19 offset:3648
	ds_read_b128 v[114:117], v151 offset:7488
	s_mov_b32 s2, 0x68000
	v_add_co_u32_e32 v18, vcc, s2, v152
	s_mov_b32 s2, 0x6c000
	s_nop 0
	v_addc_co_u32_e32 v19, vcc, 0, v153, vcc
	global_load_dwordx4 v[54:57], v[18:19], off sc1
	global_load_dwordx4 v[66:69], v[18:19], off offset:256 sc1
	v_add_co_u32_e32 v18, vcc, s2, v152
	s_waitcnt lgkmcnt(0)
	v_mfma_f32_16x16x32_f16 v[38:41], v[30:33], v[114:117], v[38:41]
	v_addc_co_u32_e32 v19, vcc, 0, v153, vcc
	global_load_dwordx4 v[30:33], v[18:19], off sc1
	s_nop 0
	global_load_dwordx4 v[18:21], v[18:19], off offset:256 sc1
	v_mfma_f32_16x16x32_f16 v[22:25], v[10:13], v[114:117], v[22:25]
	ds_read_b128 v[10:13], v151 offset:256
	ds_read_b128 v[114:117], v151 offset:864
	s_waitcnt vmcnt(24) lgkmcnt(1)
	v_mfma_f32_16x16x32_f16 v[130:133], v[58:61], v[10:13], v[130:133]
	s_waitcnt vmcnt(23)
	v_mfma_f32_16x16x32_f16 v[50:53], v[62:65], v[10:13], v[50:53]
	ds_read_b128 v[10:13], v151 offset:1472
	s_waitcnt lgkmcnt(1)
	v_mfma_f32_16x16x32_f16 v[142:145], v[58:61], v[114:117], v[158:161]
	v_mfma_f32_16x16x32_f16 v[158:161], v[62:65], v[114:117], v[178:181]
	s_waitcnt lgkmcnt(0)
	v_mfma_f32_16x16x32_f16 v[178:181], v[58:61], v[10:13], v[182:185]
	v_mfma_f32_16x16x32_f16 v[182:185], v[62:65], v[10:13], v[198:201]
	v_add_u32_e32 v10, 0x9d9c0, v244
	v_min_u32_e32 v10, v10, v157
	global_load_dwordx4 v[10:13], v10, s[8:9] nt
	s_waitcnt vmcnt(21)
	v_cvt_pk_f16_f32 v115, v148, v149
	v_cvt_pk_f16_f32 v114, v146, v147
	ds_write_b16 v238, v114 offset:4256
	ds_write_b16_d16_hi v239, v114 offset:4256
	ds_write_b16 v240, v115 offset:4256
	ds_write_b16_d16_hi v241, v115 offset:4256
	ds_read_b128 v[114:117], v151 offset:2080
	ds_read_b128 v[146:149], v151 offset:2688
	s_waitcnt lgkmcnt(1)
	v_mfma_f32_16x16x32_f16 v[198:201], v[58:61], v[114:117], v[202:205]
	v_mfma_f32_16x16x32_f16 v[202:205], v[62:65], v[114:117], v[210:213]
	s_waitcnt lgkmcnt(0)
	v_mfma_f32_16x16x32_f16 v[134:137], v[58:61], v[146:149], v[134:137]
	v_mfma_f32_16x16x32_f16 v[146:149], v[62:65], v[146:149], v[190:193]
	ds_read_b128 v[114:117], v151 offset:3296
	s_nop 1
	ds_read_b128 v[190:193], v151 offset:3904
	s_waitcnt lgkmcnt(1)
	v_mfma_f32_16x16x32_f16 v[206:209], v[58:61], v[114:117], v[206:209]
	v_mfma_f32_16x16x32_f16 v[122:125], v[62:65], v[114:117], v[122:125]
	s_waitcnt lgkmcnt(0)
	v_mfma_f32_16x16x32_f16 v[210:213], v[58:61], v[190:193], v[214:217]
	v_mfma_f32_16x16x32_f16 v[190:193], v[62:65], v[190:193], v[218:221]
	v_add_u32_e32 v114, 0xb4000, v150
	v_min_u32_e32 v114, v114, v157
	global_load_dwordx4 v[114:117], v114, s[8:9] nt
	s_waitcnt vmcnt(21)
	v_cvt_pk_f16_f32 v113, v112, v113
	v_cvt_pk_f16_f32 v112, v110, v111
	ds_write_b16 v234, v112 offset:4864
	ds_write_b16_d16_hi v235, v112 offset:4864
	ds_write_b16 v236, v113 offset:4864
	ds_write_b16_d16_hi v237, v113 offset:4864
	s_mov_b32 s2, 0xb4000
	ds_read_b128 v[110:113], v151 offset:4512
	ds_read_b128 v[214:217], v151 offset:6336
	s_waitcnt lgkmcnt(1)
	v_mfma_f32_16x16x32_f16 v[166:169], v[58:61], v[110:113], v[166:169]
	v_mfma_f32_16x16x32_f16 v[162:165], v[62:65], v[110:113], v[162:165]
	ds_read_b128 v[110:113], v151 offset:5120
	ds_read_b128 v[218:221], v151 offset:5728
	s_waitcnt lgkmcnt(1)
	v_mfma_f32_16x16x32_f16 v[138:141], v[58:61], v[110:113], v[138:141]
	v_mfma_f32_16x16x32_f16 v[170:173], v[62:65], v[110:113], v[170:173]
	s_waitcnt lgkmcnt(0)
	v_mfma_f32_16x16x32_f16 v[174:177], v[58:61], v[218:221], v[174:177]
	v_mfma_f32_16x16x32_f16 v[126:129], v[62:65], v[218:221], v[126:129]
	v_mfma_f32_16x16x32_f16 v[118:121], v[58:61], v[214:217], v[118:121]
	v_mfma_f32_16x16x32_f16 v[214:217], v[62:65], v[214:217], v[222:225]
	v_add_u32_e32 v110, 0xca640, v244
	v_min_u32_e32 v110, v110, v157
	global_load_dwordx4 v[110:113], v110, s[8:9] nt
	s_waitcnt vmcnt(21)
	v_cvt_pk_f16_f32 v9, v8, v9
	v_cvt_pk_f16_f32 v8, v6, v7
	ds_write_b16 v238, v8 offset:5472
	ds_write_b16_d16_hi v239, v8 offset:5472
	ds_write_b16 v240, v9 offset:5472
	ds_write_b16_d16_hi v241, v9 offset:5472
	ds_read_b128 v[6:9], v151 offset:6944
	ds_read_b128 v[218:221], v151 offset:7552
	s_waitcnt lgkmcnt(1)
	v_mfma_f32_16x16x32_f16 v[186:189], v[58:61], v[6:9], v[186:189]
	v_mfma_f32_16x16x32_f16 v[6:9], v[62:65], v[6:9], v[194:197]
	s_waitcnt lgkmcnt(0)
	v_mfma_f32_16x16x32_f16 v[58:61], v[58:61], v[218:221], v[38:41]
	v_mfma_f32_16x16x32_f16 v[194:197], v[62:65], v[218:221], v[22:25]
	s_nop 2
	ds_read_b128 v[22:25], v151 offset:320
	ds_read_b128 v[38:41], v151 offset:928
	s_waitcnt lgkmcnt(1)
	v_mfma_f32_16x16x32_f16 v[130:133], v[34:37], v[22:25], v[130:133]
	v_mfma_f32_16x16x32_f16 v[218:221], v[14:17], v[22:25], v[50:53]
	s_waitcnt lgkmcnt(0)
	v_mfma_f32_16x16x32_f16 v[142:145], v[34:37], v[38:41], v[142:145]
	v_mfma_f32_16x16x32_f16 v[158:161], v[14:17], v[38:41], v[158:161]
	v_add_u32_e32 v22, 0xe0c80, v150
	v_min_u32_e32 v22, v22, v157
	global_load_dwordx4 v[62:65], v22, s[8:9] nt
	s_waitcnt vmcnt(21)
	v_cvt_pk_f16_f32 v23, v72, v73
	v_cvt_pk_f16_f32 v22, v70, v71
	ds_write_b16 v234, v22 offset:6080
	ds_write_b16_d16_hi v235, v22 offset:6080
	ds_write_b16 v236, v23 offset:6080
	ds_write_b16_d16_hi v237, v23 offset:6080
	ds_read_b128 v[22:25], v151 offset:1536
	ds_read_b128 v[38:41], v151 offset:2144
	s_waitcnt lgkmcnt(1)
	v_mfma_f32_16x16x32_f16 v[178:181], v[34:37], v[22:25], v[178:181]
	v_mfma_f32_16x16x32_f16 v[182:185], v[14:17], v[22:25], v[182:185]
	s_waitcnt lgkmcnt(0)
	v_mfma_f32_16x16x32_f16 v[198:201], v[34:37], v[38:41], v[198:201]
	v_mfma_f32_16x16x32_f16 v[202:205], v[14:17], v[38:41], v[202:205]
	ds_read_b128 v[22:25], v151 offset:2752
	ds_read_b128 v[38:41], v151 offset:3360
	s_waitcnt lgkmcnt(1)
	v_mfma_f32_16x16x32_f16 v[134:137], v[34:37], v[22:25], v[134:137]
	v_mfma_f32_16x16x32_f16 v[146:149], v[14:17], v[22:25], v[146:149]
	s_waitcnt lgkmcnt(0)
	v_mfma_f32_16x16x32_f16 v[206:209], v[34:37], v[38:41], v[206:209]
	v_mfma_f32_16x16x32_f16 v[122:125], v[14:17], v[38:41], v[122:125]
	v_add_u32_e32 v22, 0xf72c0, v244
	v_min_u32_e32 v22, v22, v157
	global_load_dwordx4 v[70:73], v22, s[8:9] nt
	s_waitcnt vmcnt(21)
	v_cvt_pk_f16_f32 v23, v76, v77
	v_cvt_pk_f16_f32 v22, v74, v75
	ds_write_b16 v238, v22 offset:6688
	ds_write_b16_d16_hi v239, v22 offset:6688
	ds_write_b16 v240, v23 offset:6688
	ds_write_b16_d16_hi v241, v23 offset:6688
	ds_read_b128 v[22:25], v151 offset:3968
	ds_read_b128 v[38:41], v151 offset:4576
	s_waitcnt lgkmcnt(1)
	v_mfma_f32_16x16x32_f16 v[210:213], v[34:37], v[22:25], v[210:213]
	v_mfma_f32_16x16x32_f16 v[190:193], v[14:17], v[22:25], v[190:193]
	s_waitcnt lgkmcnt(0)
	v_mfma_f32_16x16x32_f16 v[166:169], v[34:37], v[38:41], v[166:169]
	v_mfma_f32_16x16x32_f16 v[162:165], v[14:17], v[38:41], v[162:165]
	ds_read_b128 v[22:25], v151 offset:5184
	ds_read_b128 v[38:41], v151 offset:5792
	s_waitcnt lgkmcnt(1)
	v_mfma_f32_16x16x32_f16 v[138:141], v[34:37], v[22:25], v[138:141]
	v_mfma_f32_16x16x32_f16 v[170:173], v[14:17], v[22:25], v[170:173]
	s_waitcnt lgkmcnt(0)
	v_mfma_f32_16x16x32_f16 v[174:177], v[34:37], v[38:41], v[174:177]
	v_mfma_f32_16x16x32_f16 v[126:129], v[14:17], v[38:41], v[126:129]
	v_add_u32_e32 v22, 0x10d900, v150
	v_min_u32_e32 v22, v22, v157
	v_cndmask_b32_e64 v22, 0, v22, s[0:1]
	global_load_dwordx4 v[74:77], v22, s[8:9] nt
	s_waitcnt vmcnt(21)
	v_cvt_pk_f16_f32 v23, v80, v81
	v_cvt_pk_f16_f32 v22, v78, v79
	ds_write_b16 v234, v22 offset:7296
	ds_write_b16_d16_hi v235, v22 offset:7296
	ds_write_b16 v236, v23 offset:7296
	ds_write_b16_d16_hi v237, v23 offset:7296
	ds_read_b128 v[22:25], v151 offset:6400
	ds_read_b128 v[38:41], v151 offset:7008
	s_mov_b32 s3, 0x70000
	ds_read_b128 v[78:81], v151 offset:7616
	s_waitcnt lgkmcnt(0)
	v_mfma_f32_16x16x32_f16 v[118:121], v[34:37], v[22:25], v[118:121]
	s_barrier
	v_sub_u32_e32 v245, v234, v243
	v_add_u32_e32 v246, 0xfffffdc0, v245
	v_min_u32_e32 v245, v245, v246
	v_add_u32_e32 v234, v242, v245
	v_sub_u32_e32 v245, v235, v243
	v_add_u32_e32 v246, 0xfffffdc0, v245
	v_min_u32_e32 v245, v245, v246
	v_add_u32_e32 v235, v242, v245
	v_sub_u32_e32 v245, v236, v243
	v_add_u32_e32 v246, 0xfffffdc0, v245
	v_min_u32_e32 v245, v245, v246
	v_add_u32_e32 v236, v242, v245
	v_sub_u32_e32 v245, v237, v243
	v_add_u32_e32 v246, 0xfffffdc0, v245
	v_min_u32_e32 v245, v245, v246
	v_add_u32_e32 v237, v242, v245
	v_sub_u32_e32 v245, v238, v243
	v_add_u32_e32 v246, 0xfffffdc0, v245
	v_min_u32_e32 v245, v245, v246
	v_add_u32_e32 v238, v242, v245
	v_sub_u32_e32 v245, v239, v243
	v_add_u32_e32 v246, 0xfffffdc0, v245
	v_min_u32_e32 v245, v245, v246
	v_add_u32_e32 v239, v242, v245
	v_sub_u32_e32 v245, v240, v243
	v_add_u32_e32 v246, 0xfffffdc0, v245
	v_min_u32_e32 v245, v245, v246
	v_add_u32_e32 v240, v242, v245
	v_sub_u32_e32 v245, v241, v243
	v_add_u32_e32 v246, 0xfffffdc0, v245
	v_min_u32_e32 v245, v245, v246
	v_add_u32_e32 v241, v242, v245
	v_mfma_f32_16x16x32_f16 v[214:217], v[14:17], v[22:25], v[214:217]
	v_add_co_u32_e32 v22, vcc, s3, v152
	s_mov_b32 s3, 0x74000
	s_nop 0
	v_addc_co_u32_e32 v23, vcc, 0, v153, vcc
	v_mfma_f32_16x16x32_f16 v[222:225], v[14:17], v[38:41], v[6:9]
	s_nop 2
	v_add_co_u32_e32 v6, vcc, s3, v152
	v_mfma_f32_16x16x32_f16 v[186:189], v[34:37], v[38:41], v[186:189]
	s_nop 0
	v_addc_co_u32_e32 v7, vcc, 0, v153, vcc
	global_load_dwordx4 v[38:41], v[22:23], off sc1
	global_load_dwordx4 v[50:53], v[22:23], off offset:256 sc1
	s_nop 0
	global_load_dwordx4 v[22:25], v[6:7], off sc1
	s_nop 0
	global_load_dwordx4 v[6:9], v[6:7], off offset:256 sc1
	v_mfma_f32_16x16x32_f16 v[34:37], v[34:37], v[78:81], v[58:61]
	v_mfma_f32_16x16x32_f16 v[14:17], v[14:17], v[78:81], v[194:197]
	v_add_u32_e32 v157, 0x111524dc, v154
	s_nop 0
	ds_read_b128 v[58:61], v151 offset:384
	v_add_u32_e32 v78, 0x1000, v150
	s_waitcnt vmcnt(24) lgkmcnt(0)
	v_mfma_f32_16x16x32_f16 v[130:133], v[42:45], v[58:61], v[130:133]
	s_waitcnt vmcnt(23)
	v_mfma_f32_16x16x32_f16 v[58:61], v[46:49], v[58:61], v[218:221]
	v_min_u32_e32 v78, v78, v157
	global_load_dwordx4 v[78:81], v78, s[8:9] nt
	s_waitcnt vmcnt(21)
	v_cvt_pk_f16_f32 v85, v84, v85
	v_cvt_pk_f16_f32 v84, v82, v83
	ds_write_b16 v234, v84 offset:0
	ds_write_b16_d16_hi v235, v84 offset:0
	ds_write_b16 v236, v85 offset:0
	ds_write_b16_d16_hi v237, v85 offset:0
	ds_read_b128 v[82:85], v151 offset:992
	ds_read_b128 v[194:197], v151 offset:1600
	s_waitcnt lgkmcnt(1)
	v_mfma_f32_16x16x32_f16 v[142:145], v[42:45], v[82:85], v[142:145]
	v_mfma_f32_16x16x32_f16 v[158:161], v[46:49], v[82:85], v[158:161]
	s_waitcnt lgkmcnt(0)
	v_mfma_f32_16x16x32_f16 v[178:181], v[42:45], v[194:197], v[178:181]
	v_mfma_f32_16x16x32_f16 v[182:185], v[46:49], v[194:197], v[182:185]
	ds_read_b128 v[82:85], v151 offset:2208
	ds_read_b128 v[194:197], v151 offset:2816
	s_waitcnt lgkmcnt(1)
	v_mfma_f32_16x16x32_f16 v[198:201], v[42:45], v[82:85], v[198:201]
	v_mfma_f32_16x16x32_f16 v[202:205], v[46:49], v[82:85], v[202:205]
	s_waitcnt lgkmcnt(0)
	v_mfma_f32_16x16x32_f16 v[134:137], v[42:45], v[194:197], v[134:137]
	v_mfma_f32_16x16x32_f16 v[146:149], v[46:49], v[194:197], v[146:149]
	v_add_u32_e32 v82, 0x17640, v244
	v_min_u32_e32 v82, v82, v157
	global_load_dwordx4 v[82:85], v82, s[8:9] nt
	s_waitcnt vmcnt(21)
	v_cvt_pk_f16_f32 v89, v88, v89
	v_cvt_pk_f16_f32 v88, v86, v87
	ds_write_b16 v238, v88 offset:608
	ds_write_b16_d16_hi v239, v88 offset:608
	ds_write_b16 v240, v89 offset:608
	ds_write_b16_d16_hi v241, v89 offset:608
	ds_read_b128 v[86:89], v151 offset:3424
	ds_read_b128 v[194:197], v151 offset:5248
	s_waitcnt lgkmcnt(1)
	v_mfma_f32_16x16x32_f16 v[206:209], v[42:45], v[86:89], v[206:209]
	v_mfma_f32_16x16x32_f16 v[122:125], v[46:49], v[86:89], v[122:125]
	ds_read_b128 v[86:89], v151 offset:4032
	ds_read_b128 v[218:221], v151 offset:4640
	s_waitcnt lgkmcnt(1)
	v_mfma_f32_16x16x32_f16 v[210:213], v[42:45], v[86:89], v[210:213]
	v_mfma_f32_16x16x32_f16 v[190:193], v[46:49], v[86:89], v[190:193]
	s_waitcnt lgkmcnt(0)
	v_mfma_f32_16x16x32_f16 v[166:169], v[42:45], v[218:221], v[166:169]
	v_mfma_f32_16x16x32_f16 v[162:165], v[46:49], v[218:221], v[162:165]
	v_mfma_f32_16x16x32_f16 v[138:141], v[42:45], v[194:197], v[138:141]
	v_mfma_f32_16x16x32_f16 v[170:173], v[46:49], v[194:197], v[170:173]
	v_add_u32_e32 v86, 0x2dc80, v150
	v_min_u32_e32 v86, v86, v157
	global_load_dwordx4 v[86:89], v86, s[8:9] nt
	s_waitcnt vmcnt(21)
	v_cvt_pk_f16_f32 v93, v92, v93
	v_cvt_pk_f16_f32 v92, v90, v91
	ds_write_b16 v234, v92 offset:1216
	ds_write_b16_d16_hi v235, v92 offset:1216
	ds_write_b16 v236, v93 offset:1216
	ds_write_b16_d16_hi v237, v93 offset:1216
	ds_read_b128 v[90:93], v151 offset:5856
	ds_read_b128 v[194:197], v151 offset:6464
	s_waitcnt lgkmcnt(1)
	v_mfma_f32_16x16x32_f16 v[174:177], v[42:45], v[90:93], v[174:177]
	v_mfma_f32_16x16x32_f16 v[126:129], v[46:49], v[90:93], v[126:129]
	s_waitcnt lgkmcnt(0)
	v_mfma_f32_16x16x32_f16 v[118:121], v[42:45], v[194:197], v[118:121]
	v_mfma_f32_16x16x32_f16 v[194:197], v[46:49], v[194:197], v[214:217]
	ds_read_b128 v[90:93], v151 offset:7072
	s_nop 1
	ds_read_b128 v[214:217], v151 offset:7680
	s_waitcnt lgkmcnt(1)
	v_mfma_f32_16x16x32_f16 v[186:189], v[42:45], v[90:93], v[186:189]
	v_mfma_f32_16x16x32_f16 v[218:221], v[46:49], v[90:93], v[222:225]
	s_waitcnt lgkmcnt(0)
	v_mfma_f32_16x16x32_f16 v[34:37], v[42:45], v[214:217], v[34:37]
	v_mfma_f32_16x16x32_f16 v[46:49], v[46:49], v[214:217], v[14:17]
	s_nop 2
	v_add_u32_e32 v14, 0x442c0, v244
	v_min_u32_e32 v14, v14, v157
	global_load_dwordx4 v[90:93], v14, s[8:9] nt
	s_waitcnt vmcnt(21)
	v_cvt_pk_f16_f32 v15, v96, v97
	v_cvt_pk_f16_f32 v14, v94, v95
	ds_write_b16 v238, v14 offset:1824
	ds_write_b16_d16_hi v239, v14 offset:1824
	ds_write_b16 v240, v15 offset:1824
	ds_write_b16_d16_hi v241, v15 offset:1824
	ds_read_b128 v[14:17], v151 offset:448
	ds_read_b128 v[42:45], v151 offset:1056
	s_waitcnt lgkmcnt(1)
	v_mfma_f32_16x16x32_f16 v[130:133], v[26:29], v[14:17], v[130:133]
	v_mfma_f32_16x16x32_f16 v[214:217], v[2:5], v[14:17], v[58:61]
	s_waitcnt lgkmcnt(0)
	v_mfma_f32_16x16x32_f16 v[142:145], v[26:29], v[42:45], v[142:145]
	v_mfma_f32_16x16x32_f16 v[158:161], v[2:5], v[42:45], v[158:161]
	ds_read_b128 v[14:17], v151 offset:1664
	ds_read_b128 v[42:45], v151 offset:2272
	s_waitcnt lgkmcnt(1)
	v_mfma_f32_16x16x32_f16 v[178:181], v[26:29], v[14:17], v[178:181]
	v_mfma_f32_16x16x32_f16 v[182:185], v[2:5], v[14:17], v[182:185]
	s_waitcnt lgkmcnt(0)
	v_mfma_f32_16x16x32_f16 v[198:201], v[26:29], v[42:45], v[198:201]
	v_mfma_f32_16x16x32_f16 v[202:205], v[2:5], v[42:45], v[202:205]
	v_add_u32_e32 v14, 0x5a900, v150
	v_min_u32_e32 v14, v14, v157
	global_load_dwordx4 v[94:97], v14, s[8:9] nt
	s_waitcnt vmcnt(21)
	v_cvt_pk_f16_f32 v15, v100, v101
	v_cvt_pk_f16_f32 v14, v98, v99
	ds_write_b16 v234, v14 offset:2432
	ds_write_b16_d16_hi v235, v14 offset:2432
	ds_write_b16 v236, v15 offset:2432
	ds_write_b16_d16_hi v237, v15 offset:2432
	ds_read_b128 v[14:17], v151 offset:2880
	ds_read_b128 v[42:45], v151 offset:3488
	s_waitcnt lgkmcnt(1)
	v_mfma_f32_16x16x32_f16 v[134:137], v[26:29], v[14:17], v[134:137]
	v_mfma_f32_16x16x32_f16 v[146:149], v[2:5], v[14:17], v[146:149]
	s_waitcnt lgkmcnt(0)
	v_mfma_f32_16x16x32_f16 v[206:209], v[26:29], v[42:45], v[206:209]
	v_mfma_f32_16x16x32_f16 v[122:125], v[2:5], v[42:45], v[122:125]
	ds_read_b128 v[14:17], v151 offset:4096
	ds_read_b128 v[42:45], v151 offset:4704
	s_waitcnt lgkmcnt(1)
	v_mfma_f32_16x16x32_f16 v[210:213], v[26:29], v[14:17], v[210:213]
	v_mfma_f32_16x16x32_f16 v[190:193], v[2:5], v[14:17], v[190:193]
	s_waitcnt lgkmcnt(0)
	v_mfma_f32_16x16x32_f16 v[166:169], v[26:29], v[42:45], v[166:169]
	v_mfma_f32_16x16x32_f16 v[162:165], v[2:5], v[42:45], v[162:165]
	v_add_u32_e32 v14, 0x70f40, v244
	v_min_u32_e32 v14, v14, v157
	global_load_dwordx4 v[98:101], v14, s[8:9] nt
	s_waitcnt vmcnt(21)
	v_cvt_pk_f16_f32 v15, v104, v105
	v_cvt_pk_f16_f32 v14, v102, v103
	ds_write_b16 v238, v14 offset:3040
	ds_write_b16_d16_hi v239, v14 offset:3040
	ds_write_b16 v240, v15 offset:3040
	ds_write_b16_d16_hi v241, v15 offset:3040
	ds_read_b128 v[14:17], v151 offset:5312
	ds_read_b128 v[42:45], v151 offset:5920
	s_waitcnt lgkmcnt(1)
	v_mfma_f32_16x16x32_f16 v[138:141], v[26:29], v[14:17], v[138:141]
	v_mfma_f32_16x16x32_f16 v[170:173], v[2:5], v[14:17], v[170:173]
	s_waitcnt lgkmcnt(0)
	v_mfma_f32_16x16x32_f16 v[174:177], v[26:29], v[42:45], v[174:177]
	v_mfma_f32_16x16x32_f16 v[126:129], v[2:5], v[42:45], v[126:129]
	ds_read_b128 v[14:17], v151 offset:6528
	ds_read_b128 v[42:45], v151 offset:7136
	s_waitcnt lgkmcnt(1)
	v_mfma_f32_16x16x32_f16 v[118:121], v[26:29], v[14:17], v[118:121]
	v_mfma_f32_16x16x32_f16 v[194:197], v[2:5], v[14:17], v[194:197]
	s_waitcnt lgkmcnt(0)
	v_mfma_f32_16x16x32_f16 v[186:189], v[26:29], v[42:45], v[186:189]
	v_mfma_f32_16x16x32_f16 v[218:221], v[2:5], v[42:45], v[218:221]
	v_add_u32_e32 v14, 0x87580, v150
	v_min_u32_e32 v14, v14, v157
	global_load_dwordx4 v[102:105], v14, s[8:9] nt
	s_waitcnt vmcnt(21)
	v_cvt_pk_f16_f32 v15, v108, v109
	v_cvt_pk_f16_f32 v14, v106, v107
	ds_write_b16 v234, v14 offset:3648
	ds_write_b16_d16_hi v235, v14 offset:3648
	ds_write_b16 v236, v15 offset:3648
	ds_write_b16_d16_hi v237, v15 offset:3648
	ds_read_b128 v[106:109], v151 offset:7744
	s_mov_b32 s3, 0x78000
	v_add_co_u32_e32 v14, vcc, s3, v152
	s_mov_b32 s3, 0x7c000
	s_nop 0
	v_addc_co_u32_e32 v15, vcc, 0, v153, vcc
	global_load_dwordx4 v[42:45], v[14:15], off sc1
	global_load_dwordx4 v[58:61], v[14:15], off offset:256 sc1
	v_add_co_u32_e32 v14, vcc, s3, v152
	s_waitcnt lgkmcnt(0)
	v_mfma_f32_16x16x32_f16 v[26:29], v[26:29], v[106:109], v[34:37]
	v_addc_co_u32_e32 v15, vcc, 0, v153, vcc
	s_nop 1
	global_load_dwordx4 v[34:37], v[14:15], off sc1
	s_nop 0
	global_load_dwordx4 v[14:17], v[14:15], off offset:256 sc1
	v_mfma_f32_16x16x32_f16 v[46:49], v[2:5], v[106:109], v[46:49]
	ds_read_b128 v[2:5], v151 offset:512
	ds_read_b128 v[106:109], v151 offset:1120
	s_waitcnt vmcnt(24) lgkmcnt(1)
	v_mfma_f32_16x16x32_f16 v[130:133], v[54:57], v[2:5], v[130:133]
	s_waitcnt vmcnt(23)
	v_mfma_f32_16x16x32_f16 v[214:217], v[66:69], v[2:5], v[214:217]
	ds_read_b128 v[2:5], v151 offset:1728
	s_waitcnt lgkmcnt(1)
	v_mfma_f32_16x16x32_f16 v[142:145], v[54:57], v[106:109], v[142:145]
	v_mfma_f32_16x16x32_f16 v[158:161], v[66:69], v[106:109], v[158:161]
	s_waitcnt lgkmcnt(0)
	v_mfma_f32_16x16x32_f16 v[178:181], v[54:57], v[2:5], v[178:181]
	v_mfma_f32_16x16x32_f16 v[182:185], v[66:69], v[2:5], v[182:185]
	v_add_u32_e32 v2, 0x9dbc0, v244
	v_min_u32_e32 v2, v2, v157
	global_load_dwordx4 v[2:5], v2, s[8:9] nt
	s_waitcnt vmcnt(21)
	v_cvt_pk_f16_f32 v13, v12, v13
	v_cvt_pk_f16_f32 v12, v10, v11
	ds_write_b16 v238, v12 offset:4256
	ds_write_b16_d16_hi v239, v12 offset:4256
	ds_write_b16 v240, v13 offset:4256
	ds_write_b16_d16_hi v241, v13 offset:4256
	ds_read_b128 v[10:13], v151 offset:2336
	ds_read_b128 v[106:109], v151 offset:2944
	s_waitcnt lgkmcnt(1)
	v_mfma_f32_16x16x32_f16 v[198:201], v[54:57], v[10:13], v[198:201]
	v_mfma_f32_16x16x32_f16 v[10:13], v[66:69], v[10:13], v[202:205]
	s_waitcnt lgkmcnt(0)
	v_mfma_f32_16x16x32_f16 v[134:137], v[54:57], v[106:109], v[134:137]
	v_mfma_f32_16x16x32_f16 v[146:149], v[66:69], v[106:109], v[146:149]
	ds_read_b128 v[106:109], v151 offset:3552
	ds_read_b128 v[202:205], v151 offset:4160
	s_waitcnt lgkmcnt(1)
	v_mfma_f32_16x16x32_f16 v[206:209], v[54:57], v[106:109], v[206:209]
	v_mfma_f32_16x16x32_f16 v[122:125], v[66:69], v[106:109], v[122:125]
	s_waitcnt lgkmcnt(0)
	v_mfma_f32_16x16x32_f16 v[210:213], v[54:57], v[202:205], v[210:213]
	v_mfma_f32_16x16x32_f16 v[190:193], v[66:69], v[202:205], v[190:193]
	v_add_u32_e32 v106, 0xb4200, v150
	v_min_u32_e32 v106, v106, v157
	global_load_dwordx4 v[106:109], v106, s[8:9] nt
	s_waitcnt vmcnt(21)
	v_cvt_pk_f16_f32 v117, v116, v117
	v_cvt_pk_f16_f32 v116, v114, v115
	ds_write_b16 v234, v116 offset:4864
	ds_write_b16_d16_hi v235, v116 offset:4864
	ds_write_b16 v236, v117 offset:4864
	ds_write_b16_d16_hi v237, v117 offset:4864
	ds_read_b128 v[114:117], v151 offset:4768
	ds_read_b128 v[202:205], v151 offset:6592
	s_waitcnt lgkmcnt(1)
	v_mfma_f32_16x16x32_f16 v[166:169], v[54:57], v[114:117], v[166:169]
	v_mfma_f32_16x16x32_f16 v[162:165], v[66:69], v[114:117], v[162:165]
	ds_read_b128 v[114:117], v151 offset:5376
	ds_read_b128 v[222:225], v151 offset:5984
	s_waitcnt lgkmcnt(1)
	v_mfma_f32_16x16x32_f16 v[138:141], v[54:57], v[114:117], v[138:141]
	v_mfma_f32_16x16x32_f16 v[170:173], v[66:69], v[114:117], v[170:173]
	s_waitcnt lgkmcnt(0)
	v_mfma_f32_16x16x32_f16 v[174:177], v[54:57], v[222:225], v[174:177]
	v_mfma_f32_16x16x32_f16 v[126:129], v[66:69], v[222:225], v[126:129]
	v_mfma_f32_16x16x32_f16 v[222:225], v[54:57], v[202:205], v[118:121]
	v_mfma_f32_16x16x32_f16 v[194:197], v[66:69], v[202:205], v[194:197]
	v_add_u32_e32 v114, 0xca840, v244
	v_min_u32_e32 v114, v114, v157
	global_load_dwordx4 v[114:117], v114, s[8:9] nt
	s_waitcnt vmcnt(21)
	v_cvt_pk_f16_f32 v113, v112, v113
	v_cvt_pk_f16_f32 v112, v110, v111
	ds_write_b16 v238, v112 offset:5472
	ds_write_b16_d16_hi v239, v112 offset:5472
	ds_write_b16 v240, v113 offset:5472
	ds_write_b16_d16_hi v241, v113 offset:5472
	ds_read_b128 v[110:113], v151 offset:7200
	ds_read_b128 v[118:121], v151 offset:7808
	s_waitcnt lgkmcnt(1)
	v_mfma_f32_16x16x32_f16 v[186:189], v[54:57], v[110:113], v[186:189]
	v_mfma_f32_16x16x32_f16 v[202:205], v[66:69], v[110:113], v[218:221]
	s_waitcnt lgkmcnt(0)
	v_mfma_f32_16x16x32_f16 v[26:29], v[54:57], v[118:121], v[26:29]
	v_mfma_f32_16x16x32_f16 v[66:69], v[66:69], v[118:121], v[46:49]
	s_nop 2
	ds_read_b128 v[46:49], v151 offset:0
	ds_read_b128 v[54:57], v151 offset:608
	s_waitcnt lgkmcnt(1)
	v_mfma_f32_16x16x32_f16 v[130:133], v[30:33], v[46:49], v[130:133]
	v_mfma_f32_16x16x32_f16 v[214:217], v[18:21], v[46:49], v[214:217]
	s_waitcnt lgkmcnt(0)
	v_mfma_f32_16x16x32_f16 v[142:145], v[30:33], v[54:57], v[142:145]
	v_mfma_f32_16x16x32_f16 v[158:161], v[18:21], v[54:57], v[158:161]
	v_add_u32_e32 v46, 0xe0e80, v150
	v_min_u32_e32 v46, v46, v157
	global_load_dwordx4 v[110:113], v46, s[8:9] nt
	s_waitcnt vmcnt(21)
	v_cvt_pk_f16_f32 v47, v64, v65
	v_cvt_pk_f16_f32 v46, v62, v63
	ds_write_b16 v234, v46 offset:6080
	ds_write_b16_d16_hi v235, v46 offset:6080
	ds_write_b16 v236, v47 offset:6080
	ds_write_b16_d16_hi v237, v47 offset:6080
	ds_read_b128 v[46:49], v151 offset:1216
	ds_read_b128 v[54:57], v151 offset:1824
	s_waitcnt lgkmcnt(1)
	v_mfma_f32_16x16x32_f16 v[62:65], v[30:33], v[46:49], v[178:181]
	v_mfma_f32_16x16x32_f16 v[178:181], v[18:21], v[46:49], v[182:185]
	s_waitcnt lgkmcnt(0)
	v_mfma_f32_16x16x32_f16 v[182:185], v[30:33], v[54:57], v[198:201]
	v_mfma_f32_16x16x32_f16 v[198:201], v[18:21], v[54:57], v[10:13]
	s_nop 2
	ds_read_b128 v[10:13], v151 offset:2432
	ds_read_b128 v[46:49], v151 offset:3040
	s_waitcnt lgkmcnt(1)
	v_mfma_f32_16x16x32_f16 v[134:137], v[30:33], v[10:13], v[134:137]
	v_mfma_f32_16x16x32_f16 v[146:149], v[18:21], v[10:13], v[146:149]
	s_waitcnt lgkmcnt(0)
	v_mfma_f32_16x16x32_f16 v[206:209], v[30:33], v[46:49], v[206:209]
	v_mfma_f32_16x16x32_f16 v[122:125], v[18:21], v[46:49], v[122:125]
	v_add_u32_e32 v10, 0xf74c0, v244
	v_min_u32_e32 v10, v10, v157
	global_load_dwordx4 v[118:121], v10, s[8:9] nt
	s_waitcnt vmcnt(21)
	v_cvt_pk_f16_f32 v11, v72, v73
	v_cvt_pk_f16_f32 v10, v70, v71
	ds_write_b16 v238, v10 offset:6688
	ds_write_b16_d16_hi v239, v10 offset:6688
	ds_write_b16 v240, v11 offset:6688
	ds_write_b16_d16_hi v241, v11 offset:6688
	ds_read_b128 v[10:13], v151 offset:3648
	ds_read_b128 v[46:49], v151 offset:4256
	s_waitcnt lgkmcnt(1)
	v_mfma_f32_16x16x32_f16 v[210:213], v[30:33], v[10:13], v[210:213]
	v_mfma_f32_16x16x32_f16 v[190:193], v[18:21], v[10:13], v[190:193]
	s_waitcnt lgkmcnt(0)
	v_mfma_f32_16x16x32_f16 v[166:169], v[30:33], v[46:49], v[166:169]
	v_mfma_f32_16x16x32_f16 v[162:165], v[18:21], v[46:49], v[162:165]
	ds_read_b128 v[10:13], v151 offset:4864
	ds_read_b128 v[46:49], v151 offset:5472
	s_waitcnt lgkmcnt(1)
	v_mfma_f32_16x16x32_f16 v[138:141], v[30:33], v[10:13], v[138:141]
	v_mfma_f32_16x16x32_f16 v[170:173], v[18:21], v[10:13], v[170:173]
	s_waitcnt lgkmcnt(0)
	v_mfma_f32_16x16x32_f16 v[174:177], v[30:33], v[46:49], v[174:177]
	v_mfma_f32_16x16x32_f16 v[126:129], v[18:21], v[46:49], v[126:129]
	v_add_u32_e32 v10, 0x10db00, v150
	v_min_u32_e32 v10, v10, v157
	v_cndmask_b32_e64 v10, 0, v10, s[0:1]
	global_load_dwordx4 v[70:73], v10, s[8:9] nt
	s_waitcnt vmcnt(21)
	v_cvt_pk_f16_f32 v11, v76, v77
	v_cvt_pk_f16_f32 v10, v74, v75
	ds_write_b16 v234, v10 offset:7296
	ds_write_b16_d16_hi v235, v10 offset:7296
	ds_write_b16 v236, v11 offset:7296
	ds_write_b16_d16_hi v237, v11 offset:7296
	ds_read_b128 v[10:13], v151 offset:6080
	ds_read_b128 v[46:49], v151 offset:6688
	ds_read_b128 v[74:77], v151 offset:7296
	s_mov_b32 s3, 0x80000
	s_waitcnt lgkmcnt(0)
	v_mfma_f32_16x16x32_f16 v[218:221], v[30:33], v[10:13], v[222:225]
	s_barrier
	v_sub_u32_e32 v245, v234, v243
	v_add_u32_e32 v246, 0xfffffdc0, v245
	v_min_u32_e32 v245, v245, v246
	v_add_u32_e32 v234, v242, v245
	v_sub_u32_e32 v245, v235, v243
	v_add_u32_e32 v246, 0xfffffdc0, v245
	v_min_u32_e32 v245, v245, v246
	v_add_u32_e32 v235, v242, v245
	v_sub_u32_e32 v245, v236, v243
	v_add_u32_e32 v246, 0xfffffdc0, v245
	v_min_u32_e32 v245, v245, v246
	v_add_u32_e32 v236, v242, v245
	v_sub_u32_e32 v245, v237, v243
	v_add_u32_e32 v246, 0xfffffdc0, v245
	v_min_u32_e32 v245, v245, v246
	v_add_u32_e32 v237, v242, v245
	v_sub_u32_e32 v245, v238, v243
	v_add_u32_e32 v246, 0xfffffdc0, v245
	v_min_u32_e32 v245, v245, v246
	v_add_u32_e32 v238, v242, v245
	v_sub_u32_e32 v245, v239, v243
	v_add_u32_e32 v246, 0xfffffdc0, v245
	v_min_u32_e32 v245, v245, v246
	v_add_u32_e32 v239, v242, v245
	v_sub_u32_e32 v245, v240, v243
	v_add_u32_e32 v246, 0xfffffdc0, v245
	v_min_u32_e32 v245, v245, v246
	v_add_u32_e32 v240, v242, v245
	v_sub_u32_e32 v245, v241, v243
	v_add_u32_e32 v246, 0xfffffdc0, v245
	v_min_u32_e32 v245, v245, v246
	v_add_u32_e32 v241, v242, v245
	v_mfma_f32_16x16x32_f16 v[194:197], v[18:21], v[10:13], v[194:197]
	v_add_co_u32_e32 v10, vcc, s3, v152
	s_mov_b32 s3, 0x84000
	s_nop 0
	v_addc_co_u32_e32 v11, vcc, 0, v153, vcc
	v_mfma_f32_16x16x32_f16 v[186:189], v[30:33], v[46:49], v[186:189]
	v_mfma_f32_16x16x32_f16 v[202:205], v[18:21], v[46:49], v[202:205]
	global_load_dwordx4 v[46:49], v[10:11], off sc1
	global_load_dwordx4 v[54:57], v[10:11], off offset:256 sc1
	v_add_co_u32_e32 v10, vcc, s3, v152
	v_mfma_f32_16x16x32_f16 v[30:33], v[30:33], v[74:77], v[26:29]
	s_nop 0
	v_addc_co_u32_e32 v11, vcc, 0, v153, vcc
	s_nop 0
	global_load_dwordx4 v[26:29], v[10:11], off sc1
	s_nop 0
	global_load_dwordx4 v[10:13], v[10:11], off offset:256 sc1
	v_mfma_f32_16x16x32_f16 v[18:21], v[18:21], v[74:77], v[66:69]
	v_add_u32_e32 v157, 0x111526dc, v154
	s_nop 1
	ds_read_b128 v[66:69], v151 offset:64
	v_add_u32_e32 v74, 0x1200, v150
	s_waitcnt vmcnt(24) lgkmcnt(0)
	v_mfma_f32_16x16x32_f16 v[130:133], v[38:41], v[66:69], v[130:133]
	s_waitcnt vmcnt(23)
	v_mfma_f32_16x16x32_f16 v[66:69], v[50:53], v[66:69], v[214:217]
	v_min_u32_e32 v74, v74, v157
	global_load_dwordx4 v[74:77], v74, s[8:9] nt
	s_waitcnt vmcnt(21)
	v_cvt_pk_f16_f32 v81, v80, v81
	v_cvt_pk_f16_f32 v80, v78, v79
	ds_write_b16 v234, v80 offset:0
	ds_write_b16_d16_hi v235, v80 offset:0
	ds_write_b16 v236, v81 offset:0
	ds_write_b16_d16_hi v237, v81 offset:0
	ds_read_b128 v[78:81], v151 offset:672
	ds_read_b128 v[214:217], v151 offset:1280
	s_waitcnt lgkmcnt(1)
	v_mfma_f32_16x16x32_f16 v[142:145], v[38:41], v[78:81], v[142:145]
	v_mfma_f32_16x16x32_f16 v[158:161], v[50:53], v[78:81], v[158:161]
	s_waitcnt lgkmcnt(0)
	v_mfma_f32_16x16x32_f16 v[62:65], v[38:41], v[214:217], v[62:65]
	v_mfma_f32_16x16x32_f16 v[178:181], v[50:53], v[214:217], v[178:181]
	ds_read_b128 v[78:81], v151 offset:1888
	ds_read_b128 v[214:217], v151 offset:2496
	s_waitcnt lgkmcnt(1)
	v_mfma_f32_16x16x32_f16 v[182:185], v[38:41], v[78:81], v[182:185]
	v_mfma_f32_16x16x32_f16 v[198:201], v[50:53], v[78:81], v[198:201]
	s_waitcnt lgkmcnt(0)
	v_mfma_f32_16x16x32_f16 v[134:137], v[38:41], v[214:217], v[134:137]
	v_mfma_f32_16x16x32_f16 v[146:149], v[50:53], v[214:217], v[146:149]
	v_add_u32_e32 v78, 0x17840, v244
	v_min_u32_e32 v78, v78, v157
	global_load_dwordx4 v[78:81], v78, s[8:9] nt
	s_waitcnt vmcnt(21)
	v_cvt_pk_f16_f32 v85, v84, v85
	v_cvt_pk_f16_f32 v84, v82, v83
	ds_write_b16 v238, v84 offset:608
	ds_write_b16_d16_hi v239, v84 offset:608
	ds_write_b16 v240, v85 offset:608
	ds_write_b16_d16_hi v241, v85 offset:608
	ds_read_b128 v[82:85], v151 offset:3104
	ds_read_b128 v[214:217], v151 offset:4928
	s_waitcnt lgkmcnt(1)
	v_mfma_f32_16x16x32_f16 v[206:209], v[38:41], v[82:85], v[206:209]
	v_mfma_f32_16x16x32_f16 v[122:125], v[50:53], v[82:85], v[122:125]
	ds_read_b128 v[82:85], v151 offset:3712
	ds_read_b128 v[222:225], v151 offset:4320
	s_waitcnt lgkmcnt(1)
	v_mfma_f32_16x16x32_f16 v[210:213], v[38:41], v[82:85], v[210:213]
	v_mfma_f32_16x16x32_f16 v[190:193], v[50:53], v[82:85], v[190:193]
	s_waitcnt lgkmcnt(0)
	v_mfma_f32_16x16x32_f16 v[166:169], v[38:41], v[222:225], v[166:169]
	v_mfma_f32_16x16x32_f16 v[162:165], v[50:53], v[222:225], v[162:165]
	v_mfma_f32_16x16x32_f16 v[138:141], v[38:41], v[214:217], v[138:141]
	v_mfma_f32_16x16x32_f16 v[170:173], v[50:53], v[214:217], v[170:173]
	v_add_u32_e32 v82, 0x2de80, v150
	v_min_u32_e32 v82, v82, v157
	global_load_dwordx4 v[82:85], v82, s[8:9] nt
	s_waitcnt vmcnt(21)
	v_cvt_pk_f16_f32 v89, v88, v89
	v_cvt_pk_f16_f32 v88, v86, v87
	ds_write_b16 v234, v88 offset:1216
	ds_write_b16_d16_hi v235, v88 offset:1216
	ds_write_b16 v236, v89 offset:1216
	ds_write_b16_d16_hi v237, v89 offset:1216
	ds_read_b128 v[86:89], v151 offset:5536
	ds_read_b128 v[214:217], v151 offset:6144
	s_waitcnt lgkmcnt(1)
	v_mfma_f32_16x16x32_f16 v[174:177], v[38:41], v[86:89], v[174:177]
	v_mfma_f32_16x16x32_f16 v[126:129], v[50:53], v[86:89], v[126:129]
	s_waitcnt lgkmcnt(0)
	v_mfma_f32_16x16x32_f16 v[218:221], v[38:41], v[214:217], v[218:221]
	v_mfma_f32_16x16x32_f16 v[194:197], v[50:53], v[214:217], v[194:197]
	ds_read_b128 v[86:89], v151 offset:6752
	ds_read_b128 v[214:217], v151 offset:7360
	s_waitcnt lgkmcnt(1)
	v_mfma_f32_16x16x32_f16 v[186:189], v[38:41], v[86:89], v[186:189]
	v_mfma_f32_16x16x32_f16 v[202:205], v[50:53], v[86:89], v[202:205]
	s_waitcnt lgkmcnt(0)
	v_mfma_f32_16x16x32_f16 v[30:33], v[38:41], v[214:217], v[30:33]
	v_mfma_f32_16x16x32_f16 v[38:41], v[50:53], v[214:217], v[18:21]
	s_nop 2
	v_add_u32_e32 v18, 0x444c0, v244
	v_min_u32_e32 v18, v18, v157
	global_load_dwordx4 v[50:53], v18, s[8:9] nt
	s_waitcnt vmcnt(21)
	v_cvt_pk_f16_f32 v19, v92, v93
	v_cvt_pk_f16_f32 v18, v90, v91
	ds_write_b16 v238, v18 offset:1824
	ds_write_b16_d16_hi v239, v18 offset:1824
	ds_write_b16 v240, v19 offset:1824
	ds_write_b16_d16_hi v241, v19 offset:1824
	ds_read_b128 v[18:21], v151 offset:128
	ds_read_b128 v[86:89], v151 offset:736
	s_waitcnt lgkmcnt(1)
	v_mfma_f32_16x16x32_f16 v[130:133], v[22:25], v[18:21], v[130:133]
	v_mfma_f32_16x16x32_f16 v[214:217], v[6:9], v[18:21], v[66:69]
	ds_read_b128 v[18:21], v151 offset:1344
	s_nop 1
	ds_read_b128 v[66:69], v151 offset:1952
	s_waitcnt lgkmcnt(2)
	v_mfma_f32_16x16x32_f16 v[142:145], v[22:25], v[86:89], v[142:145]
	v_mfma_f32_16x16x32_f16 v[158:161], v[6:9], v[86:89], v[158:161]
	s_waitcnt lgkmcnt(1)
	v_mfma_f32_16x16x32_f16 v[222:225], v[22:25], v[18:21], v[62:65]
	v_mfma_f32_16x16x32_f16 v[178:181], v[6:9], v[18:21], v[178:181]
	s_waitcnt lgkmcnt(0)
	v_mfma_f32_16x16x32_f16 v[182:185], v[22:25], v[66:69], v[182:185]
	v_mfma_f32_16x16x32_f16 v[198:201], v[6:9], v[66:69], v[198:201]
	v_add_u32_e32 v18, 0x5ab00, v150
	v_min_u32_e32 v18, v18, v157
	global_load_dwordx4 v[86:89], v18, s[8:9] nt
	s_waitcnt vmcnt(21)
	v_cvt_pk_f16_f32 v19, v96, v97
	v_cvt_pk_f16_f32 v18, v94, v95
	ds_write_b16 v234, v18 offset:2432
	ds_write_b16_d16_hi v235, v18 offset:2432
	ds_write_b16 v236, v19 offset:2432
	ds_write_b16_d16_hi v237, v19 offset:2432
	ds_read_b128 v[18:21], v151 offset:2560
	ds_read_b128 v[62:65], v151 offset:3168
	s_waitcnt lgkmcnt(1)
	v_mfma_f32_16x16x32_f16 v[134:137], v[22:25], v[18:21], v[134:137]
	v_mfma_f32_16x16x32_f16 v[146:149], v[6:9], v[18:21], v[146:149]
	s_waitcnt lgkmcnt(0)
	v_mfma_f32_16x16x32_f16 v[206:209], v[22:25], v[62:65], v[206:209]
	v_mfma_f32_16x16x32_f16 v[122:125], v[6:9], v[62:65], v[122:125]
	ds_read_b128 v[18:21], v151 offset:3776
	ds_read_b128 v[62:65], v151 offset:4384
	s_waitcnt lgkmcnt(1)
	v_mfma_f32_16x16x32_f16 v[210:213], v[22:25], v[18:21], v[210:213]
	v_mfma_f32_16x16x32_f16 v[190:193], v[6:9], v[18:21], v[190:193]
	s_waitcnt lgkmcnt(0)
	v_mfma_f32_16x16x32_f16 v[166:169], v[22:25], v[62:65], v[166:169]
	v_mfma_f32_16x16x32_f16 v[162:165], v[6:9], v[62:65], v[162:165]
	v_add_u32_e32 v18, 0x71140, v244
	v_min_u32_e32 v18, v18, v157
	global_load_dwordx4 v[90:93], v18, s[8:9] nt
	s_waitcnt vmcnt(21)
	v_cvt_pk_f16_f32 v19, v100, v101
	v_cvt_pk_f16_f32 v18, v98, v99
	ds_write_b16 v238, v18 offset:3040
	ds_write_b16_d16_hi v239, v18 offset:3040
	ds_write_b16 v240, v19 offset:3040
	ds_write_b16_d16_hi v241, v19 offset:3040
	ds_read_b128 v[18:21], v151 offset:4992
	ds_read_b128 v[62:65], v151 offset:5600
	s_waitcnt lgkmcnt(1)
	v_mfma_f32_16x16x32_f16 v[98:101], v[22:25], v[18:21], v[138:141]
	v_mfma_f32_16x16x32_f16 v[138:141], v[6:9], v[18:21], v[170:173]
	s_waitcnt lgkmcnt(0)
	v_mfma_f32_16x16x32_f16 v[170:173], v[22:25], v[62:65], v[174:177]
	v_mfma_f32_16x16x32_f16 v[126:129], v[6:9], v[62:65], v[126:129]
	ds_read_b128 v[18:21], v151 offset:6208
	ds_read_b128 v[62:65], v151 offset:6816
	s_waitcnt lgkmcnt(1)
	v_mfma_f32_16x16x32_f16 v[174:177], v[22:25], v[18:21], v[218:221]
	v_mfma_f32_16x16x32_f16 v[194:197], v[6:9], v[18:21], v[194:197]
	s_waitcnt lgkmcnt(0)
	v_mfma_f32_16x16x32_f16 v[186:189], v[22:25], v[62:65], v[186:189]
	v_mfma_f32_16x16x32_f16 v[202:205], v[6:9], v[62:65], v[202:205]
	v_add_u32_e32 v18, 0x87780, v150
	v_min_u32_e32 v18, v18, v157
	global_load_dwordx4 v[94:97], v18, s[8:9] nt
	s_waitcnt vmcnt(21)
	v_cvt_pk_f16_f32 v19, v104, v105
	v_cvt_pk_f16_f32 v18, v102, v103
	ds_write_b16 v234, v18 offset:3648
	ds_write_b16_d16_hi v235, v18 offset:3648
	ds_write_b16 v236, v19 offset:3648
	ds_write_b16_d16_hi v237, v19 offset:3648
	ds_read_b128 v[102:105], v151 offset:7424
	s_mov_b32 s3, 0x88000
	v_add_co_u32_e32 v18, vcc, s3, v152
	s_mov_b32 s3, 0x8c000
	s_nop 0
	v_addc_co_u32_e32 v19, vcc, 0, v153, vcc
	global_load_dwordx4 v[62:65], v[18:19], off sc1
	global_load_dwordx4 v[66:69], v[18:19], off offset:256 sc1
	v_add_co_u32_e32 v18, vcc, s3, v152
	s_waitcnt lgkmcnt(0)
	v_mfma_f32_16x16x32_f16 v[22:25], v[22:25], v[102:105], v[30:33]
	v_addc_co_u32_e32 v19, vcc, 0, v153, vcc
	s_nop 1
	global_load_dwordx4 v[30:33], v[18:19], off sc1
	s_nop 0
	global_load_dwordx4 v[18:21], v[18:19], off offset:256 sc1
	v_mfma_f32_16x16x32_f16 v[38:41], v[6:9], v[102:105], v[38:41]
	ds_read_b128 v[6:9], v151 offset:192
	ds_read_b128 v[102:105], v151 offset:800
	s_waitcnt vmcnt(24) lgkmcnt(1)
	v_mfma_f32_16x16x32_f16 v[130:133], v[42:45], v[6:9], v[130:133]
	s_waitcnt vmcnt(23)
	v_mfma_f32_16x16x32_f16 v[214:217], v[58:61], v[6:9], v[214:217]
	ds_read_b128 v[6:9], v151 offset:1408
	s_waitcnt lgkmcnt(1)
	v_mfma_f32_16x16x32_f16 v[142:145], v[42:45], v[102:105], v[142:145]
	v_mfma_f32_16x16x32_f16 v[158:161], v[58:61], v[102:105], v[158:161]
	s_waitcnt lgkmcnt(0)
	v_mfma_f32_16x16x32_f16 v[218:221], v[42:45], v[6:9], v[222:225]
	v_mfma_f32_16x16x32_f16 v[178:181], v[58:61], v[6:9], v[178:181]
	v_add_u32_e32 v6, 0x9ddc0, v244
	v_min_u32_e32 v6, v6, v157
	global_load_dwordx4 v[6:9], v6, s[8:9] nt
	s_waitcnt vmcnt(21)
	v_cvt_pk_f16_f32 v5, v4, v5
	v_cvt_pk_f16_f32 v4, v2, v3
	ds_write_b16 v238, v4 offset:4256
	ds_write_b16_d16_hi v239, v4 offset:4256
	ds_write_b16 v240, v5 offset:4256
	ds_write_b16_d16_hi v241, v5 offset:4256
	ds_read_b128 v[2:5], v151 offset:2016
	ds_read_b128 v[102:105], v151 offset:2624
	s_waitcnt lgkmcnt(1)
	v_mfma_f32_16x16x32_f16 v[182:185], v[42:45], v[2:5], v[182:185]
	v_mfma_f32_16x16x32_f16 v[2:5], v[58:61], v[2:5], v[198:201]
	s_waitcnt lgkmcnt(0)
	v_mfma_f32_16x16x32_f16 v[134:137], v[42:45], v[102:105], v[134:137]
	v_mfma_f32_16x16x32_f16 v[146:149], v[58:61], v[102:105], v[146:149]
	ds_read_b128 v[102:105], v151 offset:3232
	ds_read_b128 v[198:201], v151 offset:3840
	s_waitcnt lgkmcnt(1)
	v_mfma_f32_16x16x32_f16 v[206:209], v[42:45], v[102:105], v[206:209]
	v_mfma_f32_16x16x32_f16 v[122:125], v[58:61], v[102:105], v[122:125]
	s_waitcnt lgkmcnt(0)
	v_mfma_f32_16x16x32_f16 v[210:213], v[42:45], v[198:201], v[210:213]
	v_mfma_f32_16x16x32_f16 v[190:193], v[58:61], v[198:201], v[190:193]
	v_add_u32_e32 v102, 0xb4400, v150
	v_min_u32_e32 v102, v102, v157
	global_load_dwordx4 v[102:105], v102, s[8:9] nt
	s_waitcnt vmcnt(21)
	v_cvt_pk_f16_f32 v109, v108, v109
	v_cvt_pk_f16_f32 v108, v106, v107
	ds_write_b16 v234, v108 offset:4864
	ds_write_b16_d16_hi v235, v108 offset:4864
	ds_write_b16 v236, v109 offset:4864
	ds_write_b16_d16_hi v237, v109 offset:4864
	ds_read_b128 v[106:109], v151 offset:4448
	ds_read_b128 v[198:201], v151 offset:6272
	s_waitcnt lgkmcnt(1)
	v_mfma_f32_16x16x32_f16 v[166:169], v[42:45], v[106:109], v[166:169]
	v_mfma_f32_16x16x32_f16 v[162:165], v[58:61], v[106:109], v[162:165]
	ds_read_b128 v[106:109], v151 offset:5056
	ds_read_b128 v[222:225], v151 offset:5664
	s_waitcnt lgkmcnt(1)
	v_mfma_f32_16x16x32_f16 v[98:101], v[42:45], v[106:109], v[98:101]
	v_mfma_f32_16x16x32_f16 v[138:141], v[58:61], v[106:109], v[138:141]
	s_waitcnt lgkmcnt(0)
	v_mfma_f32_16x16x32_f16 v[170:173], v[42:45], v[222:225], v[170:173]
	v_mfma_f32_16x16x32_f16 v[126:129], v[58:61], v[222:225], v[126:129]
	v_mfma_f32_16x16x32_f16 v[174:177], v[42:45], v[198:201], v[174:177]
	v_mfma_f32_16x16x32_f16 v[194:197], v[58:61], v[198:201], v[194:197]
	v_add_u32_e32 v106, 0xcaa40, v244
	v_min_u32_e32 v106, v106, v157
	global_load_dwordx4 v[106:109], v106, s[8:9] nt
	s_waitcnt vmcnt(21)
	v_cvt_pk_f16_f32 v117, v116, v117
	v_cvt_pk_f16_f32 v116, v114, v115
	ds_write_b16 v238, v116 offset:5472
	ds_write_b16_d16_hi v239, v116 offset:5472
	ds_write_b16 v240, v117 offset:5472
	ds_write_b16_d16_hi v241, v117 offset:5472
	ds_read_b128 v[114:117], v151 offset:6880
	ds_read_b128 v[198:201], v151 offset:7488
	s_waitcnt lgkmcnt(1)
	v_mfma_f32_16x16x32_f16 v[186:189], v[42:45], v[114:117], v[186:189]
	v_mfma_f32_16x16x32_f16 v[202:205], v[58:61], v[114:117], v[202:205]
	s_waitcnt lgkmcnt(0)
	v_mfma_f32_16x16x32_f16 v[22:25], v[42:45], v[198:201], v[22:25]
	v_mfma_f32_16x16x32_f16 v[58:61], v[58:61], v[198:201], v[38:41]
	s_nop 2
	ds_read_b128 v[38:41], v151 offset:256
	ds_read_b128 v[42:45], v151 offset:864
	s_waitcnt lgkmcnt(1)
	v_mfma_f32_16x16x32_f16 v[130:133], v[34:37], v[38:41], v[130:133]
	v_mfma_f32_16x16x32_f16 v[198:201], v[14:17], v[38:41], v[214:217]
	s_waitcnt lgkmcnt(0)
	v_mfma_f32_16x16x32_f16 v[142:145], v[34:37], v[42:45], v[142:145]
	v_mfma_f32_16x16x32_f16 v[158:161], v[14:17], v[42:45], v[158:161]
	v_add_u32_e32 v38, 0xe1080, v150
	v_min_u32_e32 v38, v38, v157
	global_load_dwordx4 v[114:117], v38, s[8:9] nt
	s_waitcnt vmcnt(21)
	v_cvt_pk_f16_f32 v39, v112, v113
	v_cvt_pk_f16_f32 v38, v110, v111
	ds_write_b16 v234, v38 offset:6080
	ds_write_b16_d16_hi v235, v38 offset:6080
	ds_write_b16 v236, v39 offset:6080
	ds_write_b16_d16_hi v237, v39 offset:6080
	ds_read_b128 v[38:41], v151 offset:1472
	ds_read_b128 v[42:45], v151 offset:2080
	s_waitcnt lgkmcnt(1)
	v_mfma_f32_16x16x32_f16 v[214:217], v[34:37], v[38:41], v[218:221]
	v_mfma_f32_16x16x32_f16 v[178:181], v[14:17], v[38:41], v[178:181]
	s_waitcnt lgkmcnt(0)
	v_mfma_f32_16x16x32_f16 v[218:221], v[14:17], v[42:45], v[2:5]
	s_nop 2
	ds_read_b128 v[2:5], v151 offset:2688
	ds_read_b128 v[38:41], v151 offset:3296
	v_mfma_f32_16x16x32_f16 v[182:185], v[34:37], v[42:45], v[182:185]
	s_waitcnt lgkmcnt(1)
	v_mfma_f32_16x16x32_f16 v[134:137], v[34:37], v[2:5], v[134:137]
	v_mfma_f32_16x16x32_f16 v[146:149], v[14:17], v[2:5], v[146:149]
	s_waitcnt lgkmcnt(0)
	v_mfma_f32_16x16x32_f16 v[206:209], v[34:37], v[38:41], v[206:209]
	v_mfma_f32_16x16x32_f16 v[122:125], v[14:17], v[38:41], v[122:125]
	v_add_u32_e32 v2, 0xf76c0, v244
	v_min_u32_e32 v2, v2, v157
	global_load_dwordx4 v[110:113], v2, s[8:9] nt
	s_waitcnt vmcnt(21)
	v_cvt_pk_f16_f32 v3, v120, v121
	v_cvt_pk_f16_f32 v2, v118, v119
	ds_write_b16 v238, v2 offset:6688
	ds_write_b16_d16_hi v239, v2 offset:6688
	ds_write_b16 v240, v3 offset:6688
	ds_write_b16_d16_hi v241, v3 offset:6688
	ds_read_b128 v[2:5], v151 offset:3904
	ds_read_b128 v[38:41], v151 offset:4512
	s_waitcnt lgkmcnt(1)
	v_mfma_f32_16x16x32_f16 v[210:213], v[34:37], v[2:5], v[210:213]
	v_mfma_f32_16x16x32_f16 v[190:193], v[14:17], v[2:5], v[190:193]
	s_waitcnt lgkmcnt(0)
	v_mfma_f32_16x16x32_f16 v[166:169], v[34:37], v[38:41], v[166:169]
	v_mfma_f32_16x16x32_f16 v[162:165], v[14:17], v[38:41], v[162:165]
	ds_read_b128 v[2:5], v151 offset:5120
	ds_read_b128 v[38:41], v151 offset:5728
	s_waitcnt lgkmcnt(1)
	v_mfma_f32_16x16x32_f16 v[98:101], v[34:37], v[2:5], v[98:101]
	v_mfma_f32_16x16x32_f16 v[138:141], v[14:17], v[2:5], v[138:141]
	s_waitcnt lgkmcnt(0)
	v_mfma_f32_16x16x32_f16 v[170:173], v[34:37], v[38:41], v[170:173]
	v_mfma_f32_16x16x32_f16 v[126:129], v[14:17], v[38:41], v[126:129]
	v_add_u32_e32 v2, 0x10dd00, v150
	v_min_u32_e32 v2, v2, v157
	v_cndmask_b32_e64 v2, 0, v2, s[0:1]
	global_load_dwordx4 v[118:121], v2, s[8:9] nt
	s_waitcnt vmcnt(21)
	v_cvt_pk_f16_f32 v3, v72, v73
	v_cvt_pk_f16_f32 v2, v70, v71
	ds_write_b16 v234, v2 offset:7296
	ds_write_b16_d16_hi v235, v2 offset:7296
	ds_write_b16 v236, v3 offset:7296
	ds_write_b16_d16_hi v237, v3 offset:7296
	ds_read_b128 v[2:5], v151 offset:6336
	ds_read_b128 v[38:41], v151 offset:6944
	ds_read_b128 v[70:73], v151 offset:7552
	s_mov_b32 s3, 0x90000
	s_waitcnt lgkmcnt(0)
	v_mfma_f32_16x16x32_f16 v[174:177], v[34:37], v[2:5], v[174:177]
	s_barrier
	v_sub_u32_e32 v245, v234, v243
	v_add_u32_e32 v246, 0xfffffdc0, v245
	v_min_u32_e32 v245, v245, v246
	v_add_u32_e32 v234, v242, v245
	v_sub_u32_e32 v245, v235, v243
	v_add_u32_e32 v246, 0xfffffdc0, v245
	v_min_u32_e32 v245, v245, v246
	v_add_u32_e32 v235, v242, v245
	v_sub_u32_e32 v245, v236, v243
	v_add_u32_e32 v246, 0xfffffdc0, v245
	v_min_u32_e32 v245, v245, v246
	v_add_u32_e32 v236, v242, v245
	v_sub_u32_e32 v245, v237, v243
	v_add_u32_e32 v246, 0xfffffdc0, v245
	v_min_u32_e32 v245, v245, v246
	v_add_u32_e32 v237, v242, v245
	v_sub_u32_e32 v245, v238, v243
	v_add_u32_e32 v246, 0xfffffdc0, v245
	v_min_u32_e32 v245, v245, v246
	v_add_u32_e32 v238, v242, v245
	v_sub_u32_e32 v245, v239, v243
	v_add_u32_e32 v246, 0xfffffdc0, v245
	v_min_u32_e32 v245, v245, v246
	v_add_u32_e32 v239, v242, v245
	v_sub_u32_e32 v245, v240, v243
	v_add_u32_e32 v246, 0xfffffdc0, v245
	v_min_u32_e32 v245, v245, v246
	v_add_u32_e32 v240, v242, v245
	v_sub_u32_e32 v245, v241, v243
	v_add_u32_e32 v246, 0xfffffdc0, v245
	v_min_u32_e32 v245, v245, v246
	v_add_u32_e32 v241, v242, v245
	v_mfma_f32_16x16x32_f16 v[194:197], v[14:17], v[2:5], v[194:197]
	v_add_co_u32_e32 v2, vcc, s3, v152
	s_mov_b32 s3, 0x94000
	s_nop 0
	v_addc_co_u32_e32 v3, vcc, 0, v153, vcc
	v_mfma_f32_16x16x32_f16 v[186:189], v[34:37], v[38:41], v[186:189]
	v_mfma_f32_16x16x32_f16 v[202:205], v[14:17], v[38:41], v[202:205]
	global_load_dwordx4 v[38:41], v[2:3], off sc1
	global_load_dwordx4 v[42:45], v[2:3], off offset:256 sc1
	v_add_co_u32_e32 v2, vcc, s3, v152
	v_mfma_f32_16x16x32_f16 v[34:37], v[34:37], v[70:73], v[22:25]
	s_nop 0
	v_addc_co_u32_e32 v3, vcc, 0, v153, vcc
	s_nop 0
	global_load_dwordx4 v[22:25], v[2:3], off sc1
	s_nop 0
	global_load_dwordx4 v[2:5], v[2:3], off offset:256 sc1
	v_mfma_f32_16x16x32_f16 v[14:17], v[14:17], v[70:73], v[58:61]
	v_add_u32_e32 v157, 0x111528dc, v154
	s_nop 1
	ds_read_b128 v[58:61], v151 offset:320
	v_add_u32_e32 v70, 0x1400, v150
	s_waitcnt vmcnt(24) lgkmcnt(0)
	v_mfma_f32_16x16x32_f16 v[130:133], v[46:49], v[58:61], v[130:133]
	s_waitcnt vmcnt(23)
	v_mfma_f32_16x16x32_f16 v[198:201], v[54:57], v[58:61], v[198:201]
	v_min_u32_e32 v58, v70, v157
	global_load_dwordx4 v[58:61], v58, s[8:9] nt
	s_waitcnt vmcnt(21)
	v_cvt_pk_f16_f32 v71, v76, v77
	v_cvt_pk_f16_f32 v70, v74, v75
	ds_write_b16 v234, v70 offset:0
	ds_write_b16_d16_hi v235, v70 offset:0
	ds_write_b16 v236, v71 offset:0
	ds_write_b16_d16_hi v237, v71 offset:0
	ds_read_b128 v[70:73], v151 offset:928
	ds_read_b128 v[74:77], v151 offset:1536
	s_waitcnt lgkmcnt(1)
	v_mfma_f32_16x16x32_f16 v[142:145], v[46:49], v[70:73], v[142:145]
	v_mfma_f32_16x16x32_f16 v[158:161], v[54:57], v[70:73], v[158:161]
	s_waitcnt lgkmcnt(0)
	v_mfma_f32_16x16x32_f16 v[214:217], v[46:49], v[74:77], v[214:217]
	v_mfma_f32_16x16x32_f16 v[178:181], v[54:57], v[74:77], v[178:181]
	ds_read_b128 v[70:73], v151 offset:2144
	ds_read_b128 v[74:77], v151 offset:2752
	s_waitcnt lgkmcnt(1)
	v_mfma_f32_16x16x32_f16 v[182:185], v[46:49], v[70:73], v[182:185]
	v_mfma_f32_16x16x32_f16 v[218:221], v[54:57], v[70:73], v[218:221]
	s_waitcnt lgkmcnt(0)
	v_mfma_f32_16x16x32_f16 v[134:137], v[46:49], v[74:77], v[134:137]
	v_mfma_f32_16x16x32_f16 v[146:149], v[54:57], v[74:77], v[146:149]
	v_add_u32_e32 v70, 0x17a40, v244
	v_min_u32_e32 v70, v70, v157
	global_load_dwordx4 v[70:73], v70, s[8:9] nt
	s_waitcnt vmcnt(21)
	v_cvt_pk_f16_f32 v75, v80, v81
	v_cvt_pk_f16_f32 v74, v78, v79
	ds_write_b16 v238, v74 offset:608
	ds_write_b16_d16_hi v239, v74 offset:608
	ds_write_b16 v240, v75 offset:608
	ds_write_b16_d16_hi v241, v75 offset:608
	ds_read_b128 v[74:77], v151 offset:3360
	ds_read_b128 v[78:81], v151 offset:5184
	s_waitcnt lgkmcnt(1)
	v_mfma_f32_16x16x32_f16 v[206:209], v[46:49], v[74:77], v[206:209]
	v_mfma_f32_16x16x32_f16 v[122:125], v[54:57], v[74:77], v[122:125]
	ds_read_b128 v[74:77], v151 offset:3968
	ds_read_b128 v[222:225], v151 offset:4576
	s_waitcnt lgkmcnt(1)
	v_mfma_f32_16x16x32_f16 v[210:213], v[46:49], v[74:77], v[210:213]
	v_mfma_f32_16x16x32_f16 v[190:193], v[54:57], v[74:77], v[190:193]
	s_waitcnt lgkmcnt(0)
	v_mfma_f32_16x16x32_f16 v[166:169], v[46:49], v[222:225], v[166:169]
	v_mfma_f32_16x16x32_f16 v[162:165], v[54:57], v[222:225], v[162:165]
	v_mfma_f32_16x16x32_f16 v[98:101], v[46:49], v[78:81], v[98:101]
	v_mfma_f32_16x16x32_f16 v[138:141], v[54:57], v[78:81], v[138:141]
	v_add_u32_e32 v74, 0x2e080, v150
	v_min_u32_e32 v74, v74, v157
	global_load_dwordx4 v[74:77], v74, s[8:9] nt
	s_waitcnt vmcnt(21)
	v_cvt_pk_f16_f32 v79, v84, v85
	v_cvt_pk_f16_f32 v78, v82, v83
	ds_write_b16 v234, v78 offset:1216
	ds_write_b16_d16_hi v235, v78 offset:1216
	ds_write_b16 v236, v79 offset:1216
	ds_write_b16_d16_hi v237, v79 offset:1216
	ds_read_b128 v[78:81], v151 offset:5792
	ds_read_b128 v[82:85], v151 offset:6400
	s_waitcnt lgkmcnt(1)
	v_mfma_f32_16x16x32_f16 v[170:173], v[46:49], v[78:81], v[170:173]
	v_mfma_f32_16x16x32_f16 v[126:129], v[54:57], v[78:81], v[126:129]
	s_waitcnt lgkmcnt(0)
	v_mfma_f32_16x16x32_f16 v[174:177], v[46:49], v[82:85], v[174:177]
	v_mfma_f32_16x16x32_f16 v[194:197], v[54:57], v[82:85], v[194:197]
	ds_read_b128 v[78:81], v151 offset:7008
	ds_read_b128 v[82:85], v151 offset:7616
	s_waitcnt lgkmcnt(1)
	v_mfma_f32_16x16x32_f16 v[186:189], v[46:49], v[78:81], v[186:189]
	v_mfma_f32_16x16x32_f16 v[202:205], v[54:57], v[78:81], v[202:205]
	s_waitcnt lgkmcnt(0)
	v_mfma_f32_16x16x32_f16 v[34:37], v[46:49], v[82:85], v[34:37]
	v_mfma_f32_16x16x32_f16 v[46:49], v[54:57], v[82:85], v[14:17]
	s_nop 2
	v_add_u32_e32 v14, 0x446c0, v244
	v_min_u32_e32 v14, v14, v157
	global_load_dwordx4 v[78:81], v14, s[8:9] nt
	s_waitcnt vmcnt(21)
	v_cvt_pk_f16_f32 v15, v52, v53
	v_cvt_pk_f16_f32 v14, v50, v51
	ds_write_b16 v238, v14 offset:1824
	ds_write_b16_d16_hi v239, v14 offset:1824
	ds_write_b16 v240, v15 offset:1824
	ds_write_b16_d16_hi v241, v15 offset:1824
	ds_read_b128 v[14:17], v151 offset:384
	ds_read_b128 v[50:53], v151 offset:992
	s_waitcnt lgkmcnt(1)
	v_mfma_f32_16x16x32_f16 v[130:133], v[26:29], v[14:17], v[130:133]
	v_mfma_f32_16x16x32_f16 v[198:201], v[10:13], v[14:17], v[198:201]
	s_waitcnt lgkmcnt(0)
	v_mfma_f32_16x16x32_f16 v[142:145], v[26:29], v[50:53], v[142:145]
	v_mfma_f32_16x16x32_f16 v[158:161], v[10:13], v[50:53], v[158:161]
	ds_read_b128 v[14:17], v151 offset:1600
	ds_read_b128 v[50:53], v151 offset:2208
	s_waitcnt lgkmcnt(1)
	v_mfma_f32_16x16x32_f16 v[214:217], v[26:29], v[14:17], v[214:217]
	v_mfma_f32_16x16x32_f16 v[178:181], v[10:13], v[14:17], v[178:181]
	s_waitcnt lgkmcnt(0)
	v_mfma_f32_16x16x32_f16 v[182:185], v[26:29], v[50:53], v[182:185]
	v_mfma_f32_16x16x32_f16 v[218:221], v[10:13], v[50:53], v[218:221]
	v_add_u32_e32 v14, 0x5ad00, v150
	v_min_u32_e32 v14, v14, v157
	global_load_dwordx4 v[82:85], v14, s[8:9] nt
	s_waitcnt vmcnt(21)
	v_cvt_pk_f16_f32 v15, v88, v89
	v_cvt_pk_f16_f32 v14, v86, v87
	ds_write_b16 v234, v14 offset:2432
	ds_write_b16_d16_hi v235, v14 offset:2432
	ds_write_b16 v236, v15 offset:2432
	ds_write_b16_d16_hi v237, v15 offset:2432
	ds_read_b128 v[14:17], v151 offset:2816
	ds_read_b128 v[50:53], v151 offset:3424
	s_waitcnt lgkmcnt(1)
	v_mfma_f32_16x16x32_f16 v[134:137], v[26:29], v[14:17], v[134:137]
	v_mfma_f32_16x16x32_f16 v[146:149], v[10:13], v[14:17], v[146:149]
	s_waitcnt lgkmcnt(0)
	v_mfma_f32_16x16x32_f16 v[206:209], v[26:29], v[50:53], v[206:209]
	v_mfma_f32_16x16x32_f16 v[122:125], v[10:13], v[50:53], v[122:125]
	ds_read_b128 v[14:17], v151 offset:4032
	ds_read_b128 v[50:53], v151 offset:4640
	s_waitcnt lgkmcnt(1)
	v_mfma_f32_16x16x32_f16 v[210:213], v[26:29], v[14:17], v[210:213]
	v_mfma_f32_16x16x32_f16 v[190:193], v[10:13], v[14:17], v[190:193]
	s_waitcnt lgkmcnt(0)
	v_mfma_f32_16x16x32_f16 v[166:169], v[26:29], v[50:53], v[166:169]
	v_mfma_f32_16x16x32_f16 v[162:165], v[10:13], v[50:53], v[162:165]
	v_add_u32_e32 v14, 0x71340, v244
	v_min_u32_e32 v14, v14, v157
	global_load_dwordx4 v[86:89], v14, s[8:9] nt
	s_waitcnt vmcnt(21)
	v_cvt_pk_f16_f32 v15, v92, v93
	v_cvt_pk_f16_f32 v14, v90, v91
	ds_write_b16 v238, v14 offset:3040
	ds_write_b16_d16_hi v239, v14 offset:3040
	ds_write_b16 v240, v15 offset:3040
	ds_write_b16_d16_hi v241, v15 offset:3040
	ds_read_b128 v[14:17], v151 offset:5248
	ds_read_b128 v[50:53], v151 offset:5856
	s_waitcnt lgkmcnt(1)
	v_mfma_f32_16x16x32_f16 v[222:225], v[26:29], v[14:17], v[98:101]
	v_mfma_f32_16x16x32_f16 v[138:141], v[10:13], v[14:17], v[138:141]
	s_waitcnt lgkmcnt(0)
	v_mfma_f32_16x16x32_f16 v[170:173], v[26:29], v[50:53], v[170:173]
	v_mfma_f32_16x16x32_f16 v[126:129], v[10:13], v[50:53], v[126:129]
	ds_read_b128 v[14:17], v151 offset:6464
	ds_read_b128 v[50:53], v151 offset:7072
	s_waitcnt lgkmcnt(1)
	v_mfma_f32_16x16x32_f16 v[174:177], v[26:29], v[14:17], v[174:177]
	v_mfma_f32_16x16x32_f16 v[194:197], v[10:13], v[14:17], v[194:197]
	s_waitcnt lgkmcnt(0)
	v_mfma_f32_16x16x32_f16 v[186:189], v[26:29], v[50:53], v[186:189]
	v_mfma_f32_16x16x32_f16 v[202:205], v[10:13], v[50:53], v[202:205]
	v_add_u32_e32 v14, 0x87980, v150
	v_min_u32_e32 v14, v14, v157
	global_load_dwordx4 v[90:93], v14, s[8:9] nt
	s_waitcnt vmcnt(21)
	v_cvt_pk_f16_f32 v15, v96, v97
	v_cvt_pk_f16_f32 v14, v94, v95
	ds_write_b16 v234, v14 offset:3648
	ds_write_b16_d16_hi v235, v14 offset:3648
	ds_write_b16 v236, v15 offset:3648
	ds_write_b16_d16_hi v237, v15 offset:3648
	ds_read_b128 v[94:97], v151 offset:7680
	s_mov_b32 s3, 0x98000
	v_add_co_u32_e32 v14, vcc, s3, v152
	s_mov_b32 s3, 0x9c000
	s_nop 0
	v_addc_co_u32_e32 v15, vcc, 0, v153, vcc
	global_load_dwordx4 v[50:53], v[14:15], off sc1
	global_load_dwordx4 v[54:57], v[14:15], off offset:256 sc1
	v_add_co_u32_e32 v14, vcc, s3, v152
	s_waitcnt lgkmcnt(0)
	v_mfma_f32_16x16x32_f16 v[34:37], v[26:29], v[94:97], v[34:37]
	v_addc_co_u32_e32 v15, vcc, 0, v153, vcc
	global_load_dwordx4 v[26:29], v[14:15], off sc1
	s_nop 0
	global_load_dwordx4 v[14:17], v[14:15], off offset:256 sc1
	v_mfma_f32_16x16x32_f16 v[10:13], v[10:13], v[94:97], v[46:49]
	s_nop 2
	ds_read_b128 v[46:49], v151 offset:448
	ds_read_b128 v[94:97], v151 offset:1056
	s_waitcnt vmcnt(24) lgkmcnt(1)
	v_mfma_f32_16x16x32_f16 v[130:133], v[62:65], v[46:49], v[130:133]
	s_waitcnt lgkmcnt(0)
	v_mfma_f32_16x16x32_f16 v[142:145], v[62:65], v[94:97], v[142:145]
	s_waitcnt vmcnt(23)
	v_mfma_f32_16x16x32_f16 v[158:161], v[66:69], v[94:97], v[158:161]
	ds_read_b128 v[94:97], v151 offset:1664
	v_mfma_f32_16x16x32_f16 v[46:49], v[66:69], v[46:49], v[198:201]
	s_waitcnt lgkmcnt(0)
	v_mfma_f32_16x16x32_f16 v[198:201], v[62:65], v[94:97], v[214:217]
	v_mfma_f32_16x16x32_f16 v[178:181], v[66:69], v[94:97], v[178:181]
	v_add_u32_e32 v94, 0x9dfc0, v244
	v_min_u32_e32 v94, v94, v157
	global_load_dwordx4 v[94:97], v94, s[8:9] nt
	s_waitcnt vmcnt(21)
	v_cvt_pk_f16_f32 v9, v8, v9
	v_cvt_pk_f16_f32 v8, v6, v7
	ds_write_b16 v238, v8 offset:4256
	ds_write_b16_d16_hi v239, v8 offset:4256
	ds_write_b16 v240, v9 offset:4256
	ds_write_b16_d16_hi v241, v9 offset:4256
	ds_read_b128 v[6:9], v151 offset:2272
	ds_read_b128 v[98:101], v151 offset:2880
	s_waitcnt lgkmcnt(1)
	v_mfma_f32_16x16x32_f16 v[182:185], v[62:65], v[6:9], v[182:185]
	s_waitcnt lgkmcnt(0)
	v_mfma_f32_16x16x32_f16 v[134:137], v[62:65], v[98:101], v[134:137]
	v_mfma_f32_16x16x32_f16 v[146:149], v[66:69], v[98:101], v[146:149]
	ds_read_b128 v[98:101], v151 offset:3488
	ds_read_b128 v[214:217], v151 offset:4096
	v_mfma_f32_16x16x32_f16 v[6:9], v[66:69], v[6:9], v[218:221]
	s_waitcnt lgkmcnt(1)
	v_mfma_f32_16x16x32_f16 v[206:209], v[62:65], v[98:101], v[206:209]
	v_mfma_f32_16x16x32_f16 v[122:125], v[66:69], v[98:101], v[122:125]
	s_waitcnt lgkmcnt(0)
	v_mfma_f32_16x16x32_f16 v[210:213], v[62:65], v[214:217], v[210:213]
	v_mfma_f32_16x16x32_f16 v[190:193], v[66:69], v[214:217], v[190:193]
	v_add_u32_e32 v98, 0xb4600, v150
	v_min_u32_e32 v98, v98, v157
	global_load_dwordx4 v[98:101], v98, s[8:9] nt
	s_waitcnt vmcnt(21)
	v_cvt_pk_f16_f32 v105, v104, v105
	v_cvt_pk_f16_f32 v104, v102, v103
	ds_write_b16 v234, v104 offset:4864
	ds_write_b16_d16_hi v235, v104 offset:4864
	ds_write_b16 v236, v105 offset:4864
	ds_write_b16_d16_hi v237, v105 offset:4864
	ds_read_b128 v[102:105], v151 offset:4704
	ds_read_b128 v[214:217], v151 offset:6528
	s_waitcnt lgkmcnt(1)
	v_mfma_f32_16x16x32_f16 v[166:169], v[62:65], v[102:105], v[166:169]
	v_mfma_f32_16x16x32_f16 v[162:165], v[66:69], v[102:105], v[162:165]
	ds_read_b128 v[102:105], v151 offset:5312
	ds_read_b128 v[218:221], v151 offset:5920
	s_waitcnt lgkmcnt(1)
	v_mfma_f32_16x16x32_f16 v[222:225], v[62:65], v[102:105], v[222:225]
	v_mfma_f32_16x16x32_f16 v[138:141], v[66:69], v[102:105], v[138:141]
	s_waitcnt lgkmcnt(0)
	v_mfma_f32_16x16x32_f16 v[170:173], v[62:65], v[218:221], v[170:173]
	v_mfma_f32_16x16x32_f16 v[126:129], v[66:69], v[218:221], v[126:129]
	v_mfma_f32_16x16x32_f16 v[174:177], v[62:65], v[214:217], v[174:177]
	v_mfma_f32_16x16x32_f16 v[194:197], v[66:69], v[214:217], v[194:197]
	v_add_u32_e32 v102, 0xcac40, v244
	v_min_u32_e32 v102, v102, v157
	global_load_dwordx4 v[102:105], v102, s[8:9] nt
	s_waitcnt vmcnt(21)
	v_cvt_pk_f16_f32 v109, v108, v109
	v_cvt_pk_f16_f32 v108, v106, v107
	ds_write_b16 v238, v108 offset:5472
	ds_write_b16_d16_hi v239, v108 offset:5472
	ds_write_b16 v240, v109 offset:5472
	ds_write_b16_d16_hi v241, v109 offset:5472
	ds_read_b128 v[106:109], v151 offset:7136
	ds_read_b128 v[214:217], v151 offset:7744
	s_waitcnt lgkmcnt(1)
	v_mfma_f32_16x16x32_f16 v[186:189], v[62:65], v[106:109], v[186:189]
	s_waitcnt lgkmcnt(0)
	v_mfma_f32_16x16x32_f16 v[218:221], v[62:65], v[214:217], v[34:37]
	v_mfma_f32_16x16x32_f16 v[214:217], v[66:69], v[214:217], v[10:13]
	s_nop 2
	ds_read_b128 v[10:13], v151 offset:512
	ds_read_b128 v[34:37], v151 offset:1120
	v_mfma_f32_16x16x32_f16 v[202:205], v[66:69], v[106:109], v[202:205]
	s_waitcnt lgkmcnt(1)
	v_mfma_f32_16x16x32_f16 v[130:133], v[30:33], v[10:13], v[130:133]
	v_mfma_f32_16x16x32_f16 v[226:229], v[18:21], v[10:13], v[46:49]
	s_waitcnt lgkmcnt(0)
	v_mfma_f32_16x16x32_f16 v[142:145], v[30:33], v[34:37], v[142:145]
	v_mfma_f32_16x16x32_f16 v[158:161], v[18:21], v[34:37], v[158:161]
	v_add_u32_e32 v10, 0xe1280, v150
	v_min_u32_e32 v10, v10, v157
	global_load_dwordx4 v[62:65], v10, s[8:9] nt
	s_waitcnt vmcnt(21)
	v_cvt_pk_f16_f32 v11, v116, v117
	v_cvt_pk_f16_f32 v10, v114, v115
	ds_write_b16 v234, v10 offset:6080
	ds_write_b16_d16_hi v235, v10 offset:6080
	ds_write_b16 v236, v11 offset:6080
	ds_write_b16_d16_hi v237, v11 offset:6080
	ds_read_b128 v[10:13], v151 offset:1728
	ds_read_b128 v[34:37], v151 offset:2336
	s_waitcnt lgkmcnt(1)
	v_mfma_f32_16x16x32_f16 v[114:117], v[30:33], v[10:13], v[198:201]
	v_mfma_f32_16x16x32_f16 v[178:181], v[18:21], v[10:13], v[178:181]
	s_waitcnt lgkmcnt(0)
	v_mfma_f32_16x16x32_f16 v[198:201], v[18:21], v[34:37], v[6:9]
	s_nop 2
	ds_read_b128 v[6:9], v151 offset:2944
	ds_read_b128 v[10:13], v151 offset:3552
	v_mfma_f32_16x16x32_f16 v[182:185], v[30:33], v[34:37], v[182:185]
	s_waitcnt lgkmcnt(1)
	v_mfma_f32_16x16x32_f16 v[134:137], v[30:33], v[6:9], v[134:137]
	v_mfma_f32_16x16x32_f16 v[146:149], v[18:21], v[6:9], v[146:149]
	s_waitcnt lgkmcnt(0)
	v_mfma_f32_16x16x32_f16 v[206:209], v[30:33], v[10:13], v[206:209]
	v_mfma_f32_16x16x32_f16 v[122:125], v[18:21], v[10:13], v[122:125]
	v_add_u32_e32 v6, 0xf78c0, v244
	v_min_u32_e32 v6, v6, v157
	global_load_dwordx4 v[66:69], v6, s[8:9] nt
	s_waitcnt vmcnt(21)
	v_cvt_pk_f16_f32 v7, v112, v113
	v_cvt_pk_f16_f32 v6, v110, v111
	ds_write_b16 v238, v6 offset:6688
	ds_write_b16_d16_hi v239, v6 offset:6688
	ds_write_b16 v240, v7 offset:6688
	ds_write_b16_d16_hi v241, v7 offset:6688
	ds_read_b128 v[6:9], v151 offset:4160
	ds_read_b128 v[10:13], v151 offset:4768
	s_waitcnt lgkmcnt(1)
	v_mfma_f32_16x16x32_f16 v[210:213], v[30:33], v[6:9], v[210:213]
	v_mfma_f32_16x16x32_f16 v[190:193], v[18:21], v[6:9], v[190:193]
	s_waitcnt lgkmcnt(0)
	v_mfma_f32_16x16x32_f16 v[166:169], v[30:33], v[10:13], v[166:169]
	v_mfma_f32_16x16x32_f16 v[162:165], v[18:21], v[10:13], v[162:165]
	ds_read_b128 v[6:9], v151 offset:5376
	ds_read_b128 v[10:13], v151 offset:5984
	s_waitcnt lgkmcnt(1)
	v_mfma_f32_16x16x32_f16 v[222:225], v[30:33], v[6:9], v[222:225]
	v_mfma_f32_16x16x32_f16 v[138:141], v[18:21], v[6:9], v[138:141]
	s_waitcnt lgkmcnt(0)
	v_mfma_f32_16x16x32_f16 v[170:173], v[30:33], v[10:13], v[170:173]
	v_mfma_f32_16x16x32_f16 v[126:129], v[18:21], v[10:13], v[126:129]
	v_add_u32_e32 v6, 0x10df00, v150
	v_min_u32_e32 v6, v6, v157
	v_cndmask_b32_e64 v6, 0, v6, s[0:1]
	global_load_dwordx4 v[106:109], v6, s[8:9] nt
	s_waitcnt vmcnt(21)
	v_cvt_pk_f16_f32 v7, v120, v121
	v_cvt_pk_f16_f32 v6, v118, v119
	ds_write_b16 v234, v6 offset:7296
	ds_write_b16_d16_hi v235, v6 offset:7296
	ds_write_b16 v236, v7 offset:7296
	ds_write_b16_d16_hi v237, v7 offset:7296
	ds_read_b128 v[6:9], v151 offset:6592
	ds_read_b128 v[10:13], v151 offset:7200
	s_mov_b32 s3, 0xa0000
	ds_read_b128 v[110:113], v151 offset:7808
	s_waitcnt lgkmcnt(0)
	v_mfma_f32_16x16x32_f16 v[118:121], v[30:33], v[6:9], v[174:177]
	s_barrier
	v_sub_u32_e32 v245, v234, v243
	v_add_u32_e32 v246, 0xfffffdc0, v245
	v_min_u32_e32 v245, v245, v246
	v_add_u32_e32 v234, v242, v245
	v_sub_u32_e32 v245, v235, v243
	v_add_u32_e32 v246, 0xfffffdc0, v245
	v_min_u32_e32 v245, v245, v246
	v_add_u32_e32 v235, v242, v245
	v_sub_u32_e32 v245, v236, v243
	v_add_u32_e32 v246, 0xfffffdc0, v245
	v_min_u32_e32 v245, v245, v246
	v_add_u32_e32 v236, v242, v245
	v_sub_u32_e32 v245, v237, v243
	v_add_u32_e32 v246, 0xfffffdc0, v245
	v_min_u32_e32 v245, v245, v246
	v_add_u32_e32 v237, v242, v245
	v_sub_u32_e32 v245, v238, v243
	v_add_u32_e32 v246, 0xfffffdc0, v245
	v_min_u32_e32 v245, v245, v246
	v_add_u32_e32 v238, v242, v245
	v_sub_u32_e32 v245, v239, v243
	v_add_u32_e32 v246, 0xfffffdc0, v245
	v_min_u32_e32 v245, v245, v246
	v_add_u32_e32 v239, v242, v245
	v_sub_u32_e32 v245, v240, v243
	v_add_u32_e32 v246, 0xfffffdc0, v245
	v_min_u32_e32 v245, v245, v246
	v_add_u32_e32 v240, v242, v245
	v_sub_u32_e32 v245, v241, v243
	v_add_u32_e32 v246, 0xfffffdc0, v245
	v_min_u32_e32 v245, v245, v246
	v_add_u32_e32 v241, v242, v245
	v_mfma_f32_16x16x32_f16 v[174:177], v[18:21], v[6:9], v[194:197]
	v_add_co_u32_e32 v6, vcc, s3, v152
	s_mov_b32 s3, 0xa4000
	s_nop 0
	v_addc_co_u32_e32 v7, vcc, 0, v153, vcc
	global_load_dwordx4 v[34:37], v[6:7], off sc1
	global_load_dwordx4 v[46:49], v[6:7], off offset:256 sc1
	v_add_co_u32_e32 v6, vcc, s3, v152
	v_mfma_f32_16x16x32_f16 v[186:189], v[30:33], v[10:13], v[186:189]
	s_nop 0
	v_addc_co_u32_e32 v7, vcc, 0, v153, vcc
	v_mfma_f32_16x16x32_f16 v[194:197], v[18:21], v[10:13], v[202:205]
	global_load_dwordx4 v[10:13], v[6:7], off sc1
	s_nop 0
	global_load_dwordx4 v[6:9], v[6:7], off offset:256 sc1
	v_mfma_f32_16x16x32_f16 v[30:33], v[30:33], v[110:113], v[218:221]
	v_mfma_f32_16x16x32_f16 v[18:21], v[18:21], v[110:113], v[214:217]
	v_min_u32_e32 v110, 0x54, v154
	v_add_u32_e32 v154, 0x11152adc, v110
	ds_read_b128 v[110:113], v151 offset:0
	v_add_u32_e32 v157, 0x1600, v250
	s_waitcnt vmcnt(24) lgkmcnt(0)
	v_mfma_f32_16x16x32_f16 v[130:133], v[38:41], v[110:113], v[130:133]
	s_waitcnt vmcnt(23)
	v_mfma_f32_16x16x32_f16 v[202:205], v[42:45], v[110:113], v[226:229]
	v_min_u32_e32 v110, v157, v154
	global_load_dwordx4 v[110:113], v110, s[8:9] nt
	s_waitcnt vmcnt(21)
	v_cvt_pk_f16_f32 v61, v60, v61
	v_cvt_pk_f16_f32 v60, v58, v59
	ds_write_b16 v234, v60 offset:0
	ds_write_b16_d16_hi v235, v60 offset:0
	ds_write_b16 v236, v61 offset:0
	ds_write_b16_d16_hi v237, v61 offset:0
	ds_read_b128 v[58:61], v151 offset:608
	ds_read_b128 v[214:217], v151 offset:1216
	s_waitcnt lgkmcnt(1)
	v_mfma_f32_16x16x32_f16 v[142:145], v[38:41], v[58:61], v[142:145]
	v_mfma_f32_16x16x32_f16 v[158:161], v[42:45], v[58:61], v[158:161]
	s_waitcnt lgkmcnt(0)
	v_mfma_f32_16x16x32_f16 v[114:117], v[38:41], v[214:217], v[114:117]
	v_mfma_f32_16x16x32_f16 v[178:181], v[42:45], v[214:217], v[178:181]
	ds_read_b128 v[58:61], v151 offset:1824
	ds_read_b128 v[214:217], v151 offset:2432
	s_waitcnt lgkmcnt(1)
	v_mfma_f32_16x16x32_f16 v[182:185], v[38:41], v[58:61], v[182:185]
	v_mfma_f32_16x16x32_f16 v[198:201], v[42:45], v[58:61], v[198:201]
	s_waitcnt lgkmcnt(0)
	v_mfma_f32_16x16x32_f16 v[134:137], v[38:41], v[214:217], v[134:137]
	v_mfma_f32_16x16x32_f16 v[146:149], v[42:45], v[214:217], v[146:149]
	v_add_u32_e32 v58, 0x17c40, v251
	v_min_u32_e32 v58, v58, v154
	global_load_dwordx4 v[58:61], v58, s[8:9] nt
	s_waitcnt vmcnt(21)
	v_cvt_pk_f16_f32 v73, v72, v73
	v_cvt_pk_f16_f32 v72, v70, v71
	ds_write_b16 v238, v72 offset:608
	ds_write_b16_d16_hi v239, v72 offset:608
	ds_write_b16 v240, v73 offset:608
	ds_write_b16_d16_hi v241, v73 offset:608
	ds_read_b128 v[70:73], v151 offset:3040
	ds_read_b128 v[214:217], v151 offset:4864
	s_waitcnt lgkmcnt(1)
	v_mfma_f32_16x16x32_f16 v[206:209], v[38:41], v[70:73], v[206:209]
	v_mfma_f32_16x16x32_f16 v[122:125], v[42:45], v[70:73], v[122:125]
	ds_read_b128 v[70:73], v151 offset:3648
	ds_read_b128 v[218:221], v151 offset:4256
	s_waitcnt lgkmcnt(1)
	v_mfma_f32_16x16x32_f16 v[210:213], v[38:41], v[70:73], v[210:213]
	v_mfma_f32_16x16x32_f16 v[190:193], v[42:45], v[70:73], v[190:193]
	s_waitcnt lgkmcnt(0)
	v_mfma_f32_16x16x32_f16 v[166:169], v[38:41], v[218:221], v[166:169]
	v_mfma_f32_16x16x32_f16 v[162:165], v[42:45], v[218:221], v[162:165]
	v_mfma_f32_16x16x32_f16 v[218:221], v[38:41], v[214:217], v[222:225]
	v_mfma_f32_16x16x32_f16 v[138:141], v[42:45], v[214:217], v[138:141]
	v_add_u32_e32 v70, 0x2e280, v250
	v_min_u32_e32 v70, v70, v154
	global_load_dwordx4 v[70:73], v70, s[8:9] nt
	s_waitcnt vmcnt(21)
	v_cvt_pk_f16_f32 v77, v76, v77
	v_cvt_pk_f16_f32 v76, v74, v75
	ds_write_b16 v234, v76 offset:1216
	ds_write_b16_d16_hi v235, v76 offset:1216
	ds_write_b16 v236, v77 offset:1216
	ds_write_b16_d16_hi v237, v77 offset:1216
	ds_read_b128 v[74:77], v151 offset:5472
	ds_read_b128 v[214:217], v151 offset:6080
	s_waitcnt lgkmcnt(1)
	v_mfma_f32_16x16x32_f16 v[170:173], v[38:41], v[74:77], v[170:173]
	v_mfma_f32_16x16x32_f16 v[126:129], v[42:45], v[74:77], v[126:129]
	s_waitcnt lgkmcnt(0)
	v_mfma_f32_16x16x32_f16 v[118:121], v[38:41], v[214:217], v[118:121]
	v_mfma_f32_16x16x32_f16 v[174:177], v[42:45], v[214:217], v[174:177]
	ds_read_b128 v[74:77], v151 offset:6688
	ds_read_b128 v[214:217], v151 offset:7296
	s_waitcnt lgkmcnt(1)
	v_mfma_f32_16x16x32_f16 v[186:189], v[38:41], v[74:77], v[186:189]
	v_mfma_f32_16x16x32_f16 v[194:197], v[42:45], v[74:77], v[194:197]
	s_waitcnt lgkmcnt(0)
	v_mfma_f32_16x16x32_f16 v[30:33], v[38:41], v[214:217], v[30:33]
	v_mfma_f32_16x16x32_f16 v[214:217], v[42:45], v[214:217], v[18:21]
	s_nop 2
	v_add_u32_e32 v18, 0x448c0, v251
	v_min_u32_e32 v18, v18, v154
	global_load_dwordx4 v[42:45], v18, s[8:9] nt
	s_waitcnt vmcnt(21)
	v_cvt_pk_f16_f32 v19, v80, v81
	v_cvt_pk_f16_f32 v18, v78, v79
	ds_write_b16 v238, v18 offset:1824
	ds_write_b16_d16_hi v239, v18 offset:1824
	ds_write_b16 v240, v19 offset:1824
	ds_write_b16_d16_hi v241, v19 offset:1824
	ds_read_b128 v[18:21], v151 offset:64
	ds_read_b128 v[38:41], v151 offset:672
	s_waitcnt lgkmcnt(1)
	v_mfma_f32_16x16x32_f16 v[130:133], v[22:25], v[18:21], v[130:133]
	v_mfma_f32_16x16x32_f16 v[202:205], v[2:5], v[18:21], v[202:205]
	s_waitcnt lgkmcnt(0)
	v_mfma_f32_16x16x32_f16 v[142:145], v[22:25], v[38:41], v[142:145]
	v_mfma_f32_16x16x32_f16 v[158:161], v[2:5], v[38:41], v[158:161]
	ds_read_b128 v[18:21], v151 offset:1280
	ds_read_b128 v[38:41], v151 offset:1888
	s_waitcnt lgkmcnt(1)
	v_mfma_f32_16x16x32_f16 v[114:117], v[22:25], v[18:21], v[114:117]
	v_mfma_f32_16x16x32_f16 v[178:181], v[2:5], v[18:21], v[178:181]
	s_waitcnt lgkmcnt(0)
	v_mfma_f32_16x16x32_f16 v[182:185], v[22:25], v[38:41], v[182:185]
	v_mfma_f32_16x16x32_f16 v[198:201], v[2:5], v[38:41], v[198:201]
	v_add_u32_e32 v18, 0x5af00, v250
	v_min_u32_e32 v18, v18, v154
	global_load_dwordx4 v[74:77], v18, s[8:9] nt
	s_waitcnt vmcnt(21)
	v_cvt_pk_f16_f32 v19, v84, v85
	v_cvt_pk_f16_f32 v18, v82, v83
	ds_write_b16 v234, v18 offset:2432
	ds_write_b16_d16_hi v235, v18 offset:2432
	ds_write_b16 v236, v19 offset:2432
	ds_write_b16_d16_hi v237, v19 offset:2432
	ds_read_b128 v[18:21], v151 offset:2496
	ds_read_b128 v[38:41], v151 offset:3104
	s_waitcnt lgkmcnt(1)
	v_mfma_f32_16x16x32_f16 v[134:137], v[22:25], v[18:21], v[134:137]
	v_mfma_f32_16x16x32_f16 v[146:149], v[2:5], v[18:21], v[146:149]
	s_waitcnt lgkmcnt(0)
	v_mfma_f32_16x16x32_f16 v[206:209], v[22:25], v[38:41], v[206:209]
	v_mfma_f32_16x16x32_f16 v[122:125], v[2:5], v[38:41], v[122:125]
	ds_read_b128 v[18:21], v151 offset:3712
	ds_read_b128 v[38:41], v151 offset:4320
	s_waitcnt lgkmcnt(1)
	v_mfma_f32_16x16x32_f16 v[210:213], v[22:25], v[18:21], v[210:213]
	v_mfma_f32_16x16x32_f16 v[190:193], v[2:5], v[18:21], v[190:193]
	s_waitcnt lgkmcnt(0)
	v_mfma_f32_16x16x32_f16 v[166:169], v[22:25], v[38:41], v[166:169]
	v_mfma_f32_16x16x32_f16 v[162:165], v[2:5], v[38:41], v[162:165]
	v_add_u32_e32 v18, 0x71540, v251
	v_min_u32_e32 v18, v18, v154
	global_load_dwordx4 v[78:81], v18, s[8:9] nt
	s_waitcnt vmcnt(21)
	v_cvt_pk_f16_f32 v19, v88, v89
	v_cvt_pk_f16_f32 v18, v86, v87
	ds_write_b16 v238, v18 offset:3040
	ds_write_b16_d16_hi v239, v18 offset:3040
	ds_write_b16 v240, v19 offset:3040
	ds_write_b16_d16_hi v241, v19 offset:3040
	ds_read_b128 v[18:21], v151 offset:4928
	ds_read_b128 v[38:41], v151 offset:5536
	s_waitcnt lgkmcnt(1)
	v_mfma_f32_16x16x32_f16 v[218:221], v[22:25], v[18:21], v[218:221]
	v_mfma_f32_16x16x32_f16 v[138:141], v[2:5], v[18:21], v[138:141]
	s_waitcnt lgkmcnt(0)
	v_mfma_f32_16x16x32_f16 v[170:173], v[22:25], v[38:41], v[170:173]
	v_mfma_f32_16x16x32_f16 v[126:129], v[2:5], v[38:41], v[126:129]
	ds_read_b128 v[18:21], v151 offset:6144
	ds_read_b128 v[38:41], v151 offset:6752
	s_waitcnt lgkmcnt(1)
	v_mfma_f32_16x16x32_f16 v[118:121], v[22:25], v[18:21], v[118:121]
	v_mfma_f32_16x16x32_f16 v[174:177], v[2:5], v[18:21], v[174:177]
	s_waitcnt lgkmcnt(0)
	v_mfma_f32_16x16x32_f16 v[186:189], v[22:25], v[38:41], v[186:189]
	v_mfma_f32_16x16x32_f16 v[194:197], v[2:5], v[38:41], v[194:197]
	v_add_u32_e32 v18, 0x87b80, v250
	v_min_u32_e32 v18, v18, v154
	global_load_dwordx4 v[82:85], v18, s[8:9] nt
	s_waitcnt vmcnt(21)
	v_cvt_pk_f16_f32 v19, v92, v93
	v_cvt_pk_f16_f32 v18, v90, v91
	ds_write_b16 v234, v18 offset:3648
	ds_write_b16_d16_hi v235, v18 offset:3648
	ds_write_b16 v236, v19 offset:3648
	ds_write_b16_d16_hi v237, v19 offset:3648
	ds_read_b128 v[86:89], v151 offset:7360
	s_mov_b32 s3, 0xa8000
	v_add_co_u32_e32 v18, vcc, s3, v152
	s_mov_b32 s3, 0xac000
	s_nop 0
	v_addc_co_u32_e32 v19, vcc, 0, v153, vcc
	s_waitcnt lgkmcnt(0)
	v_mfma_f32_16x16x32_f16 v[222:225], v[22:25], v[86:89], v[30:33]
	s_nop 2
	global_load_dwordx4 v[30:33], v[18:19], off sc1
	global_load_dwordx4 v[38:41], v[18:19], off offset:256 sc1
	v_add_co_u32_e32 v18, vcc, s3, v152
	v_mfma_f32_16x16x32_f16 v[2:5], v[2:5], v[86:89], v[214:217]
	s_nop 0
	v_addc_co_u32_e32 v19, vcc, 0, v153, vcc
	global_load_dwordx4 v[22:25], v[18:19], off sc1
	s_nop 0
	global_load_dwordx4 v[18:21], v[18:19], off offset:256 sc1
	ds_read_b128 v[86:89], v151 offset:128
	ds_read_b128 v[90:93], v151 offset:736
	s_waitcnt vmcnt(24) lgkmcnt(1)
	v_mfma_f32_16x16x32_f16 v[130:133], v[50:53], v[86:89], v[130:133]
	s_waitcnt vmcnt(23)
	v_mfma_f32_16x16x32_f16 v[202:205], v[54:57], v[86:89], v[202:205]
	ds_read_b128 v[86:89], v151 offset:1344
	s_waitcnt lgkmcnt(0)
	v_mfma_f32_16x16x32_f16 v[114:117], v[50:53], v[86:89], v[114:117]
	v_mfma_f32_16x16x32_f16 v[142:145], v[50:53], v[90:93], v[142:145]
	v_mfma_f32_16x16x32_f16 v[158:161], v[54:57], v[90:93], v[158:161]
	v_mfma_f32_16x16x32_f16 v[178:181], v[54:57], v[86:89], v[178:181]
	v_add_u32_e32 v86, 0x9e1c0, v251
	v_min_u32_e32 v86, v86, v154
	global_load_dwordx4 v[86:89], v86, s[8:9] nt
	s_waitcnt vmcnt(21)
	v_cvt_pk_f16_f32 v91, v96, v97
	v_cvt_pk_f16_f32 v90, v94, v95
	ds_write_b16 v238, v90 offset:4256
	ds_write_b16_d16_hi v239, v90 offset:4256
	ds_write_b16 v240, v91 offset:4256
	ds_write_b16_d16_hi v241, v91 offset:4256
	ds_read_b128 v[90:93], v151 offset:1952
	ds_read_b128 v[94:97], v151 offset:2560
	s_waitcnt lgkmcnt(1)
	v_mfma_f32_16x16x32_f16 v[182:185], v[50:53], v[90:93], v[182:185]
	v_mfma_f32_16x16x32_f16 v[198:201], v[54:57], v[90:93], v[198:201]
	s_waitcnt lgkmcnt(0)
	v_mfma_f32_16x16x32_f16 v[134:137], v[50:53], v[94:97], v[134:137]
	v_mfma_f32_16x16x32_f16 v[146:149], v[54:57], v[94:97], v[146:149]
	ds_read_b128 v[90:93], v151 offset:3168
	ds_read_b128 v[94:97], v151 offset:3776
	s_waitcnt lgkmcnt(1)
	v_mfma_f32_16x16x32_f16 v[206:209], v[50:53], v[90:93], v[206:209]
	v_mfma_f32_16x16x32_f16 v[122:125], v[54:57], v[90:93], v[122:125]
	s_waitcnt lgkmcnt(0)
	v_mfma_f32_16x16x32_f16 v[210:213], v[50:53], v[94:97], v[210:213]
	v_mfma_f32_16x16x32_f16 v[190:193], v[54:57], v[94:97], v[190:193]
	v_add_u32_e32 v90, 0xb4800, v250
	v_min_u32_e32 v90, v90, v154
	global_load_dwordx4 v[90:93], v90, s[8:9] nt
	s_waitcnt vmcnt(21)
	v_cvt_pk_f16_f32 v95, v100, v101
	v_cvt_pk_f16_f32 v94, v98, v99
	ds_write_b16 v234, v94 offset:4864
	ds_write_b16_d16_hi v235, v94 offset:4864
	ds_write_b16 v236, v95 offset:4864
	ds_write_b16_d16_hi v237, v95 offset:4864
	ds_read_b128 v[94:97], v151 offset:4384
	ds_read_b128 v[98:101], v151 offset:6208
	s_waitcnt lgkmcnt(1)
	v_mfma_f32_16x16x32_f16 v[166:169], v[50:53], v[94:97], v[166:169]
	v_mfma_f32_16x16x32_f16 v[162:165], v[54:57], v[94:97], v[162:165]
	ds_read_b128 v[94:97], v151 offset:4992
	ds_read_b128 v[214:217], v151 offset:5600
	s_waitcnt lgkmcnt(1)
	v_mfma_f32_16x16x32_f16 v[218:221], v[50:53], v[94:97], v[218:221]
	v_mfma_f32_16x16x32_f16 v[138:141], v[54:57], v[94:97], v[138:141]
	s_waitcnt lgkmcnt(0)
	v_mfma_f32_16x16x32_f16 v[170:173], v[50:53], v[214:217], v[170:173]
	v_mfma_f32_16x16x32_f16 v[126:129], v[54:57], v[214:217], v[126:129]
	v_mfma_f32_16x16x32_f16 v[118:121], v[50:53], v[98:101], v[118:121]
	v_mfma_f32_16x16x32_f16 v[174:177], v[54:57], v[98:101], v[174:177]
	v_add_u32_e32 v94, 0xcae40, v251
	v_min_u32_e32 v94, v94, v154
	global_load_dwordx4 v[94:97], v94, s[8:9] nt
	s_waitcnt vmcnt(21)
	v_cvt_pk_f16_f32 v99, v104, v105
	v_cvt_pk_f16_f32 v98, v102, v103
	ds_write_b16 v238, v98 offset:5472
	ds_write_b16_d16_hi v239, v98 offset:5472
	ds_write_b16 v240, v99 offset:5472
	ds_write_b16_d16_hi v241, v99 offset:5472
	ds_read_b128 v[98:101], v151 offset:6816
	ds_read_b128 v[102:105], v151 offset:7424
	s_waitcnt lgkmcnt(1)
	v_mfma_f32_16x16x32_f16 v[186:189], v[50:53], v[98:101], v[186:189]
	s_waitcnt lgkmcnt(0)
	v_mfma_f32_16x16x32_f16 v[214:217], v[50:53], v[102:105], v[222:225]
	v_mfma_f32_16x16x32_f16 v[102:105], v[54:57], v[102:105], v[2:5]
	s_nop 2
	ds_read_b128 v[2:5], v151 offset:192
	ds_read_b128 v[50:53], v151 offset:800
	v_mfma_f32_16x16x32_f16 v[194:197], v[54:57], v[98:101], v[194:197]
	s_waitcnt lgkmcnt(1)
	v_mfma_f32_16x16x32_f16 v[130:133], v[26:29], v[2:5], v[130:133]
	v_mfma_f32_16x16x32_f16 v[202:205], v[14:17], v[2:5], v[202:205]
	s_waitcnt lgkmcnt(0)
	v_mfma_f32_16x16x32_f16 v[142:145], v[26:29], v[50:53], v[142:145]
	v_mfma_f32_16x16x32_f16 v[158:161], v[14:17], v[50:53], v[158:161]
	v_add_u32_e32 v2, 0xe1480, v250
	v_min_u32_e32 v2, v2, v154
	global_load_dwordx4 v[98:101], v2, s[8:9] nt
	s_waitcnt vmcnt(21)
	v_cvt_pk_f16_f32 v3, v64, v65
	v_cvt_pk_f16_f32 v2, v62, v63
	ds_write_b16 v234, v2 offset:6080
	ds_write_b16_d16_hi v235, v2 offset:6080
	ds_write_b16 v236, v3 offset:6080
	ds_write_b16_d16_hi v237, v3 offset:6080
	ds_read_b128 v[2:5], v151 offset:1408
	ds_read_b128 v[50:53], v151 offset:2016
	s_waitcnt lgkmcnt(1)
	v_mfma_f32_16x16x32_f16 v[222:225], v[26:29], v[2:5], v[114:117]
	v_mfma_f32_16x16x32_f16 v[178:181], v[14:17], v[2:5], v[178:181]
	s_waitcnt lgkmcnt(0)
	v_mfma_f32_16x16x32_f16 v[182:185], v[26:29], v[50:53], v[182:185]
	v_mfma_f32_16x16x32_f16 v[198:201], v[14:17], v[50:53], v[198:201]
	ds_read_b128 v[2:5], v151 offset:2624
	ds_read_b128 v[50:53], v151 offset:3232
	s_waitcnt lgkmcnt(1)
	v_mfma_f32_16x16x32_f16 v[134:137], v[26:29], v[2:5], v[134:137]
	v_mfma_f32_16x16x32_f16 v[146:149], v[14:17], v[2:5], v[146:149]
	s_waitcnt lgkmcnt(0)
	v_mfma_f32_16x16x32_f16 v[206:209], v[26:29], v[50:53], v[206:209]
	v_mfma_f32_16x16x32_f16 v[122:125], v[14:17], v[50:53], v[122:125]
	v_add_u32_e32 v2, 0xf7ac0, v251
	v_min_u32_e32 v2, v2, v154
	global_load_dwordx4 v[62:65], v2, s[8:9] nt
	s_waitcnt vmcnt(21)
	v_cvt_pk_f16_f32 v3, v68, v69
	v_cvt_pk_f16_f32 v2, v66, v67
	ds_write_b16 v238, v2 offset:6688
	ds_write_b16_d16_hi v239, v2 offset:6688
	ds_write_b16 v240, v3 offset:6688
	ds_write_b16_d16_hi v241, v3 offset:6688
	ds_read_b128 v[2:5], v151 offset:3840
	ds_read_b128 v[50:53], v151 offset:4448
	s_waitcnt lgkmcnt(1)
	v_mfma_f32_16x16x32_f16 v[210:213], v[26:29], v[2:5], v[210:213]
	v_mfma_f32_16x16x32_f16 v[190:193], v[14:17], v[2:5], v[190:193]
	s_waitcnt lgkmcnt(0)
	v_mfma_f32_16x16x32_f16 v[166:169], v[26:29], v[50:53], v[166:169]
	v_mfma_f32_16x16x32_f16 v[162:165], v[14:17], v[50:53], v[162:165]
	ds_read_b128 v[2:5], v151 offset:5056
	ds_read_b128 v[50:53], v151 offset:5664
	s_waitcnt lgkmcnt(1)
	v_mfma_f32_16x16x32_f16 v[218:221], v[26:29], v[2:5], v[218:221]
	v_mfma_f32_16x16x32_f16 v[138:141], v[14:17], v[2:5], v[138:141]
	s_waitcnt lgkmcnt(0)
	v_mfma_f32_16x16x32_f16 v[170:173], v[26:29], v[50:53], v[170:173]
	v_mfma_f32_16x16x32_f16 v[126:129], v[14:17], v[50:53], v[126:129]
	v_add_u32_e32 v2, 0x10e100, v250
	v_min_u32_e32 v2, v2, v154
	v_cndmask_b32_e64 v2, 0, v2, s[0:1]
	global_load_dwordx4 v[66:69], v2, s[8:9] nt
	s_waitcnt vmcnt(21)
	v_cvt_pk_f16_f32 v3, v108, v109
	v_cvt_pk_f16_f32 v2, v106, v107
	ds_write_b16 v234, v2 offset:7296
	ds_write_b16_d16_hi v235, v2 offset:7296
	ds_write_b16 v236, v3 offset:7296
	ds_write_b16_d16_hi v237, v3 offset:7296
	ds_read_b128 v[2:5], v151 offset:6272
	ds_read_b128 v[50:53], v151 offset:6880
	ds_read_b128 v[106:109], v151 offset:7488
	s_mov_b32 s3, 0xb0000
	s_waitcnt lgkmcnt(0)
	v_mfma_f32_16x16x32_f16 v[116:119], v[26:29], v[2:5], v[118:121]
	s_barrier
	v_sub_u32_e32 v245, v234, v243
	v_add_u32_e32 v246, 0xfffffdc0, v245
	v_min_u32_e32 v245, v245, v246
	v_add_u32_e32 v234, v242, v245
	v_sub_u32_e32 v245, v235, v243
	v_add_u32_e32 v246, 0xfffffdc0, v245
	v_min_u32_e32 v245, v245, v246
	v_add_u32_e32 v235, v242, v245
	v_sub_u32_e32 v245, v236, v243
	v_add_u32_e32 v246, 0xfffffdc0, v245
	v_min_u32_e32 v245, v245, v246
	v_add_u32_e32 v236, v242, v245
	v_sub_u32_e32 v245, v237, v243
	v_add_u32_e32 v246, 0xfffffdc0, v245
	v_min_u32_e32 v245, v245, v246
	v_add_u32_e32 v237, v242, v245
	v_sub_u32_e32 v245, v238, v243
	v_add_u32_e32 v246, 0xfffffdc0, v245
	v_min_u32_e32 v245, v245, v246
	v_add_u32_e32 v238, v242, v245
	v_sub_u32_e32 v245, v239, v243
	v_add_u32_e32 v246, 0xfffffdc0, v245
	v_min_u32_e32 v245, v245, v246
	v_add_u32_e32 v239, v242, v245
	v_sub_u32_e32 v245, v240, v243
	v_add_u32_e32 v246, 0xfffffdc0, v245
	v_min_u32_e32 v245, v245, v246
	v_add_u32_e32 v240, v242, v245
	v_sub_u32_e32 v245, v241, v243
	v_add_u32_e32 v246, 0xfffffdc0, v245
	v_min_u32_e32 v245, v245, v246
	v_add_u32_e32 v241, v242, v245
	v_mfma_f32_16x16x32_f16 v[174:177], v[14:17], v[2:5], v[174:177]
	v_add_co_u32_e32 v2, vcc, s3, v152
	s_nop 1
	v_addc_co_u32_e32 v3, vcc, 0, v153, vcc
	v_mfma_f32_16x16x32_f16 v[186:189], v[26:29], v[50:53], v[186:189]
	v_mfma_f32_16x16x32_f16 v[214:217], v[26:29], v[106:109], v[214:217]
	v_add_co_u32_e32 v26, vcc, s2, v152
	s_nop 1
	v_addc_co_u32_e32 v27, vcc, 0, v153, vcc
	v_mfma_f32_16x16x32_f16 v[194:197], v[14:17], v[50:53], v[194:197]
	global_load_dwordx4 v[50:53], v[2:3], off sc1
	global_load_dwordx4 v[54:57], v[2:3], off offset:256 sc1
	s_nop 0
	global_load_dwordx4 v[2:5], v[26:27], off sc1
	s_nop 0
	global_load_dwordx4 v[26:29], v[26:27], off offset:256 sc1
	v_mfma_f32_16x16x32_f16 v[14:17], v[14:17], v[106:109], v[102:105]
	v_mov_b32_e32 v114, 0
	s_nop 1
	ds_read_b128 v[102:105], v151 offset:256
	v_mov_b32_e32 v115, 0
	v_add_u32_e32 v106, 0x1800, v150
	s_waitcnt vmcnt(24) lgkmcnt(0)
	v_mfma_f32_16x16x32_f16 v[130:133], v[34:37], v[102:105], v[130:133]
	s_waitcnt vmcnt(23)
	v_mfma_f32_16x16x32_f16 v[202:205], v[46:49], v[102:105], v[202:205]
	v_min_u32_e32 v102, v106, v114
	global_load_dwordx4 v[102:105], v102, s[8:9] nt
	s_waitcnt vmcnt(21)
	v_cvt_pk_f16_f32 v107, v112, v113
	v_cvt_pk_f16_f32 v106, v110, v111
	ds_write_b16 v234, v106 offset:0
	ds_write_b16_d16_hi v235, v106 offset:0
	ds_write_b16 v236, v107 offset:0
	ds_write_b16_d16_hi v237, v107 offset:0
	ds_read_b128 v[106:109], v151 offset:864
	ds_read_b128 v[110:113], v151 offset:1472
	s_waitcnt lgkmcnt(1)
	v_mfma_f32_16x16x32_f16 v[142:145], v[34:37], v[106:109], v[142:145]
	v_mfma_f32_16x16x32_f16 v[158:161], v[46:49], v[106:109], v[158:161]
	s_waitcnt lgkmcnt(0)
	v_mfma_f32_16x16x32_f16 v[222:225], v[34:37], v[110:113], v[222:225]
	v_mfma_f32_16x16x32_f16 v[110:113], v[46:49], v[110:113], v[178:181]
	ds_read_b128 v[106:109], v151 offset:2080
	s_nop 1
	ds_read_b128 v[178:181], v151 offset:2688
	s_waitcnt lgkmcnt(1)
	v_mfma_f32_16x16x32_f16 v[182:185], v[34:37], v[106:109], v[182:185]
	v_mfma_f32_16x16x32_f16 v[198:201], v[46:49], v[106:109], v[198:201]
	s_waitcnt lgkmcnt(0)
	v_mfma_f32_16x16x32_f16 v[134:137], v[34:37], v[178:181], v[134:137]
	v_mfma_f32_16x16x32_f16 v[146:149], v[46:49], v[178:181], v[146:149]
	v_add_u32_e32 v106, 0x17e40, v244
	v_min_u32_e32 v106, v106, v114
	global_load_dwordx4 v[106:109], v106, s[8:9] nt
	s_waitcnt vmcnt(21)
	v_cvt_pk_f16_f32 v61, v60, v61
	v_cvt_pk_f16_f32 v60, v58, v59
	ds_write_b16 v238, v60 offset:608
	ds_write_b16_d16_hi v239, v60 offset:608
	ds_write_b16 v240, v61 offset:608
	ds_write_b16_d16_hi v241, v61 offset:608
	ds_read_b128 v[58:61], v151 offset:3296
	ds_read_b128 v[178:181], v151 offset:5120
	s_waitcnt lgkmcnt(1)
	v_mfma_f32_16x16x32_f16 v[206:209], v[34:37], v[58:61], v[206:209]
	v_mfma_f32_16x16x32_f16 v[120:123], v[46:49], v[58:61], v[122:125]
	ds_read_b128 v[58:61], v151 offset:3904
	ds_read_b128 v[226:229], v151 offset:4512
	s_waitcnt lgkmcnt(1)
	v_mfma_f32_16x16x32_f16 v[210:213], v[34:37], v[58:61], v[210:213]
	v_mfma_f32_16x16x32_f16 v[190:193], v[46:49], v[58:61], v[190:193]
	s_waitcnt lgkmcnt(0)
	v_mfma_f32_16x16x32_f16 v[166:169], v[34:37], v[226:229], v[166:169]
	v_mfma_f32_16x16x32_f16 v[162:165], v[46:49], v[226:229], v[162:165]
	v_mfma_f32_16x16x32_f16 v[218:221], v[34:37], v[178:181], v[218:221]
	v_mfma_f32_16x16x32_f16 v[138:141], v[46:49], v[178:181], v[138:141]
	v_add_u32_e32 v58, 0x2e480, v150
	v_min_u32_e32 v58, v58, v114
	global_load_dwordx4 v[58:61], v58, s[8:9] nt
	s_waitcnt vmcnt(21)
	v_cvt_pk_f16_f32 v73, v72, v73
	v_cvt_pk_f16_f32 v72, v70, v71
	ds_write_b16 v234, v72 offset:1216
	ds_write_b16_d16_hi v235, v72 offset:1216
	ds_write_b16 v236, v73 offset:1216
	ds_write_b16_d16_hi v237, v73 offset:1216
	ds_read_b128 v[70:73], v151 offset:5728
	ds_read_b128 v[178:181], v151 offset:6336
	s_waitcnt lgkmcnt(1)
	v_mfma_f32_16x16x32_f16 v[170:173], v[34:37], v[70:73], v[170:173]
	v_mfma_f32_16x16x32_f16 v[124:127], v[46:49], v[70:73], v[126:129]
	s_waitcnt lgkmcnt(0)
	v_mfma_f32_16x16x32_f16 v[116:119], v[34:37], v[178:181], v[116:119]
	v_mfma_f32_16x16x32_f16 v[174:177], v[46:49], v[178:181], v[174:177]
	ds_read_b128 v[70:73], v151 offset:6944
	ds_read_b128 v[178:181], v151 offset:7552
	s_waitcnt lgkmcnt(1)
	v_mfma_f32_16x16x32_f16 v[186:189], v[34:37], v[70:73], v[186:189]
	v_mfma_f32_16x16x32_f16 v[194:197], v[46:49], v[70:73], v[194:197]
	s_waitcnt lgkmcnt(0)
	v_mfma_f32_16x16x32_f16 v[214:217], v[34:37], v[178:181], v[214:217]
	v_mfma_f32_16x16x32_f16 v[178:181], v[46:49], v[178:181], v[14:17]
	s_nop 2
	v_add_u32_e32 v14, 0x44ac0, v244
	v_min_u32_e32 v14, v14, v114
	global_load_dwordx4 v[34:37], v14, s[8:9] nt
	s_waitcnt vmcnt(21)
	v_cvt_pk_f16_f32 v15, v44, v45
	v_cvt_pk_f16_f32 v14, v42, v43
	ds_write_b16 v238, v14 offset:1824
	ds_write_b16_d16_hi v239, v14 offset:1824
	ds_write_b16 v240, v15 offset:1824
	ds_write_b16_d16_hi v241, v15 offset:1824
	ds_read_b128 v[14:17], v151 offset:320
	ds_read_b128 v[42:45], v151 offset:928
	s_waitcnt lgkmcnt(1)
	v_mfma_f32_16x16x32_f16 v[128:131], v[10:13], v[14:17], v[130:133]
	v_mfma_f32_16x16x32_f16 v[202:205], v[6:9], v[14:17], v[202:205]
	s_waitcnt lgkmcnt(0)
	v_mfma_f32_16x16x32_f16 v[142:145], v[10:13], v[42:45], v[142:145]
	v_mfma_f32_16x16x32_f16 v[158:161], v[6:9], v[42:45], v[158:161]
	ds_read_b128 v[14:17], v151 offset:1536
	ds_read_b128 v[42:45], v151 offset:2144
	s_waitcnt lgkmcnt(1)
	v_mfma_f32_16x16x32_f16 v[222:225], v[10:13], v[14:17], v[222:225]
	v_mfma_f32_16x16x32_f16 v[110:113], v[6:9], v[14:17], v[110:113]
	s_waitcnt lgkmcnt(0)
	v_mfma_f32_16x16x32_f16 v[182:185], v[10:13], v[42:45], v[182:185]
	v_mfma_f32_16x16x32_f16 v[198:201], v[6:9], v[42:45], v[198:201]
	v_add_u32_e32 v14, 0x5b100, v150
	v_min_u32_e32 v14, v14, v114
	global_load_dwordx4 v[70:73], v14, s[8:9] nt
	s_waitcnt vmcnt(21)
	v_cvt_pk_f16_f32 v15, v76, v77
	v_cvt_pk_f16_f32 v14, v74, v75
	ds_write_b16 v234, v14 offset:2432
	ds_write_b16_d16_hi v235, v14 offset:2432
	ds_write_b16 v236, v15 offset:2432
	ds_write_b16_d16_hi v237, v15 offset:2432
	ds_read_b128 v[14:17], v151 offset:2752
	ds_read_b128 v[42:45], v151 offset:3360
	s_waitcnt lgkmcnt(1)
	v_mfma_f32_16x16x32_f16 v[132:135], v[10:13], v[14:17], v[134:137]
	v_mfma_f32_16x16x32_f16 v[146:149], v[6:9], v[14:17], v[146:149]
	s_waitcnt lgkmcnt(0)
	v_mfma_f32_16x16x32_f16 v[206:209], v[10:13], v[42:45], v[206:209]
	v_mfma_f32_16x16x32_f16 v[120:123], v[6:9], v[42:45], v[120:123]
	ds_read_b128 v[14:17], v151 offset:3968
	ds_read_b128 v[42:45], v151 offset:4576
	s_waitcnt lgkmcnt(1)
	v_mfma_f32_16x16x32_f16 v[210:213], v[10:13], v[14:17], v[210:213]
	v_mfma_f32_16x16x32_f16 v[190:193], v[6:9], v[14:17], v[190:193]
	s_waitcnt lgkmcnt(0)
	v_mfma_f32_16x16x32_f16 v[166:169], v[10:13], v[42:45], v[166:169]
	v_mfma_f32_16x16x32_f16 v[162:165], v[6:9], v[42:45], v[162:165]
	v_add_u32_e32 v14, 0x71740, v244
	v_min_u32_e32 v14, v14, v114
	global_load_dwordx4 v[74:77], v14, s[8:9] nt
	s_waitcnt vmcnt(21)
	v_cvt_pk_f16_f32 v15, v80, v81
	v_cvt_pk_f16_f32 v14, v78, v79
	ds_write_b16 v238, v14 offset:3040
	ds_write_b16_d16_hi v239, v14 offset:3040
	ds_write_b16 v240, v15 offset:3040
	ds_write_b16_d16_hi v241, v15 offset:3040
	ds_read_b128 v[14:17], v151 offset:5184
	ds_read_b128 v[42:45], v151 offset:5792
	s_waitcnt lgkmcnt(1)
	v_mfma_f32_16x16x32_f16 v[218:221], v[10:13], v[14:17], v[218:221]
	v_mfma_f32_16x16x32_f16 v[136:139], v[6:9], v[14:17], v[138:141]
	s_waitcnt lgkmcnt(0)
	v_mfma_f32_16x16x32_f16 v[170:173], v[10:13], v[42:45], v[170:173]
	v_mfma_f32_16x16x32_f16 v[124:127], v[6:9], v[42:45], v[124:127]
	ds_read_b128 v[14:17], v151 offset:6400
	ds_read_b128 v[42:45], v151 offset:7008
	s_waitcnt lgkmcnt(1)
	v_mfma_f32_16x16x32_f16 v[116:119], v[10:13], v[14:17], v[116:119]
	v_mfma_f32_16x16x32_f16 v[174:177], v[6:9], v[14:17], v[174:177]
	s_waitcnt lgkmcnt(0)
	v_mfma_f32_16x16x32_f16 v[186:189], v[10:13], v[42:45], v[186:189]
	v_mfma_f32_16x16x32_f16 v[194:197], v[6:9], v[42:45], v[194:197]
	v_add_u32_e32 v14, 0x87d80, v150
	v_min_u32_e32 v14, v14, v114
	global_load_dwordx4 v[78:81], v14, s[8:9] nt
	s_waitcnt vmcnt(21)
	v_cvt_pk_f16_f32 v15, v84, v85
	v_cvt_pk_f16_f32 v14, v82, v83
	ds_write_b16 v234, v14 offset:3648
	ds_write_b16_d16_hi v235, v14 offset:3648
	ds_write_b16 v236, v15 offset:3648
	ds_write_b16_d16_hi v237, v15 offset:3648
	ds_read_b128 v[82:85], v151 offset:7616
	s_mov_b32 s2, 0xb8000
	v_add_co_u32_e32 v14, vcc, s2, v152
	s_mov_b32 s2, 0xbc000
	s_nop 0
	v_addc_co_u32_e32 v15, vcc, 0, v153, vcc
	v_add_co_u32_e32 v42, vcc, s2, v152
	s_waitcnt lgkmcnt(0)
	v_mfma_f32_16x16x32_f16 v[214:217], v[10:13], v[82:85], v[214:217]
	v_addc_co_u32_e32 v43, vcc, 0, v153, vcc
	global_load_dwordx4 v[10:13], v[14:15], off sc1
	s_nop 0
	global_load_dwordx4 v[14:17], v[14:15], off offset:256 sc1
	s_nop 0
	global_load_dwordx4 v[46:49], v[42:43], off sc1
	s_nop 0
	global_load_dwordx4 v[42:45], v[42:43], off offset:256 sc1
	v_mfma_f32_16x16x32_f16 v[178:181], v[6:9], v[82:85], v[178:181]
	ds_read_b128 v[6:9], v151 offset:384
	ds_read_b128 v[82:85], v151 offset:992
	s_waitcnt vmcnt(24) lgkmcnt(1)
	v_mfma_f32_16x16x32_f16 v[128:131], v[30:33], v[6:9], v[128:131]
	s_waitcnt vmcnt(23)
	v_mfma_f32_16x16x32_f16 v[202:205], v[38:41], v[6:9], v[202:205]
	ds_read_b128 v[6:9], v151 offset:1600
	s_waitcnt lgkmcnt(1)
	v_mfma_f32_16x16x32_f16 v[140:143], v[30:33], v[82:85], v[142:145]
	v_mfma_f32_16x16x32_f16 v[158:161], v[38:41], v[82:85], v[158:161]
	s_waitcnt lgkmcnt(0)
	v_mfma_f32_16x16x32_f16 v[222:225], v[30:33], v[6:9], v[222:225]
	v_mfma_f32_16x16x32_f16 v[110:113], v[38:41], v[6:9], v[110:113]
	v_add_u32_e32 v6, 0x9e3c0, v244
	v_min_u32_e32 v6, v6, v114
	global_load_dwordx4 v[6:9], v6, s[8:9] nt
	s_waitcnt vmcnt(21)
	v_cvt_pk_f16_f32 v83, v88, v89
	v_cvt_pk_f16_f32 v82, v86, v87
	ds_write_b16 v238, v82 offset:4256
	ds_write_b16_d16_hi v239, v82 offset:4256
	ds_write_b16 v240, v83 offset:4256
	ds_write_b16_d16_hi v241, v83 offset:4256
	ds_read_b128 v[82:85], v151 offset:2208
	ds_read_b128 v[86:89], v151 offset:2816
	s_waitcnt lgkmcnt(1)
	v_mfma_f32_16x16x32_f16 v[182:185], v[30:33], v[82:85], v[182:185]
	v_mfma_f32_16x16x32_f16 v[198:201], v[38:41], v[82:85], v[198:201]
	s_waitcnt lgkmcnt(0)
	v_mfma_f32_16x16x32_f16 v[132:135], v[30:33], v[86:89], v[132:135]
	v_mfma_f32_16x16x32_f16 v[144:147], v[38:41], v[86:89], v[146:149]
	ds_read_b128 v[82:85], v151 offset:3424
	ds_read_b128 v[86:89], v151 offset:4032
	s_waitcnt lgkmcnt(1)
	v_mfma_f32_16x16x32_f16 v[206:209], v[30:33], v[82:85], v[206:209]
	v_mfma_f32_16x16x32_f16 v[120:123], v[38:41], v[82:85], v[120:123]
	s_waitcnt lgkmcnt(0)
	v_mfma_f32_16x16x32_f16 v[210:213], v[30:33], v[86:89], v[210:213]
	v_mfma_f32_16x16x32_f16 v[190:193], v[38:41], v[86:89], v[190:193]
	v_add_u32_e32 v82, 0xb4a00, v150
	v_min_u32_e32 v82, v82, v114
	global_load_dwordx4 v[82:85], v82, s[8:9] nt
	s_waitcnt vmcnt(21)
	v_cvt_pk_f16_f32 v87, v92, v93
	v_cvt_pk_f16_f32 v86, v90, v91
	ds_write_b16 v234, v86 offset:4864
	ds_write_b16_d16_hi v235, v86 offset:4864
	ds_write_b16 v236, v87 offset:4864
	ds_write_b16_d16_hi v237, v87 offset:4864
	ds_read_b128 v[86:89], v151 offset:4640
	ds_read_b128 v[90:93], v151 offset:6464
	s_waitcnt lgkmcnt(1)
	v_mfma_f32_16x16x32_f16 v[166:169], v[30:33], v[86:89], v[166:169]
	v_mfma_f32_16x16x32_f16 v[162:165], v[38:41], v[86:89], v[162:165]
	ds_read_b128 v[86:89], v151 offset:5248
	ds_read_b128 v[226:229], v151 offset:5856
	s_waitcnt lgkmcnt(1)
	v_mfma_f32_16x16x32_f16 v[218:221], v[30:33], v[86:89], v[218:221]
	v_mfma_f32_16x16x32_f16 v[136:139], v[38:41], v[86:89], v[136:139]
	s_waitcnt lgkmcnt(0)
	v_mfma_f32_16x16x32_f16 v[170:173], v[30:33], v[226:229], v[170:173]
	v_mfma_f32_16x16x32_f16 v[124:127], v[38:41], v[226:229], v[124:127]
	v_mfma_f32_16x16x32_f16 v[116:119], v[30:33], v[90:93], v[116:119]
	v_mfma_f32_16x16x32_f16 v[90:93], v[38:41], v[90:93], v[174:177]
	v_add_u32_e32 v86, 0xcb040, v244
	v_min_u32_e32 v86, v86, v114
	global_load_dwordx4 v[86:89], v86, s[8:9] nt
	s_waitcnt vmcnt(21)
	v_cvt_pk_f16_f32 v97, v96, v97
	v_cvt_pk_f16_f32 v96, v94, v95
	ds_write_b16 v238, v96 offset:5472
	ds_write_b16_d16_hi v239, v96 offset:5472
	ds_write_b16 v240, v97 offset:5472
	ds_write_b16_d16_hi v241, v97 offset:5472
	ds_read_b128 v[94:97], v151 offset:7072
	ds_read_b128 v[174:177], v151 offset:7680
	s_waitcnt lgkmcnt(1)
	v_mfma_f32_16x16x32_f16 v[186:189], v[30:33], v[94:97], v[186:189]
	v_mfma_f32_16x16x32_f16 v[94:97], v[38:41], v[94:97], v[194:197]
	s_waitcnt lgkmcnt(0)
	v_mfma_f32_16x16x32_f16 v[194:197], v[30:33], v[174:177], v[214:217]
	v_mfma_f32_16x16x32_f16 v[174:177], v[38:41], v[174:177], v[178:181]
	ds_read_b128 v[30:33], v151 offset:448
	ds_read_b128 v[38:41], v151 offset:1056
	s_waitcnt lgkmcnt(1)
	v_mfma_f32_16x16x32_f16 v[128:131], v[22:25], v[30:33], v[128:131]
	v_mfma_f32_16x16x32_f16 v[178:181], v[18:21], v[30:33], v[202:205]
	s_waitcnt lgkmcnt(0)
	v_mfma_f32_16x16x32_f16 v[140:143], v[22:25], v[38:41], v[140:143]
	v_mfma_f32_16x16x32_f16 v[158:161], v[18:21], v[38:41], v[158:161]
	v_add_u32_e32 v30, 0xe1680, v150
	v_min_u32_e32 v30, v30, v114
	global_load_dwordx4 v[30:33], v30, s[8:9] nt
	s_waitcnt vmcnt(21)
	v_cvt_pk_f16_f32 v39, v100, v101
	v_cvt_pk_f16_f32 v38, v98, v99
	ds_write_b16 v234, v38 offset:6080
	ds_write_b16_d16_hi v235, v38 offset:6080
	ds_write_b16 v236, v39 offset:6080
	ds_write_b16_d16_hi v237, v39 offset:6080
	ds_read_b128 v[38:41], v151 offset:1664
	ds_read_b128 v[98:101], v151 offset:2272
	s_waitcnt lgkmcnt(1)
	v_mfma_f32_16x16x32_f16 v[202:205], v[22:25], v[38:41], v[222:225]
	v_mfma_f32_16x16x32_f16 v[214:217], v[18:21], v[38:41], v[110:113]
	ds_read_b128 v[38:41], v151 offset:2880
	s_nop 1
	ds_read_b128 v[110:113], v151 offset:3488
	s_waitcnt lgkmcnt(2)
	v_mfma_f32_16x16x32_f16 v[182:185], v[22:25], v[98:101], v[182:185]
	v_mfma_f32_16x16x32_f16 v[98:101], v[18:21], v[98:101], v[198:201]
	s_waitcnt lgkmcnt(1)
	v_mfma_f32_16x16x32_f16 v[132:135], v[22:25], v[38:41], v[132:135]
	v_mfma_f32_16x16x32_f16 v[144:147], v[18:21], v[38:41], v[144:147]
	s_waitcnt lgkmcnt(0)
	v_mfma_f32_16x16x32_f16 v[198:201], v[22:25], v[110:113], v[206:209]
	v_mfma_f32_16x16x32_f16 v[120:123], v[18:21], v[110:113], v[120:123]
	v_add_u32_e32 v38, 0xf7cc0, v244
	v_min_u32_e32 v38, v38, v114
	global_load_dwordx4 v[38:41], v38, s[8:9] nt
	s_waitcnt vmcnt(21)
	v_cvt_pk_f16_f32 v65, v64, v65
	v_cvt_pk_f16_f32 v64, v62, v63
	ds_write_b16 v238, v64 offset:6688
	ds_write_b16_d16_hi v239, v64 offset:6688
	ds_write_b16 v240, v65 offset:6688
	ds_write_b16_d16_hi v241, v65 offset:6688
	ds_read_b128 v[62:65], v151 offset:4096
	ds_read_b128 v[110:113], v151 offset:4704
	s_waitcnt lgkmcnt(1)
	v_mfma_f32_16x16x32_f16 v[206:209], v[22:25], v[62:65], v[210:213]
	v_mfma_f32_16x16x32_f16 v[62:65], v[18:21], v[62:65], v[190:193]
	s_waitcnt lgkmcnt(0)
	v_mfma_f32_16x16x32_f16 v[166:169], v[22:25], v[110:113], v[166:169]
	v_mfma_f32_16x16x32_f16 v[162:165], v[18:21], v[110:113], v[162:165]
	ds_read_b128 v[110:113], v151 offset:5312
	ds_read_b128 v[190:193], v151 offset:5920
	s_waitcnt lgkmcnt(1)
	v_mfma_f32_16x16x32_f16 v[210:213], v[22:25], v[110:113], v[218:221]
	v_mfma_f32_16x16x32_f16 v[136:139], v[18:21], v[110:113], v[136:139]
	s_waitcnt lgkmcnt(0)
	v_mfma_f32_16x16x32_f16 v[170:173], v[22:25], v[190:193], v[170:173]
	v_mfma_f32_16x16x32_f16 v[124:127], v[18:21], v[190:193], v[124:127]
	v_add_u32_e32 v110, 0x10e300, v150
	v_min_u32_e32 v110, v110, v114
	v_cndmask_b32_e64 v110, 0, v110, s[0:1]
	global_load_dwordx4 v[110:113], v110, s[8:9] nt
	s_waitcnt vmcnt(21)
	v_cvt_pk_f16_f32 v69, v68, v69
	v_cvt_pk_f16_f32 v68, v66, v67
	ds_write_b16 v234, v68 offset:7296
	ds_write_b16_d16_hi v235, v68 offset:7296
	ds_write_b16 v236, v69 offset:7296
	ds_write_b16_d16_hi v237, v69 offset:7296
	ds_read_b128 v[66:69], v151 offset:6528
	ds_read_b128 v[152:155], v151 offset:7136
	s_waitcnt lgkmcnt(1)
	v_mfma_f32_16x16x32_f16 v[116:119], v[22:25], v[66:69], v[116:119]
	v_mfma_f32_16x16x32_f16 v[66:69], v[18:21], v[66:69], v[90:93]
	s_waitcnt lgkmcnt(0)
	v_mfma_f32_16x16x32_f16 v[90:93], v[22:25], v[152:155], v[186:189]
	v_mfma_f32_16x16x32_f16 v[94:97], v[18:21], v[152:155], v[94:97]
	ds_read_b128 v[152:155], v151 offset:7744
	s_waitcnt lgkmcnt(0)
	s_barrier
	v_sub_u32_e32 v245, v234, v243
	v_add_u32_e32 v246, 0xfffffdc0, v245
	v_min_u32_e32 v245, v245, v246
	v_add_u32_e32 v234, v242, v245
	v_sub_u32_e32 v245, v235, v243
	v_add_u32_e32 v246, 0xfffffdc0, v245
	v_min_u32_e32 v245, v245, v246
	v_add_u32_e32 v235, v242, v245
	v_sub_u32_e32 v245, v236, v243
	v_add_u32_e32 v246, 0xfffffdc0, v245
	v_min_u32_e32 v245, v245, v246
	v_add_u32_e32 v236, v242, v245
	v_sub_u32_e32 v245, v237, v243
	v_add_u32_e32 v246, 0xfffffdc0, v245
	v_min_u32_e32 v245, v245, v246
	v_add_u32_e32 v237, v242, v245
	v_sub_u32_e32 v245, v238, v243
	v_add_u32_e32 v246, 0xfffffdc0, v245
	v_min_u32_e32 v245, v245, v246
	v_add_u32_e32 v238, v242, v245
	v_sub_u32_e32 v245, v239, v243
	v_add_u32_e32 v246, 0xfffffdc0, v245
	v_min_u32_e32 v245, v245, v246
	v_add_u32_e32 v239, v242, v245
	v_sub_u32_e32 v245, v240, v243
	v_add_u32_e32 v246, 0xfffffdc0, v245
	v_min_u32_e32 v245, v245, v246
	v_add_u32_e32 v240, v242, v245
	v_sub_u32_e32 v245, v241, v243
	v_add_u32_e32 v246, 0xfffffdc0, v245
	v_min_u32_e32 v245, v245, v246
	v_add_u32_e32 v241, v242, v245
	v_mfma_f32_16x16x32_f16 v[22:25], v[22:25], v[152:155], v[194:197]
	v_mfma_f32_16x16x32_f16 v[18:21], v[18:21], v[152:155], v[174:177]
	v_mov_b32_e32 v114, 0
	ds_read_b128 v[152:155], v151 offset:512
	s_waitcnt vmcnt(20) lgkmcnt(0)
	v_mfma_f32_16x16x32_f16 v[128:131], v[50:53], v[152:155], v[128:131]
	s_waitcnt vmcnt(19)
	v_mfma_f32_16x16x32_f16 v[152:155], v[54:57], v[152:155], v[178:181]
	s_waitcnt vmcnt(16)
	ds_read_b128 v[102:105], v151 offset:1120
	ds_read_b128 v[174:177], v151 offset:1728
	ds_read_b128 v[178:181], v151 offset:2336
	ds_read_b128 v[186:189], v151 offset:2944
	s_waitcnt lgkmcnt(3)
	v_mfma_f32_16x16x32_f16 v[140:143], v[50:53], v[102:105], v[140:143]
	v_mfma_f32_16x16x32_f16 v[102:105], v[54:57], v[102:105], v[158:161]
	s_waitcnt lgkmcnt(2)
	v_mfma_f32_16x16x32_f16 v[158:161], v[50:53], v[174:177], v[202:205]
	v_mfma_f32_16x16x32_f16 v[174:177], v[54:57], v[174:177], v[214:217]
	s_waitcnt lgkmcnt(1)
	v_mfma_f32_16x16x32_f16 v[182:185], v[50:53], v[178:181], v[182:185]
	v_mfma_f32_16x16x32_f16 v[98:101], v[54:57], v[178:181], v[98:101]
	s_waitcnt lgkmcnt(0)
	v_mfma_f32_16x16x32_f16 v[132:135], v[50:53], v[186:189], v[132:135]
	v_mfma_f32_16x16x32_f16 v[144:147], v[54:57], v[186:189], v[144:147]
	s_waitcnt vmcnt(15)
	ds_read_b128 v[106:109], v151 offset:3552
	ds_read_b128 v[178:181], v151 offset:5376
	s_waitcnt lgkmcnt(1)
	v_mfma_f32_16x16x32_f16 v[186:189], v[50:53], v[106:109], v[198:201]
	v_mfma_f32_16x16x32_f16 v[106:109], v[54:57], v[106:109], v[120:123]
	s_nop 2
	ds_read_b128 v[120:123], v151 offset:4160
	ds_read_b128 v[190:193], v151 offset:4768
	s_waitcnt lgkmcnt(1)
	v_mfma_f32_16x16x32_f16 v[194:197], v[50:53], v[120:123], v[206:209]
	v_mfma_f32_16x16x32_f16 v[62:65], v[54:57], v[120:123], v[62:65]
	s_waitcnt lgkmcnt(0)
	v_mfma_f32_16x16x32_f16 v[120:123], v[50:53], v[190:193], v[166:169]
	v_mfma_f32_16x16x32_f16 v[162:165], v[54:57], v[190:193], v[162:165]
	v_mfma_f32_16x16x32_f16 v[166:169], v[50:53], v[178:181], v[210:213]
	v_mfma_f32_16x16x32_f16 v[136:139], v[54:57], v[178:181], v[136:139]
	s_waitcnt vmcnt(14)
	ds_read_b128 v[58:61], v151 offset:5984
	ds_read_b128 v[178:181], v151 offset:6592
	s_waitcnt lgkmcnt(1)
	v_mfma_f32_16x16x32_f16 v[170:173], v[50:53], v[58:61], v[170:173]
	v_mfma_f32_16x16x32_f16 v[58:61], v[54:57], v[58:61], v[124:127]
	s_waitcnt lgkmcnt(0)
	v_mfma_f32_16x16x32_f16 v[116:119], v[50:53], v[178:181], v[116:119]
	v_mfma_f32_16x16x32_f16 v[66:69], v[54:57], v[178:181], v[66:69]
	ds_read_b128 v[124:127], v151 offset:7200
	ds_read_b128 v[178:181], v151 offset:7808
	s_waitcnt lgkmcnt(1)
	v_mfma_f32_16x16x32_f16 v[90:93], v[50:53], v[124:127], v[90:93]
	v_mfma_f32_16x16x32_f16 v[94:97], v[54:57], v[124:127], v[94:97]
	s_waitcnt lgkmcnt(0)
	v_mfma_f32_16x16x32_f16 v[22:25], v[50:53], v[178:181], v[22:25]
	v_mfma_f32_16x16x32_f16 v[18:21], v[54:57], v[178:181], v[18:21]
	s_waitcnt vmcnt(13)
	ds_read_b128 v[34:37], v151 offset:0
	ds_read_b128 v[50:53], v151 offset:608
	s_waitcnt lgkmcnt(1)
	v_mfma_f32_16x16x32_f16 v[54:57], v[2:5], v[34:37], v[128:131]
	s_waitcnt lgkmcnt(0)
	v_mfma_f32_16x16x32_f16 v[124:127], v[2:5], v[50:53], v[140:143]
	v_mfma_f32_16x16x32_f16 v[50:53], v[26:29], v[50:53], v[102:105]
	s_nop 2
	ds_read_b128 v[102:105], v151 offset:1216
	ds_read_b128 v[128:131], v151 offset:1824
	v_mfma_f32_16x16x32_f16 v[34:37], v[26:29], v[34:37], v[152:155]
	s_waitcnt lgkmcnt(1)
	v_mfma_f32_16x16x32_f16 v[140:143], v[2:5], v[102:105], v[158:161]
	v_mfma_f32_16x16x32_f16 v[102:105], v[26:29], v[102:105], v[174:177]
	s_waitcnt lgkmcnt(0)
	v_mfma_f32_16x16x32_f16 v[152:155], v[2:5], v[128:131], v[182:185]
	v_mfma_f32_16x16x32_f16 v[98:101], v[26:29], v[128:131], v[98:101]
	s_waitcnt vmcnt(12)
	ds_read_b128 v[70:73], v151 offset:2432
	ds_read_b128 v[128:131], v151 offset:3040
	s_waitcnt lgkmcnt(1)
	v_mfma_f32_16x16x32_f16 v[132:135], v[2:5], v[70:73], v[132:135]
	v_mfma_f32_16x16x32_f16 v[70:73], v[26:29], v[70:73], v[144:147]
	s_waitcnt lgkmcnt(0)
	v_mfma_f32_16x16x32_f16 v[144:147], v[2:5], v[128:131], v[186:189]
	v_mfma_f32_16x16x32_f16 v[106:109], v[26:29], v[128:131], v[106:109]
	ds_read_b128 v[128:131], v151 offset:3648
	ds_read_b128 v[158:161], v151 offset:4256
	s_waitcnt lgkmcnt(1)
	v_mfma_f32_16x16x32_f16 v[174:177], v[2:5], v[128:131], v[194:197]
	v_mfma_f32_16x16x32_f16 v[62:65], v[26:29], v[128:131], v[62:65]
	s_waitcnt lgkmcnt(0)
	v_mfma_f32_16x16x32_f16 v[120:123], v[2:5], v[158:161], v[120:123]
	v_mfma_f32_16x16x32_f16 v[128:131], v[26:29], v[158:161], v[162:165]
	s_waitcnt vmcnt(11)
	ds_read_b128 v[74:77], v151 offset:4864
	ds_read_b128 v[158:161], v151 offset:5472
	s_waitcnt lgkmcnt(1)
	v_mfma_f32_16x16x32_f16 v[162:165], v[2:5], v[74:77], v[166:169]
	v_mfma_f32_16x16x32_f16 v[74:77], v[26:29], v[74:77], v[136:139]
	s_waitcnt lgkmcnt(0)
	v_mfma_f32_16x16x32_f16 v[136:139], v[2:5], v[158:161], v[170:173]
	v_mfma_f32_16x16x32_f16 v[58:61], v[26:29], v[158:161], v[58:61]
	ds_read_b128 v[158:161], v151 offset:6080
	ds_read_b128 v[166:169], v151 offset:6688
	s_waitcnt lgkmcnt(1)
	v_mfma_f32_16x16x32_f16 v[116:119], v[2:5], v[158:161], v[116:119]
	v_mfma_f32_16x16x32_f16 v[66:69], v[26:29], v[158:161], v[66:69]
	s_waitcnt lgkmcnt(0)
	v_mfma_f32_16x16x32_f16 v[90:93], v[2:5], v[166:169], v[90:93]
	v_mfma_f32_16x16x32_f16 v[94:97], v[26:29], v[166:169], v[94:97]
	s_waitcnt vmcnt(10)
	ds_read_b128 v[78:81], v151 offset:7296
	s_waitcnt lgkmcnt(0)
	v_mfma_f32_16x16x32_f16 v[2:5], v[2:5], v[78:81], v[22:25]
	v_mfma_f32_16x16x32_f16 v[18:21], v[26:29], v[78:81], v[18:21]
	s_nop 1
	ds_read_b128 v[22:25], v151 offset:64
	ds_read_b128 v[26:29], v151 offset:672
	s_waitcnt vmcnt(9) lgkmcnt(1)
	v_mfma_f32_16x16x32_f16 v[54:57], v[10:13], v[22:25], v[54:57]
	s_waitcnt vmcnt(8)
	v_mfma_f32_16x16x32_f16 v[22:25], v[14:17], v[22:25], v[34:37]
	s_waitcnt lgkmcnt(0)
	v_mfma_f32_16x16x32_f16 v[34:37], v[10:13], v[26:29], v[124:127]
	v_mfma_f32_16x16x32_f16 v[26:29], v[14:17], v[26:29], v[50:53]
	s_nop 2
	ds_read_b128 v[50:53], v151 offset:1280
	s_waitcnt lgkmcnt(0)
	v_mfma_f32_16x16x32_f16 v[78:81], v[10:13], v[50:53], v[140:143]
	v_mfma_f32_16x16x32_f16 v[50:53], v[14:17], v[50:53], v[102:105]
	s_waitcnt vmcnt(5)
	ds_read_b128 v[6:9], v151 offset:1888
	ds_read_b128 v[102:105], v151 offset:2496
	s_waitcnt lgkmcnt(1)
	v_mfma_f32_16x16x32_f16 v[124:127], v[10:13], v[6:9], v[152:155]
	v_mfma_f32_16x16x32_f16 v[6:9], v[14:17], v[6:9], v[98:101]
	s_waitcnt lgkmcnt(0)
	v_mfma_f32_16x16x32_f16 v[132:135], v[10:13], v[102:105], v[132:135]
	v_mfma_f32_16x16x32_f16 v[70:73], v[14:17], v[102:105], v[70:73]
	ds_read_b128 v[98:101], v151 offset:3104
	ds_read_b128 v[102:105], v151 offset:3712
	s_waitcnt lgkmcnt(1)
	v_mfma_f32_16x16x32_f16 v[140:143], v[10:13], v[98:101], v[144:147]
	v_mfma_f32_16x16x32_f16 v[144:147], v[14:17], v[98:101], v[106:109]
	s_waitcnt lgkmcnt(0)
	v_mfma_f32_16x16x32_f16 v[152:155], v[10:13], v[102:105], v[174:177]
	v_mfma_f32_16x16x32_f16 v[158:161], v[14:17], v[102:105], v[62:65]
	s_waitcnt vmcnt(4)
	s_nop 1
	ds_read_b128 v[62:65], v151 offset:4320
	ds_read_b128 v[82:85], v151 offset:6144
	s_waitcnt lgkmcnt(1)
	v_mfma_f32_16x16x32_f16 v[120:123], v[10:13], v[62:65], v[120:123]
	v_mfma_f32_16x16x32_f16 v[128:131], v[14:17], v[62:65], v[128:131]
	ds_read_b128 v[62:65], v151 offset:4928
	ds_read_b128 v[98:101], v151 offset:5536
	s_waitcnt lgkmcnt(1)
	v_mfma_f32_16x16x32_f16 v[162:165], v[10:13], v[62:65], v[162:165]
	v_mfma_f32_16x16x32_f16 v[166:169], v[14:17], v[62:65], v[74:77]
	s_waitcnt lgkmcnt(0)
	v_mfma_f32_16x16x32_f16 v[136:139], v[10:13], v[98:101], v[136:139]
	v_mfma_f32_16x16x32_f16 v[170:173], v[14:17], v[98:101], v[58:61]
	v_mfma_f32_16x16x32_f16 v[116:119], v[10:13], v[82:85], v[116:119]
	v_mfma_f32_16x16x32_f16 v[174:177], v[14:17], v[82:85], v[66:69]
	s_waitcnt vmcnt(3)
	ds_read_b128 v[58:61], v151 offset:6752
	ds_read_b128 v[62:65], v151 offset:7360
	s_waitcnt lgkmcnt(1)
	v_mfma_f32_16x16x32_f16 v[178:181], v[10:13], v[58:61], v[90:93]
	v_mfma_f32_16x16x32_f16 v[182:185], v[14:17], v[58:61], v[94:97]
	s_waitcnt lgkmcnt(0)
	v_mfma_f32_16x16x32_f16 v[2:5], v[10:13], v[62:65], v[2:5]
	v_mfma_f32_16x16x32_f16 v[186:189], v[14:17], v[62:65], v[18:21]
	ds_read_b128 v[10:13], v151 offset:128
	ds_read_b128 v[14:17], v151 offset:736
	s_waitcnt lgkmcnt(1)
	v_mfma_f32_16x16x32_f16 v[148:151], v[46:49], v[10:13], v[54:57]
	v_mfma_f32_16x16x32_f16 v[106:109], v[42:45], v[10:13], v[22:25]
	s_waitcnt lgkmcnt(0)
	v_mfma_f32_16x16x32_f16 v[102:105], v[46:49], v[14:17], v[34:37]
	v_mfma_f32_16x16x32_f16 v[94:97], v[42:45], v[14:17], v[26:29]
	s_waitcnt vmcnt(2)
	ds_read_b128 v[10:13], v151 offset:1344
	ds_read_b128 v[14:17], v151 offset:1952
	s_waitcnt lgkmcnt(1)
	v_mfma_f32_16x16x32_f16 v[98:101], v[46:49], v[10:13], v[78:81]
	v_mfma_f32_16x16x32_f16 v[90:93], v[42:45], v[10:13], v[50:53]
	s_waitcnt lgkmcnt(0)
	v_mfma_f32_16x16x32_f16 v[82:85], v[42:45], v[14:17], v[6:9]
	s_nop 2
	ds_read_b128 v[6:9], v151 offset:2560
	ds_read_b128 v[10:13], v151 offset:3168
	v_mfma_f32_16x16x32_f16 v[86:89], v[46:49], v[14:17], v[124:127]
	s_waitcnt lgkmcnt(1)
	v_mfma_f32_16x16x32_f16 v[78:81], v[46:49], v[6:9], v[132:135]
	v_mfma_f32_16x16x32_f16 v[74:77], v[42:45], v[6:9], v[70:73]
	s_waitcnt lgkmcnt(0)
	v_mfma_f32_16x16x32_f16 v[70:73], v[46:49], v[10:13], v[140:143]
	v_mfma_f32_16x16x32_f16 v[62:65], v[42:45], v[10:13], v[144:147]
	s_waitcnt vmcnt(1)
	ds_read_b128 v[6:9], v151 offset:3776
	ds_read_b128 v[10:13], v151 offset:4384
	s_waitcnt lgkmcnt(1)
	v_mfma_f32_16x16x32_f16 v[66:69], v[46:49], v[6:9], v[152:155]
	v_mfma_f32_16x16x32_f16 v[58:61], v[42:45], v[6:9], v[158:161]
	s_waitcnt lgkmcnt(0)
	v_mfma_f32_16x16x32_f16 v[54:57], v[46:49], v[10:13], v[120:123]
	v_mfma_f32_16x16x32_f16 v[50:53], v[42:45], v[10:13], v[128:131]
	ds_read_b128 v[6:9], v151 offset:4992
	ds_read_b128 v[10:13], v151 offset:5600
	s_waitcnt lgkmcnt(1)
	v_mfma_f32_16x16x32_f16 v[38:41], v[46:49], v[6:9], v[162:165]
	v_mfma_f32_16x16x32_f16 v[34:37], v[42:45], v[6:9], v[166:169]
	s_waitcnt lgkmcnt(0)
	v_mfma_f32_16x16x32_f16 v[30:33], v[46:49], v[10:13], v[136:139]
	v_mfma_f32_16x16x32_f16 v[18:21], v[42:45], v[10:13], v[170:173]
	s_waitcnt vmcnt(0)
	ds_read_b128 v[6:9], v151 offset:6208
	ds_read_b128 v[10:13], v151 offset:6816
	ds_read_b128 v[110:113], v151 offset:7424
	s_waitcnt lgkmcnt(0)
	s_barrier
	v_mfma_f32_16x16x32_f16 v[22:25], v[46:49], v[6:9], v[116:119]
	s_barrier
	v_mfma_f32_16x16x32_f16 v[26:29], v[42:45], v[6:9], v[174:177]
	s_movk_i32 s0, 0xffe0
	v_lshrrev_b32_e32 v6, 2, v0
	v_and_b32_e32 v1, 15, v0
	v_ashrrev_i32_e32 v114, 1, v0
	v_and_b32_e32 v116, 12, v6
	v_mfma_f32_16x16x32_f16 v[14:17], v[46:49], v[10:13], v[178:181]
	v_and_or_b32 v120, v114, s0, v116
	v_lshlrev_b32_e32 v114, 3, v1
	v_lshlrev_b32_e32 v129, 1, v120
	v_mfma_f32_16x16x32_f16 v[6:9], v[46:49], v[110:113], v[2:5]
	v_mov_b32_e32 v46, 0x1f480
	v_lshl_add_u32 v128, v120, 2, v46
	v_or_b32_e32 v46, 0x1ee00, v114
	v_or_b32_e32 v47, 0x1ee80, v114
	v_or_b32_e32 v48, 0x1ef00, v114
	v_or_b32_e32 v49, 0x1ef80, v114
	v_mfma_f32_16x16x32_f16 v[10:13], v[42:45], v[10:13], v[182:185]
	s_movk_i32 s4, 0x210
	s_movk_i32 s0, 0x1880
	v_cmp_gt_i32_e32 vcc, s0, v0
	v_mfma_f32_16x16x32_f16 v[2:5], v[42:45], v[110:113], v[186:189]
	ds_read_b128 v[42:45], v128
	ds_read_b64 v[124:125], v46
	ds_read_b64 v[126:127], v47
	ds_read_b64 v[118:119], v48
	ds_read_b64 v[116:117], v49
	ds_read_b128 v[46:49], v128
	ds_read_b128 v[120:123], v128 offset:64
	s_waitcnt lgkmcnt(4)
	v_pk_fma_f32 v[104:105], v[126:127], v[44:45], v[104:105] op_sel_hi:[0,1,1]
	v_pk_fma_f32 v[102:103], v[126:127], v[42:43], v[102:103] op_sel_hi:[0,1,1]
	s_waitcnt lgkmcnt(0)
	v_pk_fma_f32 v[108:109], v[124:125], v[122:123], v[108:109] op_sel_hi:[0,1,1]
	v_pk_fma_f32 v[106:107], v[124:125], v[120:121], v[106:107] op_sel_hi:[0,1,1]
	v_pk_mul_f32 v[108:109], v[124:125], v[108:109] op_sel:[1,0]
	v_pk_mul_f32 v[106:107], v[124:125], v[106:107] op_sel:[1,0]
	v_cvt_pk_f16_f32 v109, v108, v109
	v_cvt_pk_f16_f32 v108, v106, v107
	v_or_b32_e32 v106, 32, v129
	v_mad_u32_u24 v107, v1, s4, v106
	ds_write_b64 v107, v[108:109]
	v_mov_b32_e32 v107, 0x2100
	v_pk_fma_f32 v[96:97], v[126:127], v[122:123], v[96:97] op_sel_hi:[0,1,1]
	v_pk_fma_f32 v[94:95], v[126:127], v[120:121], v[94:95] op_sel_hi:[0,1,1]
	v_mad_u32_u24 v107, v1, s4, v107
	v_pk_mul_f32 v[96:97], v[126:127], v[96:97] op_sel:[1,0]
	v_pk_mul_f32 v[94:95], v[126:127], v[94:95] op_sel:[1,0]
	v_pk_mul_f32 v[104:105], v[126:127], v[104:105] op_sel:[1,0]
	v_pk_mul_f32 v[102:103], v[126:127], v[102:103] op_sel:[1,0]
	v_cvt_pk_f16_f32 v97, v96, v97
	v_cvt_pk_f16_f32 v96, v94, v95
	v_add_u32_e32 v94, v107, v106
	v_cvt_pk_f16_f32 v105, v104, v105
	v_cvt_pk_f16_f32 v104, v102, v103
	v_add_u32_e32 v102, v107, v129
	ds_write_b64 v94, v[96:97]
	v_mov_b32_e32 v94, 0x4200
	v_pk_fma_f32 v[92:93], v[118:119], v[122:123], v[92:93] op_sel_hi:[0,1,1]
	v_pk_fma_f32 v[90:91], v[118:119], v[120:121], v[90:91] op_sel_hi:[0,1,1]
	ds_write_b64 v102, v[104:105]
	v_mad_u32_u24 v102, v1, s4, v94
	v_pk_mul_f32 v[92:93], v[118:119], v[92:93] op_sel:[1,0]
	v_pk_mul_f32 v[90:91], v[118:119], v[90:91] op_sel:[1,0]
	v_cvt_pk_f16_f32 v93, v92, v93
	v_cvt_pk_f16_f32 v92, v90, v91
	v_add_u32_e32 v90, v102, v106
	ds_write_b64 v90, v[92:93]
	v_mov_b32_e32 v90, 0x6300
	v_pk_fma_f32 v[84:85], v[116:117], v[122:123], v[84:85] op_sel_hi:[0,1,1]
	v_pk_fma_f32 v[82:83], v[116:117], v[120:121], v[82:83] op_sel_hi:[0,1,1]
	v_pk_fma_f32 v[110:111], v[124:125], v[44:45], v[150:151] op_sel_hi:[0,1,1]
	v_pk_fma_f32 v[112:113], v[124:125], v[42:43], v[148:149] op_sel_hi:[0,1,1]
	v_mad_u32_u24 v90, v1, s4, v90
	v_pk_mul_f32 v[84:85], v[116:117], v[84:85] op_sel:[1,0]
	v_pk_mul_f32 v[82:83], v[116:117], v[82:83] op_sel:[1,0]
	v_pk_mul_f32 v[110:111], v[124:125], v[110:111] op_sel:[1,0]
	v_pk_mul_f32 v[112:113], v[124:125], v[112:113] op_sel:[1,0]
	v_cvt_pk_f16_f32 v85, v84, v85
	v_cvt_pk_f16_f32 v84, v82, v83
	v_add_u32_e32 v82, v90, v106
	v_cvt_pk_f16_f32 v111, v110, v111
	v_cvt_pk_f16_f32 v110, v112, v113
	v_mad_u32_u24 v112, v1, s4, v129
	ds_write_b64 v82, v[84:85]
	v_or_b32_e32 v82, 0x1f000, v114
	ds_write_b64 v112, v[110:111]
	ds_read_b128 v[110:113], v128
	ds_read_b64 v[82:83], v82
	v_pk_fma_f32 v[94:95], v[118:119], v[44:45], v[100:101] op_sel_hi:[0,1,1]
	v_pk_fma_f32 v[96:97], v[118:119], v[42:43], v[98:99] op_sel_hi:[0,1,1]
	v_pk_fma_f32 v[88:89], v[116:117], v[44:45], v[88:89] op_sel_hi:[0,1,1]
	v_pk_fma_f32 v[86:87], v[116:117], v[42:43], v[86:87] op_sel_hi:[0,1,1]
	v_pk_mul_f32 v[94:95], v[118:119], v[94:95] op_sel:[1,0]
	v_pk_mul_f32 v[96:97], v[118:119], v[96:97] op_sel:[1,0]
	v_pk_mul_f32 v[88:89], v[116:117], v[88:89] op_sel:[1,0]
	v_pk_mul_f32 v[86:87], v[116:117], v[86:87] op_sel:[1,0]
	v_mov_b32_e32 v84, 0x8400
	s_waitcnt lgkmcnt(0)
	v_pk_fma_f32 v[44:45], v[82:83], v[44:45], v[80:81] op_sel_hi:[0,1,1]
	v_pk_fma_f32 v[42:43], v[82:83], v[42:43], v[78:79] op_sel_hi:[0,1,1]
	v_cvt_pk_f16_f32 v95, v94, v95
	v_cvt_pk_f16_f32 v94, v96, v97
	v_add_u32_e32 v96, v102, v129
	v_cvt_pk_f16_f32 v89, v88, v89
	v_cvt_pk_f16_f32 v88, v86, v87
	v_add_u32_e32 v86, v90, v129
	v_mad_u32_u24 v90, v1, s4, v84
	v_pk_mul_f32 v[44:45], v[82:83], v[44:45] op_sel:[1,0]
	v_pk_mul_f32 v[42:43], v[82:83], v[42:43] op_sel:[1,0]
	ds_write_b64 v96, v[94:95]
	ds_write_b64 v86, v[88:89]
	v_or_b32_e32 v84, 0x1f080, v114
	v_or_b32_e32 v86, 0x1f100, v114
	v_or_b32_e32 v88, 0x1f180, v114
	v_cvt_pk_f16_f32 v45, v44, v45
	v_cvt_pk_f16_f32 v44, v42, v43
	v_add_u32_e32 v42, v90, v129
	ds_read_b64 v[84:85], v84
	ds_read_b64 v[86:87], v86
	ds_read_b64 v[88:89], v88
	ds_write_b64 v42, v[44:45]
	v_pk_fma_f32 v[42:43], v[82:83], v[122:123], v[76:77] op_sel_hi:[0,1,1]
	v_pk_fma_f32 v[44:45], v[82:83], v[120:121], v[74:75] op_sel_hi:[0,1,1]
	v_pk_mul_f32 v[42:43], v[82:83], v[42:43] op_sel:[1,0]
	v_pk_mul_f32 v[44:45], v[82:83], v[44:45] op_sel:[1,0]
	v_cvt_pk_f16_f32 v43, v42, v43
	v_cvt_pk_f16_f32 v42, v44, v45
	v_add_u32_e32 v44, v90, v106
	ds_write_b64 v44, v[42:43]
	v_mov_b32_e32 v42, 0xa500
	v_mad_u32_u24 v74, v1, s4, v42
	s_waitcnt lgkmcnt(4)
	v_pk_fma_f32 v[42:43], v[84:85], v[48:49], v[72:73] op_sel_hi:[0,1,1]
	v_pk_fma_f32 v[44:45], v[84:85], v[46:47], v[70:71] op_sel_hi:[0,1,1]
	v_pk_mul_f32 v[42:43], v[84:85], v[42:43] op_sel:[1,0]
	v_pk_mul_f32 v[70:71], v[84:85], v[44:45] op_sel:[1,0]
	v_cvt_pk_f16_f32 v73, v42, v43
	ds_read_b128 v[42:45], v128 offset:64
	v_cvt_pk_f16_f32 v72, v70, v71
	v_add_u32_e32 v70, v74, v129
	ds_write_b64 v70, v[72:73]
	ds_read_b128 v[70:73], v128 offset:64
	s_waitcnt lgkmcnt(2)
	v_pk_fma_f32 v[64:65], v[84:85], v[44:45], v[64:65] op_sel_hi:[0,1,1]
	v_pk_fma_f32 v[62:63], v[84:85], v[42:43], v[62:63] op_sel_hi:[0,1,1]
	v_pk_mul_f32 v[64:65], v[84:85], v[64:65] op_sel:[1,0]
	v_pk_mul_f32 v[62:63], v[84:85], v[62:63] op_sel:[1,0]
	v_cvt_pk_f16_f32 v65, v64, v65
	v_cvt_pk_f16_f32 v64, v62, v63
	v_add_u32_e32 v62, v74, v106
	ds_write_b64 v62, v[64:65]
	v_mov_b32_e32 v62, 0xc600
	v_pk_fma_f32 v[60:61], v[86:87], v[44:45], v[60:61] op_sel_hi:[0,1,1]
	v_pk_fma_f32 v[58:59], v[86:87], v[42:43], v[58:59] op_sel_hi:[0,1,1]
	v_mad_u32_u24 v74, v1, s4, v62
	v_pk_mul_f32 v[60:61], v[86:87], v[60:61] op_sel:[1,0]
	v_pk_mul_f32 v[58:59], v[86:87], v[58:59] op_sel:[1,0]
	v_cvt_pk_f16_f32 v61, v60, v61
	v_cvt_pk_f16_f32 v60, v58, v59
	v_add_u32_e32 v58, v74, v106
	ds_write_b64 v58, v[60:61]
	v_mov_b32_e32 v58, 0xe700
	v_pk_fma_f32 v[52:53], v[88:89], v[44:45], v[52:53] op_sel_hi:[0,1,1]
	v_pk_fma_f32 v[50:51], v[88:89], v[42:43], v[50:51] op_sel_hi:[0,1,1]
	v_mad_u32_u24 v58, v1, s4, v58
	v_pk_mul_f32 v[52:53], v[88:89], v[52:53] op_sel:[1,0]
	v_pk_mul_f32 v[50:51], v[88:89], v[50:51] op_sel:[1,0]
	v_cvt_pk_f16_f32 v53, v52, v53
	v_cvt_pk_f16_f32 v52, v50, v51
	v_add_u32_e32 v50, v58, v106
	ds_write_b64 v50, v[52:53]
	v_or_b32_e32 v50, 0x1f200, v114
	ds_read_b64 v[50:51], v50
	v_pk_fma_f32 v[62:63], v[86:87], v[48:49], v[68:69] op_sel_hi:[0,1,1]
	v_pk_fma_f32 v[64:65], v[86:87], v[46:47], v[66:67] op_sel_hi:[0,1,1]
	v_pk_fma_f32 v[56:57], v[88:89], v[48:49], v[56:57] op_sel_hi:[0,1,1]
	v_pk_fma_f32 v[54:55], v[88:89], v[46:47], v[54:55] op_sel_hi:[0,1,1]
	v_pk_mul_f32 v[62:63], v[86:87], v[62:63] op_sel:[1,0]
	v_pk_mul_f32 v[64:65], v[86:87], v[64:65] op_sel:[1,0]
	v_pk_mul_f32 v[56:57], v[88:89], v[56:57] op_sel:[1,0]
	v_pk_mul_f32 v[54:55], v[88:89], v[54:55] op_sel:[1,0]
	v_cvt_pk_f16_f32 v63, v62, v63
	v_cvt_pk_f16_f32 v62, v64, v65
	v_add_u32_e32 v64, v74, v129
	v_cvt_pk_f16_f32 v57, v56, v57
	v_cvt_pk_f16_f32 v56, v54, v55
	v_add_u32_e32 v54, v58, v129
	v_mov_b32_e32 v52, 0x10800
	ds_write_b64 v64, v[62:63]
	ds_write_b64 v54, v[56:57]
	v_mad_u32_u24 v58, v1, s4, v52
	v_or_b32_e32 v52, 0x1f280, v114
	v_or_b32_e32 v54, 0x1f300, v114
	v_or_b32_e32 v56, 0x1f380, v114
	ds_read_b64 v[52:53], v52
	ds_read_b64 v[54:55], v54
	ds_read_b64 v[56:57], v56
	s_waitcnt lgkmcnt(5)
	v_pk_fma_f32 v[36:37], v[50:51], v[44:45], v[36:37] op_sel_hi:[0,1,1]
	v_pk_fma_f32 v[34:35], v[50:51], v[42:43], v[34:35] op_sel_hi:[0,1,1]
	v_pk_mul_f32 v[36:37], v[50:51], v[36:37] op_sel:[1,0]
	v_pk_mul_f32 v[34:35], v[50:51], v[34:35] op_sel:[1,0]
	v_cvt_pk_f16_f32 v37, v36, v37
	v_cvt_pk_f16_f32 v36, v34, v35
	v_add_u32_e32 v34, v58, v106
	v_pk_fma_f32 v[40:41], v[50:51], v[48:49], v[40:41] op_sel_hi:[0,1,1]
	v_pk_fma_f32 v[38:39], v[50:51], v[46:47], v[38:39] op_sel_hi:[0,1,1]
	ds_write_b64 v34, v[36:37]
	v_mov_b32_e32 v34, 0x12900
	s_waitcnt lgkmcnt(3)
	v_pk_fma_f32 v[20:21], v[52:53], v[44:45], v[20:21] op_sel_hi:[0,1,1]
	v_pk_fma_f32 v[18:19], v[52:53], v[42:43], v[18:19] op_sel_hi:[0,1,1]
	v_pk_mul_f32 v[40:41], v[50:51], v[40:41] op_sel:[1,0]
	v_pk_mul_f32 v[38:39], v[50:51], v[38:39] op_sel:[1,0]
	v_mad_u32_u24 v34, v1, s4, v34
	v_pk_fma_f32 v[32:33], v[52:53], v[48:49], v[32:33] op_sel_hi:[0,1,1]
	v_pk_fma_f32 v[30:31], v[52:53], v[46:47], v[30:31] op_sel_hi:[0,1,1]
	v_pk_mul_f32 v[20:21], v[52:53], v[20:21] op_sel:[1,0]
	v_pk_mul_f32 v[18:19], v[52:53], v[18:19] op_sel:[1,0]
	v_cvt_pk_f16_f32 v41, v40, v41
	v_cvt_pk_f16_f32 v40, v38, v39
	v_add_u32_e32 v38, v58, v129
	v_pk_mul_f32 v[32:33], v[52:53], v[32:33] op_sel:[1,0]
	v_pk_mul_f32 v[30:31], v[52:53], v[30:31] op_sel:[1,0]
	v_cvt_pk_f16_f32 v21, v20, v21
	v_cvt_pk_f16_f32 v20, v18, v19
	v_add_u32_e32 v18, v34, v106
	ds_write_b64 v38, v[40:41]
	v_cvt_pk_f16_f32 v33, v32, v33
	v_cvt_pk_f16_f32 v32, v30, v31
	v_add_u32_e32 v30, v34, v129
	ds_write_b64 v18, v[20:21]
	v_mov_b32_e32 v18, 0x14a00
	ds_write_b64 v30, v[32:33]
	v_mad_u32_u24 v30, v1, s4, v18
	s_waitcnt lgkmcnt(5)
	v_pk_fma_f32 v[18:19], v[54:55], v[112:113], v[24:25] op_sel_hi:[0,1,1]
	v_pk_fma_f32 v[20:21], v[54:55], v[110:111], v[22:23] op_sel_hi:[0,1,1]
	v_pk_mul_f32 v[18:19], v[54:55], v[18:19] op_sel:[1,0]
	v_pk_mul_f32 v[20:21], v[54:55], v[20:21] op_sel:[1,0]
	v_cvt_pk_f16_f32 v19, v18, v19
	v_cvt_pk_f16_f32 v18, v20, v21
	v_add_u32_e32 v20, v30, v129
	s_waitcnt lgkmcnt(4)
	v_pk_fma_f32 v[12:13], v[56:57], v[72:73], v[12:13] op_sel_hi:[0,1,1]
	v_pk_fma_f32 v[10:11], v[56:57], v[70:71], v[10:11] op_sel_hi:[0,1,1]
	ds_write_b64 v20, v[18:19]
	v_pk_fma_f32 v[18:19], v[54:55], v[72:73], v[28:29] op_sel_hi:[0,1,1]
	v_pk_fma_f32 v[20:21], v[54:55], v[70:71], v[26:27] op_sel_hi:[0,1,1]
	v_pk_mul_f32 v[12:13], v[56:57], v[12:13] op_sel:[1,0]
	v_pk_mul_f32 v[10:11], v[56:57], v[10:11] op_sel:[1,0]
	v_pk_mul_f32 v[18:19], v[54:55], v[18:19] op_sel:[1,0]
	v_pk_mul_f32 v[20:21], v[54:55], v[20:21] op_sel:[1,0]
	v_cvt_pk_f16_f32 v13, v12, v13
	v_cvt_pk_f16_f32 v12, v10, v11
	v_or_b32_e32 v10, 0x1f400, v114
	v_cvt_pk_f16_f32 v19, v18, v19
	v_cvt_pk_f16_f32 v18, v20, v21
	v_add_u32_e32 v20, v30, v106
	ds_read_b64 v[10:11], v10
	ds_write_b64 v20, v[18:19]
	v_mov_b32_e32 v18, 0x16b00
	v_pk_fma_f32 v[16:17], v[56:57], v[112:113], v[16:17] op_sel_hi:[0,1,1]
	v_pk_fma_f32 v[14:15], v[56:57], v[110:111], v[14:15] op_sel_hi:[0,1,1]
	v_mad_u32_u24 v18, v1, s4, v18
	v_pk_mul_f32 v[16:17], v[56:57], v[16:17] op_sel:[1,0]
	v_pk_mul_f32 v[14:15], v[56:57], v[14:15] op_sel:[1,0]
	v_cvt_pk_f16_f32 v17, v16, v17
	v_cvt_pk_f16_f32 v16, v14, v15
	v_add_u32_e32 v14, v18, v129
	ds_write_b64 v14, v[16:17]
	v_add_u32_e32 v14, v18, v106
	ds_write_b64 v14, v[12:13]
	v_mov_b32_e32 v12, 0x18c00
	s_waitcnt lgkmcnt(3)
	v_pk_fma_f32 v[8:9], v[10:11], v[112:113], v[8:9] op_sel_hi:[0,1,1]
	v_pk_fma_f32 v[6:7], v[10:11], v[110:111], v[6:7] op_sel_hi:[0,1,1]
	v_pk_fma_f32 v[4:5], v[10:11], v[72:73], v[4:5] op_sel_hi:[0,1,1]
	v_pk_fma_f32 v[2:3], v[10:11], v[70:71], v[2:3] op_sel_hi:[0,1,1]
	v_mad_u32_u24 v1, v1, s4, v12
	v_pk_mul_f32 v[8:9], v[10:11], v[8:9] op_sel:[1,0]
	v_pk_mul_f32 v[6:7], v[10:11], v[6:7] op_sel:[1,0]
	v_pk_mul_f32 v[4:5], v[10:11], v[4:5] op_sel:[1,0]
	v_pk_mul_f32 v[2:3], v[10:11], v[2:3] op_sel:[1,0]
	v_cvt_pk_f16_f32 v9, v8, v9
	v_cvt_pk_f16_f32 v8, v6, v7
	v_add_u32_e32 v6, v1, v129
	v_cvt_pk_f16_f32 v5, v4, v5
	v_cvt_pk_f16_f32 v4, v2, v3
	v_add_u32_e32 v1, v1, v106
	ds_write_b64 v6, v[8:9]
	ds_write_b64 v1, v[4:5]
	s_waitcnt lgkmcnt(0)
	s_barrier
	s_and_saveexec_b64 s[0:1], vcc
	s_cbranch_execz .LBB2_12
	v_lshlrev_b32_e32 v1, 4, v0
	v_and_b32_e32 v114, 0x70, v1
	v_lshl_add_u64 v[2:3], s[6:7], 0, v[114:115]
	s_mov_b64 s[0:1], 0
	s_mov_b32 s5, 0x5397829d
	s_movk_i32 s6, 0xf9e0
	s_mov_b32 s7, 0xc350
	s_movk_i32 s8, 0x167f
	s_branch .LBB2_10
